# RG-LRU phase body rewritten by hand: double-buffered A tile, scan in MFMA accumulator layout via ds_bpermute, 2 barriers per chunk
# speedup vs baseline: 1.0206x; 1.0206x over previous
.LBB0_973:
	s_cmpk_gt_i32 s19, 0x7ff
	s_cbranch_scc1 .LBB0_996
	s_ashr_i32 s6, s19, 31
	s_lshr_b32 s4, s6, 24
	s_add_i32 s11, s19, s4
	s_ashr_i32 s4, s11, 8
	s_lshr_b32 s5, s11, 31
	s_add_i32 s5, s4, s5
	s_and_b32 s5, s5, -2
	s_sub_i32 s4, s4, s5
	s_cmp_eq_u32 s4, 1
	s_movk_i32 s10, 0x108
	s_cselect_b32 s5, s10, 0x118
	s_cmp_lg_u32 s4, 0
	s_cselect_b32 s4, s5, 0xf8
	s_add_u32 s4, s2, s4
	s_addc_u32 s5, s3, 0
	s_load_dwordx2 s[4:5], s[4:5], 0x0
	s_lshr_b32 s6, s6, 23
	s_add_i32 s6, s19, s6
	s_ashr_i32 s6, s6, 9
	s_ashr_i32 s7, s6, 31
	s_lshl_b64 s[6:7], s[6:7], 22
	s_load_dwordx2 s[8:9], s[2:3], 0x130
	s_waitcnt lgkmcnt(0)
	s_add_u32 s4, s4, s6
	s_addc_u32 s5, s5, s7
	s_and_b32 s6, s11, 0xff00
	s_sub_i32 s6, s19, s6
	s_sext_i32_i16 s7, s6
	s_bfe_u32 s7, s7, 0x5001a
	s_add_i32 s7, s6, s7
	s_sext_i32_i16 s11, s7
	s_and_b32 s7, s7, 0xffe0
	s_sub_i32 s6, s6, s7
	s_lshl_b32 s7, s11, 2
	s_and_b32 s7, s7, 0xffffff80
	v_and_b32_e32 v132, -16, v141
	s_waitcnt vmcnt(0)
	v_add_u32_e32 v0, s7, v132
	s_sext_i32_i16 s6, s6
	v_ashrrev_i32_e32 v1, 31, v0
	s_lshl_b32 s6, s6, 5
	v_lshlrev_b64 v[0:1], 12, v[0:1]
	v_lshl_add_u64 v[0:1], s[4:5], 0, v[0:1]
	s_ashr_i32 s7, s6, 31
	v_and_b32_e32 v134, 28, v140
	v_lshl_add_u64 v[0:1], s[6:7], 2, v[0:1]
	v_mov_b32_e32 v137, 0
	v_lshlrev_b32_e32 v136, 2, v134
	v_lshl_add_u64 v[52:53], v[0:1], 0, v[136:137]
	s_mov_b32 s11, 0xc801000
	v_add_co_u32_e32 v8, vcc, s11, v52
	s_mov_b32 s12, 0xc803000
	s_nop 0
	v_addc_co_u32_e32 v9, vcc, 0, v53, vcc
	v_add_co_u32_e32 v16, vcc, s12, v52
	s_mov_b32 s13, 0xc805000
	s_nop 0
	v_addc_co_u32_e32 v17, vcc, 0, v53, vcc
	v_add_co_u32_e32 v24, vcc, s13, v52
	s_mov_b32 s14, 0xc807000
	s_nop 0
	v_addc_co_u32_e32 v25, vcc, 0, v53, vcc
	v_add_co_u32_e32 v32, vcc, s14, v52
	s_mov_b32 s15, 0xc809000
	s_nop 0
	v_addc_co_u32_e32 v33, vcc, 0, v53, vcc
	v_add_co_u32_e32 v40, vcc, s15, v52
	s_mov_b32 s16, 0xc80b000
	s_nop 0
	v_addc_co_u32_e32 v41, vcc, 0, v53, vcc
	v_add_co_u32_e32 v48, vcc, s16, v52
	s_mov_b32 s4, 0xc80d000
	s_nop 0
	v_addc_co_u32_e32 v49, vcc, 0, v53, vcc
	v_add_co_u32_e32 v54, vcc, s4, v52
	s_mov_b32 s4, 0xc80f000
	s_nop 0
	v_addc_co_u32_e32 v55, vcc, 0, v53, vcc
	v_add_co_u32_e32 v52, vcc, s4, v52
	global_load_dwordx4 v[0:3], v[8:9], off offset:-4096 nt
	global_load_dwordx4 v[4:7], v[8:9], off nt
	v_addc_co_u32_e32 v53, vcc, 0, v53, vcc
	global_load_dwordx4 v[8:11], v[16:17], off offset:-4096 nt
	global_load_dwordx4 v[12:15], v[16:17], off nt
	s_nop 0
	global_load_dwordx4 v[16:19], v[24:25], off offset:-4096 nt
	global_load_dwordx4 v[20:23], v[24:25], off nt
	s_nop 0
	global_load_dwordx4 v[24:27], v[32:33], off offset:-4096 nt
	global_load_dwordx4 v[28:31], v[32:33], off nt
	s_nop 0
	global_load_dwordx4 v[32:35], v[40:41], off offset:-4096 nt
	global_load_dwordx4 v[36:39], v[40:41], off nt
	s_nop 0
	global_load_dwordx4 v[40:43], v[48:49], off offset:-4096 nt
	global_load_dwordx4 v[44:47], v[48:49], off nt
	s_nop 0
	global_load_dwordx4 v[48:51], v[54:55], off offset:-4096 nt
	global_load_dwordx4 v[60:63], v[54:55], off nt
	global_load_dwordx4 v[88:91], v[52:53], off offset:-4096 nt
	global_load_dwordx4 v[100:103], v[52:53], off nt
	s_add_u32 s20, s8, 0x2900000
	s_mov_b32 s17, 0xc80c000
	s_addc_u32 s21, s9, 0
	v_ashrrev_i32_e32 v133, 31, v132
	s_mov_b32 s22, 0xc3e00000
	s_mov_b64 s[4:5], 0x200000
	v_mov_b32_e32 v142, 0x43e00000
	v_mov_b32_e32 v143, 0xffffff04
	s_branch .LBB0_977

.LBB0_1234:
	s_load_dwordx4 s[0:3], s[8:9], 0x138
	s_waitcnt lgkmcnt(0)
	s_mov_b64 s[4:5], s[0:1]
	s_cmp_lt_i32 s4, 10
	s_cselect_b64 s[0:1], -1, 0
	s_cmp_gt_i32 s5, 9
	s_cselect_b64 s[2:3], -1, 0
	s_and_b64 s[0:1], s[0:1], s[2:3]
	s_andn2_b64 vcc, exec, s[0:1]
	s_cbranch_vccnz .LBB0_1372
	s_mov_b64 s[0:1], s[8:9]
	v_mbcnt_lo_u32_b32 v146, -1, 0
	v_mbcnt_hi_u32_b32 v146, -1, v146
	s_load_dword s38, s[8:9], 0x148
	s_add_u32 s4, s8, 0x148
	v_readlane_b32 s2, v243, 0
	s_addc_u32 s5, s9, 0
	v_readlane_b32 s3, v243, 1
	s_waitcnt lgkmcnt(0)
	s_sub_i32 s39, s38, 32
	s_cmp_lt_i32 s2, s39
	s_mov_b64 s[2:3], -1
	s_cbranch_scc1 .LBB0_1257
	v_readlane_b32 s2, v243, 0
	s_sub_i32 s2, s2, s39
	s_lshl_b32 s6, s2, 3
	s_add_i32 s6, s6, s94
	s_cmpk_gt_u32 s6, 0x13ff
	v_readlane_b32 s3, v243, 1
	s_cbranch_scc1 .LBB0_1256
	s_bitcmp0_b32 s6, 8
	s_movk_i32 s16, 0xf8
	s_cselect_b32 s17, s16, 0x108
	s_add_u32 s2, s0, s17
	s_addc_u32 s3, s1, 0
	s_load_dwordx2 s[8:9], s[2:3], 0x0
	s_load_dwordx2 s[10:11], s[0:1], 0x130
	s_lshl_b32 s2, s6, 13
	s_and_b32 s2, s2, 0x3c00000
	s_waitcnt vmcnt(0)
	v_lshlrev_b32_e32 v0, 1, v146
	s_waitcnt lgkmcnt(0)
	s_add_u32 s8, s8, s2
	s_addc_u32 s9, s9, 0
	s_lshl_b32 s18, s6, 2
	s_and_b32 s2, s18, 0x380
	v_and_b32_e32 v132, -16, v0
	v_add_u32_e32 v0, s2, v132
	v_ashrrev_i32_e32 v1, 31, v0
	v_lshlrev_b64 v[0:1], 12, v[0:1]
	s_lshl_b32 s2, s6, 7
	v_lshlrev_b32_e32 v2, 2, v146
	s_mov_b32 s3, 0
	v_lshl_add_u64 v[0:1], s[8:9], 0, v[0:1]
	s_and_b32 s2, s2, 0xf80
	v_and_b32_e32 v134, 28, v2
	v_lshl_add_u64 v[0:1], v[0:1], 0, s[2:3]
	v_mov_b32_e32 v137, 0
	v_lshlrev_b32_e32 v136, 2, v134
	v_lshl_add_u64 v[56:57], v[0:1], 0, v[136:137]
	s_mov_b32 s2, 0xd801000
	v_add_co_u32_e32 v4, vcc, s2, v56
	s_mov_b32 s2, 0xd803000
	s_nop 0
	v_addc_co_u32_e32 v5, vcc, 0, v57, vcc
	v_add_co_u32_e32 v12, vcc, s2, v56
	s_mov_b32 s2, 0xd805000
	s_nop 0
	v_addc_co_u32_e32 v13, vcc, 0, v57, vcc
	v_add_co_u32_e32 v20, vcc, s2, v56
	s_mov_b32 s2, 0xd807000
	s_nop 0
	v_addc_co_u32_e32 v21, vcc, 0, v57, vcc
	v_add_co_u32_e32 v32, vcc, s2, v56
	s_mov_b32 s2, 0xd809000
	s_nop 0
	v_addc_co_u32_e32 v33, vcc, 0, v57, vcc
	v_add_co_u32_e32 v40, vcc, s2, v56
	s_mov_b32 s2, 0xd80b000
	s_nop 0
	v_addc_co_u32_e32 v41, vcc, 0, v57, vcc
	v_add_co_u32_e32 v48, vcc, s2, v56
	s_mov_b32 s2, 0xd80d000
	s_nop 0
	v_addc_co_u32_e32 v49, vcc, 0, v57, vcc
	v_add_co_u32_e32 v58, vcc, s2, v56
	s_mov_b32 s2, 0xd80f000
	s_nop 0
	v_addc_co_u32_e32 v59, vcc, 0, v57, vcc
	v_add_co_u32_e32 v64, vcc, s2, v56
	global_load_dwordx4 v[28:31], v[4:5], off offset:-4096 nt
	global_load_dwordx4 v[0:3], v[4:5], off nt
	v_addc_co_u32_e32 v65, vcc, 0, v57, vcc
	global_load_dwordx4 v[4:7], v[12:13], off offset:-4096 nt
	global_load_dwordx4 v[8:11], v[12:13], off nt
	s_nop 0
	global_load_dwordx4 v[12:15], v[20:21], off offset:-4096 nt
	global_load_dwordx4 v[16:19], v[20:21], off nt
	s_nop 0
	global_load_dwordx4 v[20:23], v[32:33], off offset:-4096 nt
	global_load_dwordx4 v[24:27], v[32:33], off nt
	s_nop 0
	global_load_dwordx4 v[32:35], v[40:41], off offset:-4096 nt
	global_load_dwordx4 v[36:39], v[40:41], off nt
	s_nop 0
	global_load_dwordx4 v[40:43], v[48:49], off offset:-4096 nt
	global_load_dwordx4 v[44:47], v[48:49], off nt
	s_nop 0
	global_load_dwordx4 v[48:51], v[58:59], off offset:-4096 nt
	global_load_dwordx4 v[52:55], v[58:59], off nt
	s_nop 0
	global_load_dwordx4 v[56:59], v[64:65], off offset:-4096 nt
	global_load_dwordx4 v[60:63], v[64:65], off nt
	s_lshl_b32 s19, s6, 5
	s_add_u32 s20, s10, 0x2900000
	v_readlane_b32 s8, v243, 0
	s_addc_u32 s21, s11, 0
	s_lshl_b32 s2, s8, 3
	s_add_i32 s2, s2, s94
	s_lshl_b32 s7, s38, 3
	s_sub_i32 s2, s2, s7
	s_lshl_b32 s7, s2, 2
	s_lshr_b32 s6, s6, 9
	s_and_b32 s22, s7, 0x380
	s_add_i32 s23, s2, 0x300
	s_mul_hi_u32 s7, s6, 0x300000
	s_mul_i32 s6, s6, 0x300000
	s_add_u32 s6, s10, s6
	v_ashrrev_i32_e32 v133, 31, v132
	s_addc_u32 s7, s11, s7
	v_lshl_add_u64 v[64:65], s[6:7], 0, v[132:133]
	s_mov_b64 s[6:7], 0xcb00000
	v_lshl_add_u64 v[138:139], v[64:65], 0, s[6:7]
	v_readlane_b32 s6, v243, 6
	s_lshl_b32 s2, s2, 6
	s_lshr_b32 s6, s6, 1
	s_and_b32 s2, s2, 0x700
	s_and_b32 s6, s6, 0x60
	s_or_b32 s2, s2, s6
	v_or_b32_e32 v64, s2, v134
	v_lshlrev_b32_e32 v140, 10, v64
	v_mov_b32_e32 v141, v137
	s_movk_i32 s24, 0x2000
	s_movk_i32 s25, 0x4000
	s_movk_i32 s26, 0x6000
	s_mov_b32 s27, 0x8000
	s_mov_b32 s28, 0xa000
	s_mov_b32 s29, 0xb000
	s_mov_b32 s30, 0xc000
	s_mov_b32 s31, 0xc3e00000
	s_mov_b64 s[6:7], 0x300000
	v_mov_b32_e32 v135, 0x43e00000
	v_readlane_b32 s9, v243, 1
	s_branch .LBB0_1240
.LBB0_1238:
	v_mul_f32_e32 v128, 0x42000000, v111
	v_mul_f32_e32 v129, 0x42000000, v71
	v_med3_f32 v131, v128, s31, v135
	v_med3_f32 v129, v129, s31, v135
	v_mov_b32_e32 v128, v137
	v_cvt_pk_fp8_f32 v128, v131, v129
	v_mul_f32_e32 v130, 0x42000000, v67
	v_mul_f32_e32 v129, 0x42000000, v79
	v_med3_f32 v130, v130, s31, v135
	v_med3_f32 v129, v129, s31, v135
	v_cvt_pk_fp8_f32 v128, v130, v129 op_sel:[0,0,1]
	v_mul_f32_e32 v129, 0x42000000, v75
	v_mul_f32_e32 v130, 0x42000000, v87
	v_med3_f32 v136, v129, s31, v135
	v_med3_f32 v130, v130, s31, v135
	v_mov_b32_e32 v129, v137
	v_cvt_pk_fp8_f32 v129, v136, v130
	v_mul_f32_e32 v131, 0x42000000, v83
	v_mul_f32_e32 v130, 0x42000000, v95
	v_med3_f32 v131, v131, s31, v135
	v_med3_f32 v130, v130, s31, v135
	v_cvt_pk_fp8_f32 v129, v131, v130 op_sel:[0,0,1]
	v_mul_f32_e32 v130, 0x42000000, v91
	v_mul_f32_e32 v131, 0x42000000, v103
	v_med3_f32 v142, v130, s31, v135
	v_med3_f32 v131, v131, s31, v135
	v_mov_b32_e32 v130, v137
	v_cvt_pk_fp8_f32 v130, v142, v131
	v_mul_f32_e32 v136, 0x42000000, v99
	v_mul_f32_e32 v131, 0x42000000, v107
	v_med3_f32 v136, v136, s31, v135
	v_med3_f32 v131, v131, s31, v135
	v_cvt_pk_fp8_f32 v130, v136, v131 op_sel:[0,0,1]
	v_mul_f32_e32 v131, 0x42000000, v115
	v_mul_f32_e32 v136, 0x42000000, v119
	v_med3_f32 v143, v131, s31, v135
	v_med3_f32 v136, v136, s31, v135
	v_mov_b32_e32 v131, v137
	v_cvt_pk_fp8_f32 v131, v143, v136
	v_mul_f32_e32 v142, 0x42000000, v123
	v_mul_f32_e32 v136, 0x42000000, v127
	v_med3_f32 v142, v142, s31, v135
	v_med3_f32 v136, v136, s31, v135
	v_cvt_pk_fp8_f32 v131, v142, v136 op_sel:[0,0,1]
	v_or_b32_e32 v136, s8, v144
	s_add_u32 s8, s2, s22
	s_addc_u32 s9, s12, 0
	s_addk_i32 s18, 0x800
	s_addk_i32 s19, 0x4000
	s_addk_i32 s23, 0x200
	v_lshl_add_u64 v[142:143], s[8:9], 0, v[132:133]
	v_lshlrev_b32_e32 v136, 10, v136
	s_cmpk_gt_i32 s34, 0x11ff
	v_lshl_add_u64 v[142:143], v[142:143], 0, v[136:137]
	v_lshl_add_u64 v[138:139], v[138:139], 0, s[6:7]
	s_cselect_b64 s[10:11], -1, 0
	global_store_dwordx4 v[142:143], v[128:131], off

.LBB0_1240:
	s_add_i32 s34, s23, 0xfffffe00
	s_cmpk_lt_i32 s34, 0x1300
	s_cselect_b64 s[10:11], -1, 0
	s_mov_b64 s[8:9], -1
	s_and_b64 vcc, exec, s[10:11]
	s_cbranch_vccnz .LBB0_1242
	s_and_b32 s2, s18, 0x380
	s_mov_b64 s[8:9], 0
.LBB0_1242:
	s_add_i32 s35, s23, 0xffffff00
	s_andn2_b64 vcc, exec, s[8:9]
	s_mov_b64 s[8:9], 0
	s_cbranch_vccnz .LBB0_1244
	s_bitcmp0_b32 s34, 8
	s_cselect_b64 s[8:9], -1, 0
	s_and_b64 s[12:13], s[8:9], exec
	s_cselect_b32 s2, 0x108, s16
	s_add_u32 s12, s0, s2
	s_addc_u32 s13, s1, 0
	s_load_dwordx2 s[12:13], s[12:13], 0x0
	s_lshr_b32 s2, s35, 9
	s_add_i32 s2, s2, 54
	s_lshl_b64 s[14:15], s[2:3], 22
	v_lshlrev_b32_e32 v136, 2, v134
	s_waitcnt lgkmcnt(0)
	s_add_u32 s12, s12, s14
	s_addc_u32 s13, s13, s15
	s_and_b32 s14, s18, 0x380
	v_add_u32_e32 v64, s14, v132
	v_ashrrev_i32_e32 v65, 31, v64
	s_and_b32 s2, s19, 0x3e0
	v_lshlrev_b64 v[64:65], 12, v[64:65]
	v_lshl_add_u64 v[64:65], s[12:13], 0, v[64:65]
	s_lshl_b32 s2, s2, 2
	v_lshl_add_u64 v[64:65], v[64:65], 0, s[2:3]
	v_lshl_add_u64 v[120:121], v[64:65], 0, v[136:137]
	v_add_co_u32_e32 v72, vcc, s24, v120
	s_mov_b32 s2, s14
	s_nop 0
	v_addc_co_u32_e32 v73, vcc, 0, v121, vcc
	v_add_co_u32_e32 v80, vcc, s25, v120
	global_load_dwordx4 v[68:71], v[72:73], off offset:-4096 nt
	global_load_dwordx4 v[64:67], v[72:73], off nt
	v_addc_co_u32_e32 v81, vcc, 0, v121, vcc
	v_add_co_u32_e32 v88, vcc, s26, v120
	global_load_dwordx4 v[76:79], v[80:81], off offset:-4096 nt
	global_load_dwordx4 v[72:75], v[80:81], off nt
	v_addc_co_u32_e32 v89, vcc, 0, v121, vcc
	v_add_co_u32_e32 v96, vcc, s27, v120
	global_load_dwordx4 v[84:87], v[88:89], off offset:-4096 nt
	global_load_dwordx4 v[80:83], v[88:89], off nt
	v_addc_co_u32_e32 v97, vcc, 0, v121, vcc
	v_add_co_u32_e32 v104, vcc, s28, v120
	global_load_dwordx4 v[92:95], v[96:97], off offset:-4096 nt
	global_load_dwordx4 v[88:91], v[96:97], off nt
	v_addc_co_u32_e32 v105, vcc, 0, v121, vcc
	v_add_co_u32_e32 v112, vcc, s29, v120
	global_load_dwordx4 v[100:103], v[104:105], off offset:-4096 nt
	global_load_dwordx4 v[96:99], v[104:105], off nt
	v_addc_co_u32_e32 v113, vcc, 0, v121, vcc
	global_load_dwordx4 v[108:111], v[120:121], off nt
	global_load_dwordx4 v[104:107], v[112:113], off nt
	v_add_co_u32_e32 v112, vcc, 0xc000, v120
	s_nop 1
	v_addc_co_u32_e32 v113, vcc, 0, v121, vcc
	v_add_co_u32_e32 v116, vcc, 0xd000, v120
	s_nop 1
	v_addc_co_u32_e32 v117, vcc, 0, v121, vcc
	v_add_co_u32_e32 v122, vcc, 0xe000, v120
	global_load_dwordx4 v[112:115], v[112:113], off nt
	s_nop 0
	global_load_dwordx4 v[116:119], v[116:117], off nt
	v_addc_co_u32_e32 v123, vcc, 0, v121, vcc
	v_add_co_u32_e32 v124, vcc, 0xf000, v120
	s_nop 1
	v_addc_co_u32_e32 v125, vcc, 0, v121, vcc
	global_load_dwordx4 v[120:123], v[122:123], off nt
	s_nop 0
	global_load_dwordx4 v[124:127], v[124:125], off nt

.LBB0_1249:
	s_nop 0
	v_mul_f32_e32 v128, 0x42000000, v29
	v_mul_f32_e32 v129, 0x42000000, v1
	v_med3_f32 v131, v128, s31, v135
	v_med3_f32 v129, v129, s31, v135
	v_mov_b32_e32 v128, v137
	v_cvt_pk_fp8_f32 v128, v131, v129
	v_mul_f32_e32 v130, 0x42000000, v5
	v_mul_f32_e32 v129, 0x42000000, v9
	v_med3_f32 v130, v130, s31, v135
	v_med3_f32 v129, v129, s31, v135
	v_cvt_pk_fp8_f32 v128, v130, v129 op_sel:[0,0,1]
	v_mul_f32_e32 v129, 0x42000000, v13
	v_mul_f32_e32 v130, 0x42000000, v17
	v_med3_f32 v136, v129, s31, v135
	v_med3_f32 v130, v130, s31, v135
	v_mov_b32_e32 v129, v137
	v_cvt_pk_fp8_f32 v129, v136, v130
	v_mul_f32_e32 v131, 0x42000000, v21
	v_mul_f32_e32 v130, 0x42000000, v25
	v_med3_f32 v131, v131, s31, v135
	v_med3_f32 v130, v130, s31, v135
	v_cvt_pk_fp8_f32 v129, v131, v130 op_sel:[0,0,1]
	v_mul_f32_e32 v130, 0x42000000, v33
	v_mul_f32_e32 v131, 0x42000000, v37
	v_med3_f32 v145, v130, s31, v135
	v_med3_f32 v131, v131, s31, v135
	v_mov_b32_e32 v130, v137
	v_cvt_pk_fp8_f32 v130, v145, v131
	v_mul_f32_e32 v136, 0x42000000, v41
	v_mul_f32_e32 v131, 0x42000000, v45
	v_med3_f32 v136, v136, s31, v135
	v_med3_f32 v131, v131, s31, v135
	v_cvt_pk_fp8_f32 v130, v136, v131 op_sel:[0,0,1]
	v_mul_f32_e32 v131, 0x42000000, v49
	v_mul_f32_e32 v136, 0x42000000, v53
	v_med3_f32 v147, v131, s31, v135
	v_med3_f32 v136, v136, s31, v135
	v_mov_b32_e32 v131, v137
	v_cvt_pk_fp8_f32 v131, v147, v136
	s_lshl_b32 s37, s34, 5
	s_lshl_b32 s40, s34, 6
	v_mul_f32_e32 v145, 0x42000000, v57
	v_mul_f32_e32 v136, 0x42000000, v61
	s_and_b32 s40, s40, 0x700
	s_and_b32 s37, s37, 0x60
	v_med3_f32 v145, v145, s31, v135
	v_med3_f32 v136, v136, s31, v135
	s_or_b32 s37, s37, s40
	v_cvt_pk_fp8_f32 v131, v145, v136 op_sel:[0,0,1]
	s_add_u32 s14, s14, s2
	s_addc_u32 s15, s15, 0
	v_lshl_add_u64 v[148:149], v[142:143], 0, s[14:15]
	global_store_dwordx4 v[148:149], v[128:131], off
	s_add_u32 s12, s12, s2
	s_addc_u32 s13, s13, 0
	v_mul_f32_e32 v128, 0x42000000, v30
	v_mul_f32_e32 v129, 0x42000000, v2
	v_med3_f32 v131, v128, s31, v135
	v_med3_f32 v129, v129, s31, v135
	v_mov_b32_e32 v128, v137
	v_cvt_pk_fp8_f32 v128, v131, v129
	v_mul_f32_e32 v130, 0x42000000, v6
	v_mul_f32_e32 v129, 0x42000000, v10
	v_med3_f32 v130, v130, s31, v135
	v_med3_f32 v129, v129, s31, v135
	v_cvt_pk_fp8_f32 v128, v130, v129 op_sel:[0,0,1]
	v_mul_f32_e32 v129, 0x42000000, v14
	v_mul_f32_e32 v130, 0x42000000, v18
	v_med3_f32 v136, v129, s31, v135
	v_med3_f32 v130, v130, s31, v135
	v_mov_b32_e32 v129, v137
	v_cvt_pk_fp8_f32 v129, v136, v130
	v_mul_f32_e32 v131, 0x42000000, v22
	v_mul_f32_e32 v130, 0x42000000, v26
	v_med3_f32 v131, v131, s31, v135
	v_med3_f32 v130, v130, s31, v135
	v_cvt_pk_fp8_f32 v129, v131, v130 op_sel:[0,0,1]
	v_mul_f32_e32 v130, 0x42000000, v34
	v_mul_f32_e32 v131, 0x42000000, v38
	v_med3_f32 v145, v130, s31, v135
	v_med3_f32 v131, v131, s31, v135
	v_mov_b32_e32 v130, v137
	v_cvt_pk_fp8_f32 v130, v145, v131
	v_mul_f32_e32 v136, 0x42000000, v42
	v_mul_f32_e32 v131, 0x42000000, v46
	v_med3_f32 v136, v136, s31, v135
	v_med3_f32 v131, v131, s31, v135
	v_cvt_pk_fp8_f32 v130, v136, v131 op_sel:[0,0,1]
	v_mul_f32_e32 v131, 0x42000000, v50
	v_mul_f32_e32 v136, 0x42000000, v54
	v_med3_f32 v147, v131, s31, v135
	v_med3_f32 v136, v136, s31, v135
	v_mov_b32_e32 v131, v137
	v_cvt_pk_fp8_f32 v131, v147, v136
	v_mul_f32_e32 v145, 0x42000000, v58
	v_mul_f32_e32 v136, 0x42000000, v62
	v_med3_f32 v145, v145, s31, v135
	v_med3_f32 v136, v136, s31, v135
	v_cvt_pk_fp8_f32 v131, v145, v136 op_sel:[0,0,1]
	v_lshl_add_u64 v[142:143], v[142:143], 0, s[12:13]
	v_or_b32_e32 v144, s37, v134
	s_andn2_b64 vcc, exec, s[10:11]
	global_store_dwordx4 v[142:143], v[128:131], off
	s_mov_b64 s[10:11], -1
	s_nop 0
	v_mul_f32_e32 v128, 0x42000000, v31
	v_mul_f32_e32 v129, 0x42000000, v3
	v_med3_f32 v131, v128, s31, v135
	v_med3_f32 v129, v129, s31, v135
	v_mov_b32_e32 v128, v137
	v_cvt_pk_fp8_f32 v128, v131, v129
	v_mul_f32_e32 v130, 0x42000000, v7
	v_mul_f32_e32 v129, 0x42000000, v11
	v_med3_f32 v130, v130, s31, v135
	v_med3_f32 v129, v129, s31, v135
	v_cvt_pk_fp8_f32 v128, v130, v129 op_sel:[0,0,1]
	v_mul_f32_e32 v129, 0x42000000, v15
	v_mul_f32_e32 v130, 0x42000000, v19
	v_med3_f32 v136, v129, s31, v135
	v_med3_f32 v130, v130, s31, v135
	v_mov_b32_e32 v129, v137
	v_cvt_pk_fp8_f32 v129, v136, v130
	v_mul_f32_e32 v131, 0x42000000, v23
	v_mul_f32_e32 v130, 0x42000000, v27
	v_med3_f32 v131, v131, s31, v135
	v_med3_f32 v130, v130, s31, v135
	v_cvt_pk_fp8_f32 v129, v131, v130 op_sel:[0,0,1]
	v_mul_f32_e32 v130, 0x42000000, v35
	v_mul_f32_e32 v131, 0x42000000, v39
	v_med3_f32 v142, v130, s31, v135
	v_med3_f32 v131, v131, s31, v135
	v_mov_b32_e32 v130, v137
	v_cvt_pk_fp8_f32 v130, v142, v131
	v_mul_f32_e32 v136, 0x42000000, v43
	v_mul_f32_e32 v131, 0x42000000, v47
	v_med3_f32 v136, v136, s31, v135
	v_med3_f32 v131, v131, s31, v135
	v_cvt_pk_fp8_f32 v130, v136, v131 op_sel:[0,0,1]
	v_mul_f32_e32 v131, 0x42000000, v51
	v_mul_f32_e32 v136, 0x42000000, v55
	v_med3_f32 v143, v131, s31, v135
	v_med3_f32 v136, v136, s31, v135
	v_mov_b32_e32 v131, v137
	v_cvt_pk_fp8_f32 v131, v143, v136
	v_mul_f32_e32 v142, 0x42000000, v59
	v_mul_f32_e32 v136, 0x42000000, v63
	v_med3_f32 v142, v142, s31, v135
	v_med3_f32 v136, v136, s31, v135
	v_cvt_pk_fp8_f32 v131, v142, v136 op_sel:[0,0,1]
	v_or_b32_e32 v136, s36, v144
	v_lshlrev_b32_e32 v136, 10, v136
	v_lshl_add_u64 v[142:143], v[136:137], 0, s[2:3]
	v_lshl_add_u64 v[142:143], v[138:139], 0, v[142:143]
	global_store_dwordx4 v[142:143], v[128:131], off
	s_cbranch_vccnz .LBB0_1239
	s_cmpk_gt_i32 s34, 0x11ff
	s_cbranch_scc1 .LBB0_1252
	s_add_u32 s10, s0, s17
	s_addc_u32 s11, s1, 0
	s_load_dwordx2 s[10:11], s[10:11], 0x0
	s_lshr_b32 s12, s23, 9
	s_mov_b32 s13, s3
	s_add_i32 s12, s12, 54
	s_lshl_b64 s[12:13], s[12:13], 22
	v_add_u32_e32 v0, s2, v132
	s_waitcnt lgkmcnt(0)
	s_add_u32 s10, s10, s12
	v_ashrrev_i32_e32 v1, 31, v0
	s_addc_u32 s11, s11, s13
	s_and_b32 s12, s19, 0x3e0
	v_lshlrev_b64 v[0:1], 12, v[0:1]
	v_lshl_add_u64 v[0:1], s[10:11], 0, v[0:1]
	s_lshl_b32 s2, s12, 2
	v_lshl_add_u64 v[0:1], v[0:1], 0, s[2:3]
	v_lshlrev_b32_e32 v136, 2, v134
	v_lshl_add_u64 v[56:57], v[0:1], 0, v[136:137]
	v_add_co_u32_e32 v8, vcc, s24, v56
	s_nop 1
	v_addc_co_u32_e32 v9, vcc, 0, v57, vcc
	v_add_co_u32_e32 v16, vcc, s25, v56
	global_load_dwordx4 v[0:3], v[8:9], off offset:-4096 nt
	global_load_dwordx4 v[4:7], v[8:9], off nt
	v_addc_co_u32_e32 v17, vcc, 0, v57, vcc
	v_add_co_u32_e32 v24, vcc, s26, v56
	global_load_dwordx4 v[8:11], v[16:17], off offset:-4096 nt
	global_load_dwordx4 v[12:15], v[16:17], off nt
	v_addc_co_u32_e32 v25, vcc, 0, v57, vcc
	v_add_co_u32_e32 v28, vcc, s27, v56
	global_load_dwordx4 v[16:19], v[24:25], off offset:-4096 nt
	global_load_dwordx4 v[20:23], v[24:25], off nt
	v_addc_co_u32_e32 v29, vcc, 0, v57, vcc
	global_load_dwordx4 v[24:27], v[28:29], off offset:-4096 nt
	global_load_dwordx4 v[32:35], v[28:29], off nt
	v_add_co_u32_e32 v28, vcc, s28, v56
	s_nop 1
	v_addc_co_u32_e32 v29, vcc, 0, v57, vcc
	global_load_dwordx4 v[36:39], v[28:29], off offset:-4096 nt
	global_load_dwordx4 v[40:43], v[28:29], off nt
	v_add_co_u32_e32 v28, vcc, s30, v56
	s_nop 1
	v_addc_co_u32_e32 v29, vcc, 0, v57, vcc
	v_add_co_u32_e32 v52, vcc, 0xd000, v56
	global_load_dwordx4 v[44:47], v[28:29], off offset:-4096 nt
	global_load_dwordx4 v[48:51], v[28:29], off nt
	v_addc_co_u32_e32 v53, vcc, 0, v57, vcc
	v_add_co_u32_e32 v58, vcc, 0xe000, v56
	global_load_dwordx4 v[28:31], v[56:57], off nt
	s_nop 0
	global_load_dwordx4 v[52:55], v[52:53], off nt
	v_addc_co_u32_e32 v59, vcc, 0, v57, vcc
	v_add_co_u32_e32 v60, vcc, 0xf000, v56
	s_nop 1
	v_addc_co_u32_e32 v61, vcc, 0, v57, vcc
	global_load_dwordx4 v[56:59], v[58:59], off nt
	s_nop 0
	global_load_dwordx4 v[60:63], v[60:61], off nt
.LBB0_1252:
	v_mul_f32_e32 v128, 0x42000000, v108
	v_mul_f32_e32 v129, 0x42000000, v68
	v_med3_f32 v131, v128, s31, v135
	v_med3_f32 v129, v129, s31, v135
	v_mov_b32_e32 v128, v137
	v_cvt_pk_fp8_f32 v128, v131, v129
	v_mul_f32_e32 v130, 0x42000000, v64
	v_mul_f32_e32 v129, 0x42000000, v76
	v_med3_f32 v130, v130, s31, v135
	v_med3_f32 v129, v129, s31, v135
	v_cvt_pk_fp8_f32 v128, v130, v129 op_sel:[0,0,1]
	v_mul_f32_e32 v129, 0x42000000, v72
	v_mul_f32_e32 v130, 0x42000000, v84
	v_med3_f32 v142, v129, s31, v135
	v_med3_f32 v130, v130, s31, v135
	v_mov_b32_e32 v129, v137
	v_cvt_pk_fp8_f32 v129, v142, v130
	v_mul_f32_e32 v131, 0x42000000, v80
	v_mul_f32_e32 v130, 0x42000000, v92
	v_med3_f32 v131, v131, s31, v135
	v_med3_f32 v130, v130, s31, v135
	v_cvt_pk_fp8_f32 v129, v131, v130 op_sel:[0,0,1]
	v_mul_f32_e32 v130, 0x42000000, v88
	v_mul_f32_e32 v131, 0x42000000, v100
	v_med3_f32 v143, v130, s31, v135
	v_med3_f32 v131, v131, s31, v135
	v_mov_b32_e32 v130, v137
	v_cvt_pk_fp8_f32 v130, v143, v131
	v_mul_f32_e32 v142, 0x42000000, v96
	v_mul_f32_e32 v131, 0x42000000, v104
	v_med3_f32 v142, v142, s31, v135
	v_med3_f32 v131, v131, s31, v135
	v_cvt_pk_fp8_f32 v130, v142, v131 op_sel:[0,0,1]
	v_mul_f32_e32 v131, 0x42000000, v112
	v_mul_f32_e32 v142, 0x42000000, v116
	v_med3_f32 v145, v131, s31, v135
	v_med3_f32 v142, v142, s31, v135
	v_mov_b32_e32 v131, v137
	v_cvt_pk_fp8_f32 v131, v145, v142
	v_mul_f32_e32 v143, 0x42000000, v120
	v_mul_f32_e32 v142, 0x42000000, v124
	s_lshr_b32 s2, s35, 9
	v_med3_f32 v143, v143, s31, v135
	v_med3_f32 v142, v142, s31, v135
	s_add_i32 s2, s2, 54
	v_cvt_pk_fp8_f32 v131, v143, v142 op_sel:[0,0,1]
	s_mul_hi_u32 s10, s2, 0x300000
	s_mul_i32 s2, s2, 0x300000
	s_add_u32 s2, s20, s2
	v_lshlrev_b32_e32 v136, 10, v144
	s_addc_u32 s12, s21, s10
	s_mov_b64 s[10:11], -1
	s_andn2_b64 vcc, exec, s[8:9]
	v_mul_f32_e32 v172, 0x42000000, v109
	v_mul_f32_e32 v173, 0x42000000, v69
	v_mul_f32_e32 v174, 0x42000000, v65
	v_mul_f32_e32 v175, 0x42000000, v77
	v_mul_f32_e32 v170, 0x42000000, v73
	v_mul_f32_e32 v171, 0x42000000, v85
	v_mul_f32_e32 v168, 0x42000000, v81
	v_mul_f32_e32 v169, 0x42000000, v93
	v_mul_f32_e32 v164, 0x42000000, v89
	v_mul_f32_e32 v165, 0x42000000, v101
	v_mul_f32_e32 v166, 0x42000000, v97
	v_mul_f32_e32 v167, 0x42000000, v105
	v_mul_f32_e32 v162, 0x42000000, v113
	v_mul_f32_e32 v163, 0x42000000, v117
	v_mul_f32_e32 v160, 0x42000000, v121
	v_mul_f32_e32 v161, 0x42000000, v125
	v_mul_f32_e32 v156, 0x42000000, v110
	v_mul_f32_e32 v157, 0x42000000, v70
	v_mul_f32_e32 v158, 0x42000000, v66
	v_mul_f32_e32 v159, 0x42000000, v78
	v_mul_f32_e32 v154, 0x42000000, v74
	v_mul_f32_e32 v155, 0x42000000, v86
	v_mul_f32_e32 v152, 0x42000000, v82
	v_mul_f32_e32 v153, 0x42000000, v94
	v_mul_f32_e32 v148, 0x42000000, v90
	v_mul_f32_e32 v149, 0x42000000, v102
	v_mul_f32_e32 v150, 0x42000000, v98
	v_mul_f32_e32 v151, 0x42000000, v106
	v_mul_f32_e32 v145, 0x42000000, v114
	v_mul_f32_e32 v147, 0x42000000, v118
	v_mul_f32_e32 v142, 0x42000000, v122
	v_mul_f32_e32 v143, 0x42000000, v126
	s_cbranch_vccnz .LBB0_1254
	v_med3_f32 v177, v172, s31, v135
	v_med3_f32 v178, v173, s31, v135
	v_mov_b32_e32 v176, v137
	v_cvt_pk_fp8_f32 v176, v177, v178
	v_med3_f32 v178, v170, s31, v135
	v_med3_f32 v181, v171, s31, v135
	v_mov_b32_e32 v177, v137
	v_cvt_pk_fp8_f32 v177, v178, v181
	v_med3_f32 v179, v174, s31, v135
	v_med3_f32 v180, v175, s31, v135
	v_cvt_pk_fp8_f32 v176, v179, v180 op_sel:[0,0,1]
	v_med3_f32 v178, v168, s31, v135
	v_med3_f32 v179, v169, s31, v135
	v_cvt_pk_fp8_f32 v177, v178, v179 op_sel:[0,0,1]
	v_med3_f32 v179, v164, s31, v135
	v_med3_f32 v180, v165, s31, v135
	v_mov_b32_e32 v178, v137
	v_cvt_pk_fp8_f32 v178, v179, v180
	v_med3_f32 v180, v162, s31, v135
	v_med3_f32 v183, v163, s31, v135
	v_mov_b32_e32 v179, v137
	v_cvt_pk_fp8_f32 v179, v180, v183
	v_med3_f32 v181, v166, s31, v135
	v_med3_f32 v182, v167, s31, v135
	v_cvt_pk_fp8_f32 v178, v181, v182 op_sel:[0,0,1]
	v_med3_f32 v180, v160, s31, v135
	v_med3_f32 v181, v161, s31, v135
	v_cvt_pk_fp8_f32 v179, v180, v181 op_sel:[0,0,1]
	v_med3_f32 v181, v156, s31, v135
	v_med3_f32 v182, v157, s31, v135
	v_mov_b32_e32 v180, v137
	v_cvt_pk_fp8_f32 v180, v181, v182
	v_med3_f32 v182, v154, s31, v135
	v_med3_f32 v187, v155, s31, v135
	v_mov_b32_e32 v181, v137
	v_cvt_pk_fp8_f32 v181, v182, v187
	v_med3_f32 v183, v158, s31, v135
	v_med3_f32 v186, v159, s31, v135
	v_cvt_pk_fp8_f32 v180, v183, v186 op_sel:[0,0,1]
	v_med3_f32 v182, v152, s31, v135
	v_med3_f32 v183, v153, s31, v135
	v_cvt_pk_fp8_f32 v181, v182, v183 op_sel:[0,0,1]
	v_med3_f32 v183, v148, s31, v135
	v_med3_f32 v186, v149, s31, v135
	v_mov_b32_e32 v182, v137
	v_cvt_pk_fp8_f32 v182, v183, v186
	v_med3_f32 v186, v145, s31, v135
	v_med3_f32 v189, v147, s31, v135
	v_mov_b32_e32 v183, v137
	v_cvt_pk_fp8_f32 v183, v186, v189
	s_add_u32 s8, s2, s22
	v_med3_f32 v187, v150, s31, v135
	v_med3_f32 v188, v151, s31, v135
	s_addc_u32 s9, s12, 0
	v_cvt_pk_fp8_f32 v182, v187, v188 op_sel:[0,0,1]
	v_med3_f32 v186, v142, s31, v135
	v_med3_f32 v187, v143, s31, v135
	v_lshl_add_u64 v[184:185], s[8:9], 0, v[132:133]
	v_cvt_pk_fp8_f32 v183, v186, v187 op_sel:[0,0,1]
	v_lshl_add_u64 v[184:185], v[184:185], 0, v[136:137]
	s_mov_b64 s[10:11], 0
	global_store_dwordx4 v[184:185], v[128:131], off
	global_store_dwordx4 v[184:185], v[176:179], off offset:1024
	global_store_dwordx4 v[184:185], v[180:183], off offset:2048

.LBB0_1451:
	s_load_dwordx4 s[0:3], s[8:9], 0x138
	s_waitcnt lgkmcnt(0)
	s_mov_b64 s[4:5], s[0:1]
	s_cmp_lt_i32 s4, 12
	s_cselect_b64 s[0:1], -1, 0
	s_cmp_gt_i32 s5, 11
	s_cselect_b64 s[2:3], -1, 0
	s_and_b64 s[0:1], s[0:1], s[2:3]
	s_andn2_b64 vcc, exec, s[0:1]
	s_cbranch_vccnz .LBB0_1535
	s_mov_b64 s[24:25], s[8:9]
	v_mbcnt_lo_u32_b32 v202, -1, 0
	v_mbcnt_hi_u32_b32 v202, -1, v202
	s_load_dword s0, s[8:9], 0x148
	s_waitcnt lgkmcnt(0)
	v_writelane_b32 v241, s0, 18
	s_nop 1
	v_writelane_b32 v241, s1, 19
	s_add_u32 s0, s8, 0x148
	s_addc_u32 s1, s9, 0
	v_writelane_b32 v241, s0, 34
	s_nop 1
	v_writelane_b32 v241, s1, 35
	v_readlane_b32 s0, v243, 0
	s_cmpk_gt_i32 s0, 0xff
	v_readlane_b32 s1, v243, 1
	s_cbranch_scc1 .LBB0_1482
	v_readlane_b32 s0, v243, 7
	v_readlane_b32 s1, v243, 8
	v_readlane_b32 s4, v243, 0
	v_readlane_b32 s6, v243, 12
	s_load_dwordx2 s[2:3], s[0:1], 0x130
	s_lshr_b32 s7, s6, 2
	s_and_b32 s8, s6, 3
	s_lshr_b32 s9, s4, 4
	s_bfe_u32 s10, s4, 0x20002
	s_and_b32 s11, s4, 3
	v_and_b32_e32 v160, 15, v202
	v_lshrrev_b32_e32 v161, 4, v202
	v_lshlrev_b32_e32 v209, 2, v202
	s_lshl_b32 s50, s7, 15
	v_xor_b32_e32 v178, v161, v160
	v_lshlrev_b32_e32 v178, 4, v178
	v_lshl_add_u32 v162, v160, 9, v178
	v_add_u32_e32 v162, s50, v162
	s_lshl_b32 s51, s11, 6
	s_lshl_b32 s52, s8, 4
	s_add_i32 s51, s51, s52
	v_add_u32_e32 v179, s51, v160
	v_lshrrev_b32_e32 v180, 3, v179
	v_and_b32_e32 v181, 7, v179
	v_lshlrev_b32_e32 v181, 1, v181
	v_lshlrev_b32_e32 v182, 2, v161
	v_add_u32_e32 v183, 0, v182
	v_xor_b32_e32 v184, v180, v183
	v_lshlrev_b32_e32 v184, 4, v184
	v_lshl_add_u32 v184, v183, 9, v184
	v_add3_u32 v165, v184, v181, s50
	v_add_u32_e32 v183, 1, v182
	v_xor_b32_e32 v184, v180, v183
	v_lshlrev_b32_e32 v184, 4, v184
	v_lshl_add_u32 v184, v183, 9, v184
	v_add3_u32 v166, v184, v181, s50
	v_add_u32_e32 v183, 2, v182
	v_xor_b32_e32 v184, v180, v183
	v_lshlrev_b32_e32 v184, 4, v184
	v_lshl_add_u32 v184, v183, 9, v184
	v_add3_u32 v167, v184, v181, s50
	v_add_u32_e32 v183, 3, v182
	v_xor_b32_e32 v184, v180, v183
	v_lshlrev_b32_e32 v184, 4, v184
	v_lshl_add_u32 v184, v183, 9, v184
	v_add3_u32 v168, v184, v181, s50
	v_lshrrev_b32_e32 v185, 5, v202
	v_and_b32_e32 v186, 31, v202
	s_lshl_b32 s51, s6, 4
	v_add_u32_e32 v187, 0, v185
	v_xor_b32_e32 v188, v186, v187
	v_lshlrev_b32_e32 v188, 4, v188
	v_add_u32_e32 v187, s51, v187
	v_lshl_add_u32 v211, v187, 11, v188
	v_add_u32_e32 v187, 2, v185
	v_xor_b32_e32 v188, v186, v187
	v_lshlrev_b32_e32 v188, 4, v188
	v_add_u32_e32 v187, s51, v187
	v_lshl_add_u32 v212, v187, 11, v188
	v_add_u32_e32 v187, 4, v185
	v_xor_b32_e32 v188, v186, v187
	v_lshlrev_b32_e32 v188, 4, v188
	v_add_u32_e32 v187, s51, v187
	v_lshl_add_u32 v213, v187, 11, v188
	v_add_u32_e32 v187, 6, v185
	v_xor_b32_e32 v188, v186, v187
	v_lshlrev_b32_e32 v188, 4, v188
	v_add_u32_e32 v187, s51, v187
	v_lshl_add_u32 v214, v187, 11, v188
	v_add_u32_e32 v187, 8, v185
	v_xor_b32_e32 v188, v186, v187
	v_lshlrev_b32_e32 v188, 4, v188
	v_add_u32_e32 v187, s51, v187
	v_lshl_add_u32 v215, v187, 11, v188
	v_add_u32_e32 v187, 10, v185
	v_xor_b32_e32 v188, v186, v187
	v_lshlrev_b32_e32 v188, 4, v188
	v_add_u32_e32 v187, s51, v187
	v_lshl_add_u32 v216, v187, 11, v188
	v_add_u32_e32 v187, 12, v185
	v_xor_b32_e32 v188, v186, v187
	v_lshlrev_b32_e32 v188, 4, v188
	v_add_u32_e32 v187, s51, v187
	v_lshl_add_u32 v217, v187, 11, v188
	v_add_u32_e32 v187, 14, v185
	v_xor_b32_e32 v188, v186, v187
	v_lshlrev_b32_e32 v188, 4, v188
	v_add_u32_e32 v187, s51, v187
	v_lshl_add_u32 v218, v187, 11, v188
	s_lshl_b32 s51, s6, 7
	s_add_i32 s51, s51, 0x20000
	v_lshl_add_u32 v207, v160, 3, s51
	s_lshl_b32 s51, s8, 7
	s_add_i32 s51, s51, 0x20000
	v_lshl_add_u32 v208, v160, 3, s51
	s_lshl_b32 s51, s7, 6
	v_add_u32_e32 v189, s51, v182
	s_lshl_b32 s51, s8, 4
	v_add_u32_e32 v190, s51, v160
	v_lshlrev_b32_e32 v190, 1, v190
	v_lshl_add_u32 v210, v189, 11, v190
	s_waitcnt lgkmcnt(0)
	s_lshl_b32 s50, s10, 9
	s_add_u32 s16, s2, s50
	s_addc_u32 s17, s3, 0
	s_add_u32 s16, s16, 0x1b900000
	s_addc_u32 s17, s17, 0
	s_lshl_b32 s50, s10, 9
	s_lshl_b32 s51, s11, 7
	s_add_i32 s50, s50, s51
	s_add_u32 s18, s2, s50
	s_addc_u32 s19, s3, 0
	s_add_u32 s18, s18, 0x13100000
	s_addc_u32 s19, s19, 0
	s_add_u32 s20, s2, s50
	s_addc_u32 s21, s3, 0
	s_add_u32 s20, s20, 0x29100000
	s_addc_u32 s21, s21, 0
	s_lshl_b32 s50, s4, 18
	s_add_u32 s22, s2, s50
	s_addc_u32 s23, s3, 0
	s_add_u32 s22, s22, 0x20100000
	s_addc_u32 s23, s23, 0
	s_lshl_b32 s50, s10, 10
	s_lshl_b32 s51, s11, 6
	s_add_i32 s50, s50, s51
	s_lshl_b32 s51, s8, 4
	s_add_i32 s50, s50, s51
	s_add_i32 s50, s50, 0
	s_lshl_b32 s50, s50, 9
	s_add_u32 s46, s2, s50
	s_addc_u32 s47, s3, 0
	s_add_u32 s46, s46, 0x1000000
	s_addc_u32 s47, s47, 0
	s_add_u32 s48, s46, 0x20000
	s_addc_u32 s49, s47, 0
	v_lshlrev_b32_e32 v178, 9, v160
	v_lshl_add_u32 v178, v161, 4, v178
	global_load_dwordx4 v[0:3], v178, s[46:47]
	global_load_dwordx4 v[4:7], v178, s[46:47] offset:64
	global_load_dwordx4 v[8:11], v178, s[46:47] offset:128
	global_load_dwordx4 v[12:15], v178, s[46:47] offset:192
	global_load_dwordx4 v[16:19], v178, s[46:47] offset:256
	global_load_dwordx4 v[20:23], v178, s[46:47] offset:320
	global_load_dwordx4 v[24:27], v178, s[46:47] offset:384
	global_load_dwordx4 v[28:31], v178, s[46:47] offset:448
	global_load_dwordx4 v[32:35], v178, s[48:49]
	global_load_dwordx4 v[36:39], v178, s[48:49] offset:64
	global_load_dwordx4 v[40:43], v178, s[48:49] offset:128
	global_load_dwordx4 v[44:47], v178, s[48:49] offset:192
	global_load_dwordx4 v[48:51], v178, s[48:49] offset:256
	global_load_dwordx4 v[52:55], v178, s[48:49] offset:320
	global_load_dwordx4 v[56:59], v178, s[48:49] offset:384
	global_load_dwordx4 v[60:63], v178, s[48:49] offset:448
	s_load_dwordx2 s[46:47], s[0:1], 0xa0
	s_load_dwordx2 s[48:49], s[0:1], 0xb0
	s_load_dwordx2 s[40:41], s[0:1], 0xb8
	s_lshl_b32 s50, s10, 8
	s_lshl_b32 s51, s11, 6
	s_add_i32 s50, s50, s51
	s_lshl_b32 s51, s8, 4
	s_add_i32 s50, s50, s51
	v_add_u32_e32 v179, s50, v160
	v_lshlrev_b32_e32 v179, 2, v179
	s_waitcnt lgkmcnt(0)
	global_load_dword v173, v179, s[46:47]
	global_load_dword v174, v179, s[48:49]
	global_load_dword v175, v179, s[40:41]
	v_cmp_le_u32_e64 s[34:35], 16, v202
	v_cmp_le_u32_e64 s[36:37], 32, v202
	v_add_u32_e32 v204, -16, v202
	v_add_u32_e32 v205, -32, v202
	v_add_u32_e32 v206, 48, v160
	s_cmp_eq_u32 s7, 1
	s_cselect_b64 s[38:39], -1, 0
	v_and_b32_e32 v204, 63, v204
	v_lshlrev_b32_e32 v204, 2, v204
	v_and_b32_e32 v205, 63, v205
	v_lshlrev_b32_e32 v205, 2, v205
	v_and_b32_e32 v206, 63, v206
	v_lshlrev_b32_e32 v206, 2, v206
	v_mov_b32_e32 v176, 0
	s_mov_b32 s53, 0xbfb8aa3b
	s_waitcnt vmcnt(0)
	v_mul_f32_e32 v173, s53, v173
	v_mul_f32_e32 v174, s53, v174
	v_mul_f32_e32 v175, s53, v175
	v_exp_f32_e32 v175, v175
	s_nop 0
	v_add_f32_e32 v180, 1.0, v175
	v_log_f32_e32 v180, v180
	v_mov_b32_e32 v181, 0x3eaaaaab
	v_fma_f32 v181, v175, v181, -0.5
	v_fma_f32 v181, v175, v181, 1.0
	v_mul_f32_e32 v181, v175, v181
	v_mul_f32_e32 v181, 0x3fb8aa3b, v181
	v_cmp_gt_f32_e32 vcc, 0x3cf5c28f, v175
	s_nop 1
	v_cndmask_b32_e32 v175, v180, v181, vcc
	v_mul_f32_e32 v175, 0xc1000000, v175
	s_mov_b32 s13, 0
	s_barrier
	s_cmp_lt_u32 s13, 2
	s_lshl_b32 s50, s13, 7
	s_lshl_b32 s51, s9, 8
	s_add_i32 s51, s51, 0x8000
	s_add_i32 s51, s51, s50
	s_lshl_b32 s59, s9, 11
	s_add_i32 s59, s59, s50
	s_addk_i32 s59, 0xff00
	s_cmp_lt_u32 s13, 2
	s_cselect_b32 s59, s51, s59
	s_lshl_b32 s52, s59, 11
	s_add_u32 s46, s16, s52
	s_addc_u32 s47, s17, 0
	s_lshl_b32 s52, s6, 13
	s_mov_b32 m0, s52
	s_add_i32 s52, s52, 0x400
	global_load_lds_dwordx4 v211, s[46:47]
	s_mov_b32 m0, s52
	s_add_i32 s52, s52, 0x400
	global_load_lds_dwordx4 v212, s[46:47]
	s_mov_b32 m0, s52
	s_add_i32 s52, s52, 0x400
	global_load_lds_dwordx4 v213, s[46:47]
	s_mov_b32 m0, s52
	s_add_i32 s52, s52, 0x400
	global_load_lds_dwordx4 v214, s[46:47]
	s_mov_b32 m0, s52
	s_add_i32 s52, s52, 0x400
	global_load_lds_dwordx4 v215, s[46:47]
	s_mov_b32 m0, s52
	s_add_i32 s52, s52, 0x400
	global_load_lds_dwordx4 v216, s[46:47]
	s_mov_b32 m0, s52
	s_add_i32 s52, s52, 0x400
	global_load_lds_dwordx4 v217, s[46:47]
	s_mov_b32 m0, s52
	s_nop 0
	global_load_lds_dwordx4 v218, s[46:47]
	s_waitcnt vmcnt(0)
	s_barrier
	s_cmp_eq_u32 s13, 17
	s_cbranch_scc1 .Lmylru_nodma_1
	s_add_i32 s58, s13, 1
	s_cmp_lt_u32 s58, 2
	s_lshl_b32 s50, s58, 7
	s_lshl_b32 s51, s9, 8
	s_add_i32 s51, s51, 0x8000
	s_add_i32 s51, s51, s50
	s_lshl_b32 s59, s9, 11
	s_add_i32 s59, s59, s50
	s_addk_i32 s59, 0xff00
	s_cmp_lt_u32 s58, 2
	s_cselect_b32 s59, s51, s59
	s_lshl_b32 s52, s59, 11
	s_add_u32 s46, s16, s52
	s_addc_u32 s47, s17, 0
	s_lshl_b32 s52, s6, 13
	s_add_i32 s52, s52, 0x10000
	s_mov_b32 m0, s52
	s_add_i32 s52, s52, 0x400
	global_load_lds_dwordx4 v211, s[46:47]
	s_mov_b32 m0, s52
	s_add_i32 s52, s52, 0x400
	global_load_lds_dwordx4 v212, s[46:47]
	s_mov_b32 m0, s52
	s_add_i32 s52, s52, 0x400
	global_load_lds_dwordx4 v213, s[46:47]
	s_mov_b32 m0, s52
	s_add_i32 s52, s52, 0x400
	global_load_lds_dwordx4 v214, s[46:47]
	s_mov_b32 m0, s52
	s_add_i32 s52, s52, 0x400
	global_load_lds_dwordx4 v215, s[46:47]
	s_mov_b32 m0, s52
	s_add_i32 s52, s52, 0x400
	global_load_lds_dwordx4 v216, s[46:47]
	s_mov_b32 m0, s52
	s_add_i32 s52, s52, 0x400
	global_load_lds_dwordx4 v217, s[46:47]
	s_mov_b32 m0, s52
	s_nop 0
	global_load_lds_dwordx4 v218, s[46:47]
.Lmylru_nodma_1:
	v_mov_b32_e32 v163, v162
	ds_read_b128 v[96:99], v163
	ds_read_b128 v[100:103], v163 offset:8192
	ds_read_b128 v[104:107], v163 offset:16384
	ds_read_b128 v[108:111], v163 offset:24576
	v_xor_b32_e32 v164, 0x40, v163
	ds_read_b128 v[112:115], v164
	ds_read_b128 v[116:119], v164 offset:8192
	ds_read_b128 v[120:123], v164 offset:16384
	ds_read_b128 v[124:127], v164 offset:24576
	s_waitcnt lgkmcnt(7)
	v_mfma_f32_16x16x32_bf16 v[64:67], v[96:99], v[0:3], 0
	v_mfma_f32_16x16x32_bf16 v[68:71], v[96:99], v[32:35], 0
	v_xor_b32_e32 v164, 0x80, v163
	ds_read_b128 v[96:99], v164
	s_waitcnt lgkmcnt(7)
	v_mfma_f32_16x16x32_bf16 v[72:75], v[100:103], v[0:3], 0
	v_mfma_f32_16x16x32_bf16 v[76:79], v[100:103], v[32:35], 0
	ds_read_b128 v[100:103], v164 offset:8192
	s_waitcnt lgkmcnt(7)
	v_mfma_f32_16x16x32_bf16 v[80:83], v[104:107], v[0:3], 0
	v_mfma_f32_16x16x32_bf16 v[84:87], v[104:107], v[32:35], 0
	ds_read_b128 v[104:107], v164 offset:16384
	s_waitcnt lgkmcnt(7)
	v_mfma_f32_16x16x32_bf16 v[88:91], v[108:111], v[0:3], 0
	v_mfma_f32_16x16x32_bf16 v[92:95], v[108:111], v[32:35], 0
	ds_read_b128 v[108:111], v164 offset:24576
	s_waitcnt lgkmcnt(7)
	v_mfma_f32_16x16x32_bf16 v[64:67], v[112:115], v[4:7], v[64:67]
	v_mfma_f32_16x16x32_bf16 v[68:71], v[112:115], v[36:39], v[68:71]
	v_xor_b32_e32 v164, 0xc0, v163
	ds_read_b128 v[112:115], v164
	s_waitcnt lgkmcnt(7)
	v_mfma_f32_16x16x32_bf16 v[72:75], v[116:119], v[4:7], v[72:75]
	v_mfma_f32_16x16x32_bf16 v[76:79], v[116:119], v[36:39], v[76:79]
	ds_read_b128 v[116:119], v164 offset:8192
	s_waitcnt lgkmcnt(7)
	v_mfma_f32_16x16x32_bf16 v[80:83], v[120:123], v[4:7], v[80:83]
	v_mfma_f32_16x16x32_bf16 v[84:87], v[120:123], v[36:39], v[84:87]
	ds_read_b128 v[120:123], v164 offset:16384
	s_waitcnt lgkmcnt(7)
	v_mfma_f32_16x16x32_bf16 v[88:91], v[124:127], v[4:7], v[88:91]
	v_mfma_f32_16x16x32_bf16 v[92:95], v[124:127], v[36:39], v[92:95]
	ds_read_b128 v[124:127], v164 offset:24576
	s_waitcnt lgkmcnt(7)
	v_mfma_f32_16x16x32_bf16 v[64:67], v[96:99], v[8:11], v[64:67]
	v_mfma_f32_16x16x32_bf16 v[68:71], v[96:99], v[40:43], v[68:71]
	v_xor_b32_e32 v164, 0x100, v163
	ds_read_b128 v[96:99], v164
	s_waitcnt lgkmcnt(7)
	v_mfma_f32_16x16x32_bf16 v[72:75], v[100:103], v[8:11], v[72:75]
	v_mfma_f32_16x16x32_bf16 v[76:79], v[100:103], v[40:43], v[76:79]
	ds_read_b128 v[100:103], v164 offset:8192
	s_waitcnt lgkmcnt(7)
	v_mfma_f32_16x16x32_bf16 v[80:83], v[104:107], v[8:11], v[80:83]
	v_mfma_f32_16x16x32_bf16 v[84:87], v[104:107], v[40:43], v[84:87]
	ds_read_b128 v[104:107], v164 offset:16384
	s_waitcnt lgkmcnt(7)
	v_mfma_f32_16x16x32_bf16 v[88:91], v[108:111], v[8:11], v[88:91]
	v_mfma_f32_16x16x32_bf16 v[92:95], v[108:111], v[40:43], v[92:95]
	ds_read_b128 v[108:111], v164 offset:24576
	s_waitcnt lgkmcnt(7)
	v_mfma_f32_16x16x32_bf16 v[64:67], v[112:115], v[12:15], v[64:67]
	v_mfma_f32_16x16x32_bf16 v[68:71], v[112:115], v[44:47], v[68:71]
	v_xor_b32_e32 v164, 0x140, v163
	ds_read_b128 v[112:115], v164
	s_waitcnt lgkmcnt(7)
	v_mfma_f32_16x16x32_bf16 v[72:75], v[116:119], v[12:15], v[72:75]
	v_mfma_f32_16x16x32_bf16 v[76:79], v[116:119], v[44:47], v[76:79]
	ds_read_b128 v[116:119], v164 offset:8192
	s_waitcnt lgkmcnt(7)
	v_mfma_f32_16x16x32_bf16 v[80:83], v[120:123], v[12:15], v[80:83]
	v_mfma_f32_16x16x32_bf16 v[84:87], v[120:123], v[44:47], v[84:87]
	ds_read_b128 v[120:123], v164 offset:16384
	s_waitcnt lgkmcnt(7)
	v_mfma_f32_16x16x32_bf16 v[88:91], v[124:127], v[12:15], v[88:91]
	v_mfma_f32_16x16x32_bf16 v[92:95], v[124:127], v[44:47], v[92:95]
	ds_read_b128 v[124:127], v164 offset:24576
	s_waitcnt lgkmcnt(7)
	v_mfma_f32_16x16x32_bf16 v[64:67], v[96:99], v[16:19], v[64:67]
	v_mfma_f32_16x16x32_bf16 v[68:71], v[96:99], v[48:51], v[68:71]
	v_xor_b32_e32 v164, 0x180, v163
	ds_read_b128 v[96:99], v164
	s_waitcnt lgkmcnt(7)
	v_mfma_f32_16x16x32_bf16 v[72:75], v[100:103], v[16:19], v[72:75]
	v_mfma_f32_16x16x32_bf16 v[76:79], v[100:103], v[48:51], v[76:79]
	ds_read_b128 v[100:103], v164 offset:8192
	s_waitcnt lgkmcnt(7)
	v_mfma_f32_16x16x32_bf16 v[80:83], v[104:107], v[16:19], v[80:83]
	v_mfma_f32_16x16x32_bf16 v[84:87], v[104:107], v[48:51], v[84:87]
	ds_read_b128 v[104:107], v164 offset:16384
	s_waitcnt lgkmcnt(7)
	v_mfma_f32_16x16x32_bf16 v[88:91], v[108:111], v[16:19], v[88:91]
	v_mfma_f32_16x16x32_bf16 v[92:95], v[108:111], v[48:51], v[92:95]
	ds_read_b128 v[108:111], v164 offset:24576
	s_waitcnt lgkmcnt(7)
	v_mfma_f32_16x16x32_bf16 v[64:67], v[112:115], v[20:23], v[64:67]
	v_mfma_f32_16x16x32_bf16 v[68:71], v[112:115], v[52:55], v[68:71]
	v_xor_b32_e32 v164, 0x1c0, v163
	ds_read_b128 v[112:115], v164
	s_waitcnt lgkmcnt(7)
	v_mfma_f32_16x16x32_bf16 v[72:75], v[116:119], v[20:23], v[72:75]
	v_mfma_f32_16x16x32_bf16 v[76:79], v[116:119], v[52:55], v[76:79]
	ds_read_b128 v[116:119], v164 offset:8192
	s_waitcnt lgkmcnt(7)
	v_mfma_f32_16x16x32_bf16 v[80:83], v[120:123], v[20:23], v[80:83]
	v_mfma_f32_16x16x32_bf16 v[84:87], v[120:123], v[52:55], v[84:87]
	ds_read_b128 v[120:123], v164 offset:16384
	s_waitcnt lgkmcnt(7)
	v_mfma_f32_16x16x32_bf16 v[88:91], v[124:127], v[20:23], v[88:91]
	v_mfma_f32_16x16x32_bf16 v[92:95], v[124:127], v[52:55], v[92:95]
	ds_read_b128 v[124:127], v164 offset:24576
	s_waitcnt lgkmcnt(7)
	v_mfma_f32_16x16x32_bf16 v[64:67], v[96:99], v[24:27], v[64:67]
	v_mfma_f32_16x16x32_bf16 v[68:71], v[96:99], v[56:59], v[68:71]
	s_waitcnt lgkmcnt(6)
	v_mfma_f32_16x16x32_bf16 v[72:75], v[100:103], v[24:27], v[72:75]
	v_mfma_f32_16x16x32_bf16 v[76:79], v[100:103], v[56:59], v[76:79]
	s_waitcnt lgkmcnt(5)
	v_mfma_f32_16x16x32_bf16 v[80:83], v[104:107], v[24:27], v[80:83]
	v_mfma_f32_16x16x32_bf16 v[84:87], v[104:107], v[56:59], v[84:87]
	s_waitcnt lgkmcnt(4)
	v_mfma_f32_16x16x32_bf16 v[88:91], v[108:111], v[24:27], v[88:91]
	v_mfma_f32_16x16x32_bf16 v[92:95], v[108:111], v[56:59], v[92:95]
	s_waitcnt lgkmcnt(3)
	v_mfma_f32_16x16x32_bf16 v[64:67], v[112:115], v[28:31], v[64:67]
	v_mfma_f32_16x16x32_bf16 v[68:71], v[112:115], v[60:63], v[68:71]
	s_waitcnt lgkmcnt(2)
	v_mfma_f32_16x16x32_bf16 v[72:75], v[116:119], v[28:31], v[72:75]
	v_mfma_f32_16x16x32_bf16 v[76:79], v[116:119], v[60:63], v[76:79]
	s_waitcnt lgkmcnt(1)
	v_mfma_f32_16x16x32_bf16 v[80:83], v[120:123], v[28:31], v[80:83]
	v_mfma_f32_16x16x32_bf16 v[84:87], v[120:123], v[60:63], v[84:87]
	s_waitcnt lgkmcnt(0)
	v_mfma_f32_16x16x32_bf16 v[88:91], v[124:127], v[28:31], v[88:91]
	v_mfma_f32_16x16x32_bf16 v[92:95], v[124:127], v[60:63], v[92:95]
	v_mov_b32_e32 v169, v165
	v_mov_b32_e32 v170, v166
	v_mov_b32_e32 v171, v167
	v_mov_b32_e32 v172, v168
	ds_read_u16 v144, v169
	ds_read_u16 v145, v170
	ds_read_u16 v146, v171
	ds_read_u16 v147, v172
	ds_read_u16 v148, v169 offset:8192
	ds_read_u16 v149, v170 offset:8192
	ds_read_u16 v150, v171 offset:8192
	ds_read_u16 v151, v172 offset:8192
	ds_read_u16 v152, v169 offset:16384
	ds_read_u16 v153, v170 offset:16384
	ds_read_u16 v154, v171 offset:16384
	ds_read_u16 v155, v172 offset:16384
	ds_read_u16 v156, v169 offset:24576
	ds_read_u16 v157, v170 offset:24576
	ds_read_u16 v158, v171 offset:24576
	ds_read_u16 v159, v172 offset:24576
	s_nop 7
	v_fma_f32 v178, v64, s53, v173
	v_fma_f32 v179, v65, s53, v173
	v_fma_f32 v180, v66, s53, v173
	v_fma_f32 v181, v67, s53, v173
	v_fma_f32 v182, v72, s53, v173
	v_fma_f32 v183, v73, s53, v173
	v_fma_f32 v184, v74, s53, v173
	v_fma_f32 v185, v75, s53, v173
	v_fma_f32 v186, v68, s53, v174
	v_fma_f32 v187, v69, s53, v174
	v_fma_f32 v188, v70, s53, v174
	v_fma_f32 v189, v71, s53, v174
	v_fma_f32 v190, v76, s53, v174
	v_fma_f32 v191, v77, s53, v174
	v_fma_f32 v192, v78, s53, v174
	v_fma_f32 v193, v79, s53, v174
	v_exp_f32_e32 v178, v178
	v_exp_f32_e32 v179, v179
	v_exp_f32_e32 v180, v180
	v_exp_f32_e32 v181, v181
	v_exp_f32_e32 v182, v182
	v_exp_f32_e32 v183, v183
	v_exp_f32_e32 v184, v184
	v_exp_f32_e32 v185, v185
	v_exp_f32_e32 v186, v186
	v_exp_f32_e32 v187, v187
	v_exp_f32_e32 v188, v188
	v_exp_f32_e32 v189, v189
	v_exp_f32_e32 v190, v190
	v_exp_f32_e32 v191, v191
	v_exp_f32_e32 v192, v192
	v_exp_f32_e32 v193, v193
	v_add_f32_e32 v178, 1.0, v178
	v_add_f32_e32 v179, 1.0, v179
	v_add_f32_e32 v180, 1.0, v180
	v_add_f32_e32 v181, 1.0, v181
	v_add_f32_e32 v182, 1.0, v182
	v_add_f32_e32 v183, 1.0, v183
	v_add_f32_e32 v184, 1.0, v184
	v_add_f32_e32 v185, 1.0, v185
	v_add_f32_e32 v186, 1.0, v186
	v_add_f32_e32 v187, 1.0, v187
	v_add_f32_e32 v188, 1.0, v188
	v_add_f32_e32 v189, 1.0, v189
	v_add_f32_e32 v190, 1.0, v190
	v_add_f32_e32 v191, 1.0, v191
	v_add_f32_e32 v192, 1.0, v192
	v_add_f32_e32 v193, 1.0, v193
	v_rcp_f32_e32 v178, v178
	v_rcp_f32_e32 v179, v179
	v_rcp_f32_e32 v180, v180
	v_rcp_f32_e32 v181, v181
	v_rcp_f32_e32 v182, v182
	v_rcp_f32_e32 v183, v183
	v_rcp_f32_e32 v184, v184
	v_rcp_f32_e32 v185, v185
	v_rcp_f32_e32 v186, v186
	v_rcp_f32_e32 v187, v187
	v_rcp_f32_e32 v188, v188
	v_rcp_f32_e32 v189, v189
	v_rcp_f32_e32 v190, v190
	v_rcp_f32_e32 v191, v191
	v_rcp_f32_e32 v192, v192
	v_rcp_f32_e32 v193, v193
	v_mul_f32_e32 v178, v175, v178
	v_mul_f32_e32 v179, v175, v179
	v_mul_f32_e32 v180, v175, v180
	v_mul_f32_e32 v181, v175, v181
	v_mul_f32_e32 v182, v175, v182
	v_mul_f32_e32 v183, v175, v183
	v_mul_f32_e32 v184, v175, v184
	v_mul_f32_e32 v185, v175, v185
	v_exp_f32_e32 v128, v178
	v_exp_f32_e32 v129, v179
	v_exp_f32_e32 v130, v180
	v_exp_f32_e32 v131, v181
	v_exp_f32_e32 v132, v182
	v_exp_f32_e32 v133, v183
	v_exp_f32_e32 v134, v184
	v_exp_f32_e32 v135, v185
	s_nop 0
	v_fma_f32 v194, -v128, v128, 1.0
	v_fma_f32 v195, -v129, v129, 1.0
	v_fma_f32 v196, -v130, v130, 1.0
	v_fma_f32 v197, -v131, v131, 1.0
	v_fma_f32 v198, -v132, v132, 1.0
	v_fma_f32 v199, -v133, v133, 1.0
	v_fma_f32 v200, -v134, v134, 1.0
	v_fma_f32 v201, -v135, v135, 1.0
	v_max_f32_e32 v194, 0, v194
	v_max_f32_e32 v195, 0, v195
	v_max_f32_e32 v196, 0, v196
	v_max_f32_e32 v197, 0, v197
	v_max_f32_e32 v198, 0, v198
	v_max_f32_e32 v199, 0, v199
	v_max_f32_e32 v200, 0, v200
	v_max_f32_e32 v201, 0, v201
	v_sqrt_f32_e32 v194, v194
	v_sqrt_f32_e32 v195, v195
	v_sqrt_f32_e32 v196, v196
	v_sqrt_f32_e32 v197, v197
	v_sqrt_f32_e32 v198, v198
	v_sqrt_f32_e32 v199, v199
	v_sqrt_f32_e32 v200, v200
	v_sqrt_f32_e32 v201, v201
	s_waitcnt lgkmcnt(8)
	v_lshlrev_b32_e32 v144, 16, v144
	v_lshlrev_b32_e32 v145, 16, v145
	v_lshlrev_b32_e32 v146, 16, v146
	v_lshlrev_b32_e32 v147, 16, v147
	v_lshlrev_b32_e32 v148, 16, v148
	v_lshlrev_b32_e32 v149, 16, v149
	v_lshlrev_b32_e32 v150, 16, v150
	v_lshlrev_b32_e32 v151, 16, v151
	v_mul_f32_e32 v194, v194, v186
	v_mul_f32_e32 v195, v195, v187
	v_mul_f32_e32 v196, v196, v188
	v_mul_f32_e32 v197, v197, v189
	v_mul_f32_e32 v198, v198, v190
	v_mul_f32_e32 v199, v199, v191
	v_mul_f32_e32 v200, v200, v192
	v_mul_f32_e32 v201, v201, v193
	v_mul_f32_e32 v144, v194, v144
	v_mul_f32_e32 v145, v195, v145
	v_mul_f32_e32 v146, v196, v146
	v_mul_f32_e32 v147, v197, v147
	v_mul_f32_e32 v148, v198, v148
	v_mul_f32_e32 v149, v199, v149
	v_mul_f32_e32 v150, v200, v150
	v_mul_f32_e32 v151, v201, v151
	v_fma_f32 v178, v80, s53, v173
	v_fma_f32 v179, v81, s53, v173
	v_fma_f32 v180, v82, s53, v173
	v_fma_f32 v181, v83, s53, v173
	v_fma_f32 v182, v88, s53, v173
	v_fma_f32 v183, v89, s53, v173
	v_fma_f32 v184, v90, s53, v173
	v_fma_f32 v185, v91, s53, v173
	v_fma_f32 v186, v84, s53, v174
	v_fma_f32 v187, v85, s53, v174
	v_fma_f32 v188, v86, s53, v174
	v_fma_f32 v189, v87, s53, v174
	v_fma_f32 v190, v92, s53, v174
	v_fma_f32 v191, v93, s53, v174
	v_fma_f32 v192, v94, s53, v174
	v_fma_f32 v193, v95, s53, v174
	v_exp_f32_e32 v178, v178
	v_exp_f32_e32 v179, v179
	v_exp_f32_e32 v180, v180
	v_exp_f32_e32 v181, v181
	v_exp_f32_e32 v182, v182
	v_exp_f32_e32 v183, v183
	v_exp_f32_e32 v184, v184
	v_exp_f32_e32 v185, v185
	v_exp_f32_e32 v186, v186
	v_exp_f32_e32 v187, v187
	v_exp_f32_e32 v188, v188
	v_exp_f32_e32 v189, v189
	v_exp_f32_e32 v190, v190
	v_exp_f32_e32 v191, v191
	v_exp_f32_e32 v192, v192
	v_exp_f32_e32 v193, v193
	v_add_f32_e32 v178, 1.0, v178
	v_add_f32_e32 v179, 1.0, v179
	v_add_f32_e32 v180, 1.0, v180
	v_add_f32_e32 v181, 1.0, v181
	v_add_f32_e32 v182, 1.0, v182
	v_add_f32_e32 v183, 1.0, v183
	v_add_f32_e32 v184, 1.0, v184
	v_add_f32_e32 v185, 1.0, v185
	v_add_f32_e32 v186, 1.0, v186
	v_add_f32_e32 v187, 1.0, v187
	v_add_f32_e32 v188, 1.0, v188
	v_add_f32_e32 v189, 1.0, v189
	v_add_f32_e32 v190, 1.0, v190
	v_add_f32_e32 v191, 1.0, v191
	v_add_f32_e32 v192, 1.0, v192
	v_add_f32_e32 v193, 1.0, v193
	v_rcp_f32_e32 v178, v178
	v_rcp_f32_e32 v179, v179
	v_rcp_f32_e32 v180, v180
	v_rcp_f32_e32 v181, v181
	v_rcp_f32_e32 v182, v182
	v_rcp_f32_e32 v183, v183
	v_rcp_f32_e32 v184, v184
	v_rcp_f32_e32 v185, v185
	v_rcp_f32_e32 v186, v186
	v_rcp_f32_e32 v187, v187
	v_rcp_f32_e32 v188, v188
	v_rcp_f32_e32 v189, v189
	v_rcp_f32_e32 v190, v190
	v_rcp_f32_e32 v191, v191
	v_rcp_f32_e32 v192, v192
	v_rcp_f32_e32 v193, v193
	v_mul_f32_e32 v178, v175, v178
	v_mul_f32_e32 v179, v175, v179
	v_mul_f32_e32 v180, v175, v180
	v_mul_f32_e32 v181, v175, v181
	v_mul_f32_e32 v182, v175, v182
	v_mul_f32_e32 v183, v175, v183
	v_mul_f32_e32 v184, v175, v184
	v_mul_f32_e32 v185, v175, v185
	v_exp_f32_e32 v136, v178
	v_exp_f32_e32 v137, v179
	v_exp_f32_e32 v138, v180
	v_exp_f32_e32 v139, v181
	v_exp_f32_e32 v140, v182
	v_exp_f32_e32 v141, v183
	v_exp_f32_e32 v142, v184
	v_exp_f32_e32 v143, v185
	s_nop 0
	v_fma_f32 v194, -v136, v136, 1.0
	v_fma_f32 v195, -v137, v137, 1.0
	v_fma_f32 v196, -v138, v138, 1.0
	v_fma_f32 v197, -v139, v139, 1.0
	v_fma_f32 v198, -v140, v140, 1.0
	v_fma_f32 v199, -v141, v141, 1.0
	v_fma_f32 v200, -v142, v142, 1.0
	v_fma_f32 v201, -v143, v143, 1.0
	v_max_f32_e32 v194, 0, v194
	v_max_f32_e32 v195, 0, v195
	v_max_f32_e32 v196, 0, v196
	v_max_f32_e32 v197, 0, v197
	v_max_f32_e32 v198, 0, v198
	v_max_f32_e32 v199, 0, v199
	v_max_f32_e32 v200, 0, v200
	v_max_f32_e32 v201, 0, v201
	v_sqrt_f32_e32 v194, v194
	v_sqrt_f32_e32 v195, v195
	v_sqrt_f32_e32 v196, v196
	v_sqrt_f32_e32 v197, v197
	v_sqrt_f32_e32 v198, v198
	v_sqrt_f32_e32 v199, v199
	v_sqrt_f32_e32 v200, v200
	v_sqrt_f32_e32 v201, v201
	s_waitcnt lgkmcnt(0)
	v_lshlrev_b32_e32 v152, 16, v152
	v_lshlrev_b32_e32 v153, 16, v153
	v_lshlrev_b32_e32 v154, 16, v154
	v_lshlrev_b32_e32 v155, 16, v155
	v_lshlrev_b32_e32 v156, 16, v156
	v_lshlrev_b32_e32 v157, 16, v157
	v_lshlrev_b32_e32 v158, 16, v158
	v_lshlrev_b32_e32 v159, 16, v159
	v_mul_f32_e32 v194, v194, v186
	v_mul_f32_e32 v195, v195, v187
	v_mul_f32_e32 v196, v196, v188
	v_mul_f32_e32 v197, v197, v189
	v_mul_f32_e32 v198, v198, v190
	v_mul_f32_e32 v199, v199, v191
	v_mul_f32_e32 v200, v200, v192
	v_mul_f32_e32 v201, v201, v193
	v_mul_f32_e32 v152, v194, v152
	v_mul_f32_e32 v153, v195, v153
	v_mul_f32_e32 v154, v196, v154
	v_mul_f32_e32 v155, v197, v155
	v_mul_f32_e32 v156, v198, v156
	v_mul_f32_e32 v157, v199, v157
	v_mul_f32_e32 v158, v200, v158
	v_mul_f32_e32 v159, v201, v159
	v_fma_f32 v145, v129, v144, v145
	v_fma_f32 v149, v133, v148, v149
	v_fma_f32 v153, v137, v152, v153
	v_fma_f32 v157, v141, v156, v157
	v_mul_f32_e32 v129, v129, v128
	v_mul_f32_e32 v133, v133, v132
	v_mul_f32_e32 v137, v137, v136
	v_mul_f32_e32 v141, v141, v140
	v_fma_f32 v146, v130, v145, v146
	v_fma_f32 v150, v134, v149, v150
	v_fma_f32 v154, v138, v153, v154
	v_fma_f32 v158, v142, v157, v158
	v_mul_f32_e32 v130, v130, v129
	v_mul_f32_e32 v134, v134, v133
	v_mul_f32_e32 v138, v138, v137
	v_mul_f32_e32 v142, v142, v141
	v_fma_f32 v147, v131, v146, v147
	v_fma_f32 v151, v135, v150, v151
	v_fma_f32 v155, v139, v154, v155
	v_fma_f32 v159, v143, v158, v159
	v_mul_f32_e32 v131, v131, v130
	v_mul_f32_e32 v135, v135, v134
	v_mul_f32_e32 v139, v139, v138
	v_mul_f32_e32 v143, v143, v142
	ds_bpermute_b32 v178, v204, v131
	ds_bpermute_b32 v182, v204, v147
	ds_bpermute_b32 v179, v204, v135
	ds_bpermute_b32 v183, v204, v151
	ds_bpermute_b32 v180, v204, v139
	ds_bpermute_b32 v184, v204, v155
	ds_bpermute_b32 v181, v204, v143
	ds_bpermute_b32 v185, v204, v159
	s_waitcnt lgkmcnt(0)
	v_fma_f32 v186, v182, v131, v147
	v_cndmask_b32_e64 v178, 1.0, v178, s[34:35]
	v_fma_f32 v187, v183, v135, v151
	v_cndmask_b32_e64 v179, 1.0, v179, s[34:35]
	v_fma_f32 v188, v184, v139, v155
	v_cndmask_b32_e64 v180, 1.0, v180, s[34:35]
	v_fma_f32 v189, v185, v143, v159
	v_cndmask_b32_e64 v181, 1.0, v181, s[34:35]
	v_cndmask_b32_e64 v223, v147, v186, s[34:35]
	v_mul_f32_e32 v219, v131, v178
	v_cndmask_b32_e64 v224, v151, v187, s[34:35]
	v_mul_f32_e32 v220, v135, v179
	v_cndmask_b32_e64 v225, v155, v188, s[34:35]
	v_mul_f32_e32 v221, v139, v180
	v_cndmask_b32_e64 v226, v159, v189, s[34:35]
	v_mul_f32_e32 v222, v143, v181
	ds_bpermute_b32 v178, v205, v219
	ds_bpermute_b32 v182, v205, v223
	ds_bpermute_b32 v179, v205, v220
	ds_bpermute_b32 v183, v205, v224
	ds_bpermute_b32 v180, v205, v221
	ds_bpermute_b32 v184, v205, v225
	ds_bpermute_b32 v181, v205, v222
	ds_bpermute_b32 v185, v205, v226
	s_waitcnt lgkmcnt(0)
	v_fma_f32 v186, v182, v219, v223
	v_cndmask_b32_e64 v178, 1.0, v178, s[36:37]
	v_fma_f32 v187, v183, v220, v224
	v_cndmask_b32_e64 v179, 1.0, v179, s[36:37]
	v_fma_f32 v188, v184, v221, v225
	v_cndmask_b32_e64 v180, 1.0, v180, s[36:37]
	v_fma_f32 v189, v185, v222, v226
	v_cndmask_b32_e64 v181, 1.0, v181, s[36:37]
	v_cndmask_b32_e64 v223, v223, v186, s[36:37]
	v_mul_f32_e32 v219, v219, v178
	v_cndmask_b32_e64 v224, v224, v187, s[36:37]
	v_mul_f32_e32 v220, v220, v179
	v_cndmask_b32_e64 v225, v225, v188, s[36:37]
	v_mul_f32_e32 v221, v221, v180
	v_cndmask_b32_e64 v226, v226, v189, s[36:37]
	v_mul_f32_e32 v222, v222, v181
	ds_bpermute_b32 v227, v204, v219
	ds_bpermute_b32 v231, v204, v223
	ds_bpermute_b32 v235, v206, v219
	ds_bpermute_b32 v239, v206, v223
	ds_bpermute_b32 v228, v204, v220
	ds_bpermute_b32 v232, v204, v224
	ds_bpermute_b32 v236, v206, v220
	ds_bpermute_b32 v244, v206, v224
	ds_bpermute_b32 v229, v204, v221
	ds_bpermute_b32 v233, v204, v225
	ds_bpermute_b32 v237, v206, v221
	ds_bpermute_b32 v245, v206, v225
	ds_bpermute_b32 v230, v204, v222
	ds_bpermute_b32 v234, v204, v226
	ds_bpermute_b32 v238, v206, v222
	ds_bpermute_b32 v246, v206, v226
	s_waitcnt lgkmcnt(0)
	v_cndmask_b32_e64 v227, 1.0, v227, s[34:35]
	v_cndmask_b32_e64 v231, 0, v231, s[34:35]
	v_cndmask_b32_e64 v228, 1.0, v228, s[34:35]
	v_cndmask_b32_e64 v232, 0, v232, s[34:35]
	v_cndmask_b32_e64 v229, 1.0, v229, s[34:35]
	v_cndmask_b32_e64 v233, 0, v233, s[34:35]
	v_cndmask_b32_e64 v230, 1.0, v230, s[34:35]
	v_cndmask_b32_e64 v234, 0, v234, s[34:35]
	v_mov_b32_e32 v190, v235
	v_mov_b32_e32 v194, v239
	v_mov_b32_e32 v198, v190
	v_mov_b32_e32 v201, v194
	v_fma_f32 v194, v194, v236, v244
	v_mul_f32_e32 v190, v190, v236
	v_mov_b32_e32 v199, v190
	v_mov_b32_e32 v177, v194
	v_fma_f32 v194, v194, v237, v245
	v_mul_f32_e32 v190, v190, v237
	v_mov_b32_e32 v200, v190
	v_mov_b32_e32 v203, v194
	v_fma_f32 v194, v194, v238, v246
	v_mul_f32_e32 v190, v190, v238
	v_mov_b32_e32 v191, v194
	ds_write_b64 v207, v[190:191]
	s_waitcnt lgkmcnt(0)
	s_barrier
	ds_read_b64 v[178:179], v208
	ds_read_b64 v[180:181], v208 offset:512
	s_waitcnt lgkmcnt(0)
	v_fma_f32 v182, v176, v178, v179
	v_cndmask_b32_e64 v183, v176, v182, s[38:39]
	v_fma_f32 v176, v182, v180, v181
	s_add_i32 s13, s13, 1
	s_waitcnt vmcnt(0)
	s_barrier
	s_cmp_eq_u32 s13, 17
	s_cbranch_scc1 .Lmylru_nodma_2
	s_add_i32 s58, s13, 1
	s_cmp_lt_u32 s58, 2
	s_lshl_b32 s50, s58, 7
	s_lshl_b32 s51, s9, 8
	s_add_i32 s51, s51, 0x8000
	s_add_i32 s51, s51, s50
	s_lshl_b32 s59, s9, 11
	s_add_i32 s59, s59, s50
	s_addk_i32 s59, 0xff00
	s_cmp_lt_u32 s58, 2
	s_cselect_b32 s59, s51, s59
	s_lshl_b32 s52, s59, 11
	s_add_u32 s46, s16, s52
	s_addc_u32 s47, s17, 0
	s_lshl_b32 s52, s6, 13
	s_mov_b32 m0, s52
	s_add_i32 s52, s52, 0x400
	global_load_lds_dwordx4 v211, s[46:47]
	s_mov_b32 m0, s52
	s_add_i32 s52, s52, 0x400
	global_load_lds_dwordx4 v212, s[46:47]
	s_mov_b32 m0, s52
	s_add_i32 s52, s52, 0x400
	global_load_lds_dwordx4 v213, s[46:47]
	s_mov_b32 m0, s52
	s_add_i32 s52, s52, 0x400
	global_load_lds_dwordx4 v214, s[46:47]
	s_mov_b32 m0, s52
	s_add_i32 s52, s52, 0x400
	global_load_lds_dwordx4 v215, s[46:47]
	s_mov_b32 m0, s52
	s_add_i32 s52, s52, 0x400
	global_load_lds_dwordx4 v216, s[46:47]
	s_mov_b32 m0, s52
	s_add_i32 s52, s52, 0x400
	global_load_lds_dwordx4 v217, s[46:47]
	s_mov_b32 m0, s52
	s_nop 0
	global_load_lds_dwordx4 v218, s[46:47]
.Lmylru_nodma_2:
	v_or_b32_e32 v163, 0x10000, v162
	ds_read_b128 v[96:99], v163
	ds_read_b128 v[100:103], v163 offset:8192
	ds_read_b128 v[104:107], v163 offset:16384
	ds_read_b128 v[108:111], v163 offset:24576
	v_xor_b32_e32 v164, 0x40, v163
	ds_read_b128 v[112:115], v164
	ds_read_b128 v[116:119], v164 offset:8192
	ds_read_b128 v[120:123], v164 offset:16384
	ds_read_b128 v[124:127], v164 offset:24576
	s_waitcnt lgkmcnt(7)
	v_mfma_f32_16x16x32_bf16 v[64:67], v[96:99], v[0:3], 0
	v_mfma_f32_16x16x32_bf16 v[68:71], v[96:99], v[32:35], 0
	v_xor_b32_e32 v164, 0x80, v163
	ds_read_b128 v[96:99], v164
	s_waitcnt lgkmcnt(7)
	v_mfma_f32_16x16x32_bf16 v[72:75], v[100:103], v[0:3], 0
	v_mfma_f32_16x16x32_bf16 v[76:79], v[100:103], v[32:35], 0
	ds_read_b128 v[100:103], v164 offset:8192
	s_waitcnt lgkmcnt(7)
	v_mfma_f32_16x16x32_bf16 v[80:83], v[104:107], v[0:3], 0
	v_mfma_f32_16x16x32_bf16 v[84:87], v[104:107], v[32:35], 0
	ds_read_b128 v[104:107], v164 offset:16384
	s_waitcnt lgkmcnt(7)
	v_mfma_f32_16x16x32_bf16 v[88:91], v[108:111], v[0:3], 0
	v_mfma_f32_16x16x32_bf16 v[92:95], v[108:111], v[32:35], 0
	ds_read_b128 v[108:111], v164 offset:24576
	s_waitcnt lgkmcnt(7)
	v_mfma_f32_16x16x32_bf16 v[64:67], v[112:115], v[4:7], v[64:67]
	v_mfma_f32_16x16x32_bf16 v[68:71], v[112:115], v[36:39], v[68:71]
	v_xor_b32_e32 v164, 0xc0, v163
	ds_read_b128 v[112:115], v164
	s_waitcnt lgkmcnt(7)
	v_mfma_f32_16x16x32_bf16 v[72:75], v[116:119], v[4:7], v[72:75]
	v_mfma_f32_16x16x32_bf16 v[76:79], v[116:119], v[36:39], v[76:79]
	ds_read_b128 v[116:119], v164 offset:8192
	s_waitcnt lgkmcnt(7)
	v_mfma_f32_16x16x32_bf16 v[80:83], v[120:123], v[4:7], v[80:83]
	v_mfma_f32_16x16x32_bf16 v[84:87], v[120:123], v[36:39], v[84:87]
	ds_read_b128 v[120:123], v164 offset:16384
	s_waitcnt lgkmcnt(7)
	v_mfma_f32_16x16x32_bf16 v[88:91], v[124:127], v[4:7], v[88:91]
	v_mfma_f32_16x16x32_bf16 v[92:95], v[124:127], v[36:39], v[92:95]
	ds_read_b128 v[124:127], v164 offset:24576
	s_waitcnt lgkmcnt(7)
	v_mfma_f32_16x16x32_bf16 v[64:67], v[96:99], v[8:11], v[64:67]
	v_mfma_f32_16x16x32_bf16 v[68:71], v[96:99], v[40:43], v[68:71]
	v_xor_b32_e32 v164, 0x100, v163
	ds_read_b128 v[96:99], v164
	s_waitcnt lgkmcnt(7)
	v_mfma_f32_16x16x32_bf16 v[72:75], v[100:103], v[8:11], v[72:75]
	v_mfma_f32_16x16x32_bf16 v[76:79], v[100:103], v[40:43], v[76:79]
	ds_read_b128 v[100:103], v164 offset:8192
	s_waitcnt lgkmcnt(7)
	v_mfma_f32_16x16x32_bf16 v[80:83], v[104:107], v[8:11], v[80:83]
	v_mfma_f32_16x16x32_bf16 v[84:87], v[104:107], v[40:43], v[84:87]
	ds_read_b128 v[104:107], v164 offset:16384
	s_waitcnt lgkmcnt(7)
	v_mfma_f32_16x16x32_bf16 v[88:91], v[108:111], v[8:11], v[88:91]
	v_mfma_f32_16x16x32_bf16 v[92:95], v[108:111], v[40:43], v[92:95]
	ds_read_b128 v[108:111], v164 offset:24576
	s_waitcnt lgkmcnt(7)
	v_mfma_f32_16x16x32_bf16 v[64:67], v[112:115], v[12:15], v[64:67]
	v_mfma_f32_16x16x32_bf16 v[68:71], v[112:115], v[44:47], v[68:71]
	v_xor_b32_e32 v164, 0x140, v163
	ds_read_b128 v[112:115], v164
	s_waitcnt lgkmcnt(7)
	v_mfma_f32_16x16x32_bf16 v[72:75], v[116:119], v[12:15], v[72:75]
	v_mfma_f32_16x16x32_bf16 v[76:79], v[116:119], v[44:47], v[76:79]
	ds_read_b128 v[116:119], v164 offset:8192
	s_waitcnt lgkmcnt(7)
	v_mfma_f32_16x16x32_bf16 v[80:83], v[120:123], v[12:15], v[80:83]
	v_mfma_f32_16x16x32_bf16 v[84:87], v[120:123], v[44:47], v[84:87]
	ds_read_b128 v[120:123], v164 offset:16384
	s_waitcnt lgkmcnt(7)
	v_mfma_f32_16x16x32_bf16 v[88:91], v[124:127], v[12:15], v[88:91]
	v_mfma_f32_16x16x32_bf16 v[92:95], v[124:127], v[44:47], v[92:95]
	ds_read_b128 v[124:127], v164 offset:24576
	s_waitcnt lgkmcnt(7)
	v_mfma_f32_16x16x32_bf16 v[64:67], v[96:99], v[16:19], v[64:67]
	v_mfma_f32_16x16x32_bf16 v[68:71], v[96:99], v[48:51], v[68:71]
	v_xor_b32_e32 v164, 0x180, v163
	ds_read_b128 v[96:99], v164
	s_waitcnt lgkmcnt(7)
	v_mfma_f32_16x16x32_bf16 v[72:75], v[100:103], v[16:19], v[72:75]
	v_mfma_f32_16x16x32_bf16 v[76:79], v[100:103], v[48:51], v[76:79]
	ds_read_b128 v[100:103], v164 offset:8192
	s_waitcnt lgkmcnt(7)
	v_mfma_f32_16x16x32_bf16 v[80:83], v[104:107], v[16:19], v[80:83]
	v_mfma_f32_16x16x32_bf16 v[84:87], v[104:107], v[48:51], v[84:87]
	ds_read_b128 v[104:107], v164 offset:16384
	s_waitcnt lgkmcnt(7)
	v_mfma_f32_16x16x32_bf16 v[88:91], v[108:111], v[16:19], v[88:91]
	v_mfma_f32_16x16x32_bf16 v[92:95], v[108:111], v[48:51], v[92:95]
	ds_read_b128 v[108:111], v164 offset:24576
	s_waitcnt lgkmcnt(7)
	v_mfma_f32_16x16x32_bf16 v[64:67], v[112:115], v[20:23], v[64:67]
	v_mfma_f32_16x16x32_bf16 v[68:71], v[112:115], v[52:55], v[68:71]
	v_xor_b32_e32 v164, 0x1c0, v163
	ds_read_b128 v[112:115], v164
	s_waitcnt lgkmcnt(7)
	v_mfma_f32_16x16x32_bf16 v[72:75], v[116:119], v[20:23], v[72:75]
	v_mfma_f32_16x16x32_bf16 v[76:79], v[116:119], v[52:55], v[76:79]
	ds_read_b128 v[116:119], v164 offset:8192
	s_waitcnt lgkmcnt(7)
	v_mfma_f32_16x16x32_bf16 v[80:83], v[120:123], v[20:23], v[80:83]
	v_mfma_f32_16x16x32_bf16 v[84:87], v[120:123], v[52:55], v[84:87]
	ds_read_b128 v[120:123], v164 offset:16384
	s_waitcnt lgkmcnt(7)
	v_mfma_f32_16x16x32_bf16 v[88:91], v[124:127], v[20:23], v[88:91]
	v_mfma_f32_16x16x32_bf16 v[92:95], v[124:127], v[52:55], v[92:95]
	ds_read_b128 v[124:127], v164 offset:24576
	s_waitcnt lgkmcnt(7)
	v_mfma_f32_16x16x32_bf16 v[64:67], v[96:99], v[24:27], v[64:67]
	v_mfma_f32_16x16x32_bf16 v[68:71], v[96:99], v[56:59], v[68:71]
	s_waitcnt lgkmcnt(6)
	v_mfma_f32_16x16x32_bf16 v[72:75], v[100:103], v[24:27], v[72:75]
	v_mfma_f32_16x16x32_bf16 v[76:79], v[100:103], v[56:59], v[76:79]
	s_waitcnt lgkmcnt(5)
	v_mfma_f32_16x16x32_bf16 v[80:83], v[104:107], v[24:27], v[80:83]
	v_mfma_f32_16x16x32_bf16 v[84:87], v[104:107], v[56:59], v[84:87]
	s_waitcnt lgkmcnt(4)
	v_mfma_f32_16x16x32_bf16 v[88:91], v[108:111], v[24:27], v[88:91]
	v_mfma_f32_16x16x32_bf16 v[92:95], v[108:111], v[56:59], v[92:95]
	s_waitcnt lgkmcnt(3)
	v_mfma_f32_16x16x32_bf16 v[64:67], v[112:115], v[28:31], v[64:67]
	v_mfma_f32_16x16x32_bf16 v[68:71], v[112:115], v[60:63], v[68:71]
	s_waitcnt lgkmcnt(2)
	v_mfma_f32_16x16x32_bf16 v[72:75], v[116:119], v[28:31], v[72:75]
	v_mfma_f32_16x16x32_bf16 v[76:79], v[116:119], v[60:63], v[76:79]
	s_waitcnt lgkmcnt(1)
	v_mfma_f32_16x16x32_bf16 v[80:83], v[120:123], v[28:31], v[80:83]
	v_mfma_f32_16x16x32_bf16 v[84:87], v[120:123], v[60:63], v[84:87]
	s_waitcnt lgkmcnt(0)
	v_mfma_f32_16x16x32_bf16 v[88:91], v[124:127], v[28:31], v[88:91]
	v_mfma_f32_16x16x32_bf16 v[92:95], v[124:127], v[60:63], v[92:95]
	v_or_b32_e32 v169, 0x10000, v165
	v_or_b32_e32 v170, 0x10000, v166
	v_or_b32_e32 v171, 0x10000, v167
	v_or_b32_e32 v172, 0x10000, v168
	ds_read_u16 v144, v169
	ds_read_u16 v145, v170
	ds_read_u16 v146, v171
	ds_read_u16 v147, v172
	ds_read_u16 v148, v169 offset:8192
	ds_read_u16 v149, v170 offset:8192
	ds_read_u16 v150, v171 offset:8192
	ds_read_u16 v151, v172 offset:8192
	ds_read_u16 v152, v169 offset:16384
	ds_read_u16 v153, v170 offset:16384
	ds_read_u16 v154, v171 offset:16384
	ds_read_u16 v155, v172 offset:16384
	ds_read_u16 v156, v169 offset:24576
	ds_read_u16 v157, v170 offset:24576
	ds_read_u16 v158, v171 offset:24576
	ds_read_u16 v159, v172 offset:24576
	s_nop 7
	v_fma_f32 v178, v64, s53, v173
	v_fma_f32 v179, v65, s53, v173
	v_fma_f32 v180, v66, s53, v173
	v_fma_f32 v181, v67, s53, v173
	v_fma_f32 v182, v72, s53, v173
	v_fma_f32 v183, v73, s53, v173
	v_fma_f32 v184, v74, s53, v173
	v_fma_f32 v185, v75, s53, v173
	v_fma_f32 v186, v68, s53, v174
	v_fma_f32 v187, v69, s53, v174
	v_fma_f32 v188, v70, s53, v174
	v_fma_f32 v189, v71, s53, v174
	v_fma_f32 v190, v76, s53, v174
	v_fma_f32 v191, v77, s53, v174
	v_fma_f32 v192, v78, s53, v174
	v_fma_f32 v193, v79, s53, v174
	v_exp_f32_e32 v178, v178
	v_exp_f32_e32 v179, v179
	v_exp_f32_e32 v180, v180
	v_exp_f32_e32 v181, v181
	v_exp_f32_e32 v182, v182
	v_exp_f32_e32 v183, v183
	v_exp_f32_e32 v184, v184
	v_exp_f32_e32 v185, v185
	v_exp_f32_e32 v186, v186
	v_exp_f32_e32 v187, v187
	v_exp_f32_e32 v188, v188
	v_exp_f32_e32 v189, v189
	v_exp_f32_e32 v190, v190
	v_exp_f32_e32 v191, v191
	v_exp_f32_e32 v192, v192
	v_exp_f32_e32 v193, v193
	v_add_f32_e32 v178, 1.0, v178
	v_add_f32_e32 v179, 1.0, v179
	v_add_f32_e32 v180, 1.0, v180
	v_add_f32_e32 v181, 1.0, v181
	v_add_f32_e32 v182, 1.0, v182
	v_add_f32_e32 v183, 1.0, v183
	v_add_f32_e32 v184, 1.0, v184
	v_add_f32_e32 v185, 1.0, v185
	v_add_f32_e32 v186, 1.0, v186
	v_add_f32_e32 v187, 1.0, v187
	v_add_f32_e32 v188, 1.0, v188
	v_add_f32_e32 v189, 1.0, v189
	v_add_f32_e32 v190, 1.0, v190
	v_add_f32_e32 v191, 1.0, v191
	v_add_f32_e32 v192, 1.0, v192
	v_add_f32_e32 v193, 1.0, v193
	v_rcp_f32_e32 v178, v178
	v_rcp_f32_e32 v179, v179
	v_rcp_f32_e32 v180, v180
	v_rcp_f32_e32 v181, v181
	v_rcp_f32_e32 v182, v182
	v_rcp_f32_e32 v183, v183
	v_rcp_f32_e32 v184, v184
	v_rcp_f32_e32 v185, v185
	v_rcp_f32_e32 v186, v186
	v_rcp_f32_e32 v187, v187
	v_rcp_f32_e32 v188, v188
	v_rcp_f32_e32 v189, v189
	v_rcp_f32_e32 v190, v190
	v_rcp_f32_e32 v191, v191
	v_rcp_f32_e32 v192, v192
	v_rcp_f32_e32 v193, v193
	v_mul_f32_e32 v178, v175, v178
	v_mul_f32_e32 v179, v175, v179
	v_mul_f32_e32 v180, v175, v180
	v_mul_f32_e32 v181, v175, v181
	v_mul_f32_e32 v182, v175, v182
	v_mul_f32_e32 v183, v175, v183
	v_mul_f32_e32 v184, v175, v184
	v_mul_f32_e32 v185, v175, v185
	v_exp_f32_e32 v128, v178
	v_exp_f32_e32 v129, v179
	v_exp_f32_e32 v130, v180
	v_exp_f32_e32 v131, v181
	v_exp_f32_e32 v132, v182
	v_exp_f32_e32 v133, v183
	v_exp_f32_e32 v134, v184
	v_exp_f32_e32 v135, v185
	s_nop 0
	v_fma_f32 v194, -v128, v128, 1.0
	v_fma_f32 v195, -v129, v129, 1.0
	v_fma_f32 v196, -v130, v130, 1.0
	v_fma_f32 v197, -v131, v131, 1.0
	v_fma_f32 v198, -v132, v132, 1.0
	v_fma_f32 v199, -v133, v133, 1.0
	v_fma_f32 v200, -v134, v134, 1.0
	v_fma_f32 v201, -v135, v135, 1.0
	v_max_f32_e32 v194, 0, v194
	v_max_f32_e32 v195, 0, v195
	v_max_f32_e32 v196, 0, v196
	v_max_f32_e32 v197, 0, v197
	v_max_f32_e32 v198, 0, v198
	v_max_f32_e32 v199, 0, v199
	v_max_f32_e32 v200, 0, v200
	v_max_f32_e32 v201, 0, v201
	v_sqrt_f32_e32 v194, v194
	v_sqrt_f32_e32 v195, v195
	v_sqrt_f32_e32 v196, v196
	v_sqrt_f32_e32 v197, v197
	v_sqrt_f32_e32 v198, v198
	v_sqrt_f32_e32 v199, v199
	v_sqrt_f32_e32 v200, v200
	v_sqrt_f32_e32 v201, v201
	s_waitcnt lgkmcnt(8)
	v_lshlrev_b32_e32 v144, 16, v144
	v_lshlrev_b32_e32 v145, 16, v145
	v_lshlrev_b32_e32 v146, 16, v146
	v_lshlrev_b32_e32 v147, 16, v147
	v_lshlrev_b32_e32 v148, 16, v148
	v_lshlrev_b32_e32 v149, 16, v149
	v_lshlrev_b32_e32 v150, 16, v150
	v_lshlrev_b32_e32 v151, 16, v151
	v_mul_f32_e32 v194, v194, v186
	v_mul_f32_e32 v195, v195, v187
	v_mul_f32_e32 v196, v196, v188
	v_mul_f32_e32 v197, v197, v189
	v_mul_f32_e32 v198, v198, v190
	v_mul_f32_e32 v199, v199, v191
	v_mul_f32_e32 v200, v200, v192
	v_mul_f32_e32 v201, v201, v193
	v_mul_f32_e32 v144, v194, v144
	v_mul_f32_e32 v145, v195, v145
	v_mul_f32_e32 v146, v196, v146
	v_mul_f32_e32 v147, v197, v147
	v_mul_f32_e32 v148, v198, v148
	v_mul_f32_e32 v149, v199, v149
	v_mul_f32_e32 v150, v200, v150
	v_mul_f32_e32 v151, v201, v151
	v_fma_f32 v178, v80, s53, v173
	v_fma_f32 v179, v81, s53, v173
	v_fma_f32 v180, v82, s53, v173
	v_fma_f32 v181, v83, s53, v173
	v_fma_f32 v182, v88, s53, v173
	v_fma_f32 v183, v89, s53, v173
	v_fma_f32 v184, v90, s53, v173
	v_fma_f32 v185, v91, s53, v173
	v_fma_f32 v186, v84, s53, v174
	v_fma_f32 v187, v85, s53, v174
	v_fma_f32 v188, v86, s53, v174
	v_fma_f32 v189, v87, s53, v174
	v_fma_f32 v190, v92, s53, v174
	v_fma_f32 v191, v93, s53, v174
	v_fma_f32 v192, v94, s53, v174
	v_fma_f32 v193, v95, s53, v174
	v_exp_f32_e32 v178, v178
	v_exp_f32_e32 v179, v179
	v_exp_f32_e32 v180, v180
	v_exp_f32_e32 v181, v181
	v_exp_f32_e32 v182, v182
	v_exp_f32_e32 v183, v183
	v_exp_f32_e32 v184, v184
	v_exp_f32_e32 v185, v185
	v_exp_f32_e32 v186, v186
	v_exp_f32_e32 v187, v187
	v_exp_f32_e32 v188, v188
	v_exp_f32_e32 v189, v189
	v_exp_f32_e32 v190, v190
	v_exp_f32_e32 v191, v191
	v_exp_f32_e32 v192, v192
	v_exp_f32_e32 v193, v193
	v_add_f32_e32 v178, 1.0, v178
	v_add_f32_e32 v179, 1.0, v179
	v_add_f32_e32 v180, 1.0, v180
	v_add_f32_e32 v181, 1.0, v181
	v_add_f32_e32 v182, 1.0, v182
	v_add_f32_e32 v183, 1.0, v183
	v_add_f32_e32 v184, 1.0, v184
	v_add_f32_e32 v185, 1.0, v185
	v_add_f32_e32 v186, 1.0, v186
	v_add_f32_e32 v187, 1.0, v187
	v_add_f32_e32 v188, 1.0, v188
	v_add_f32_e32 v189, 1.0, v189
	v_add_f32_e32 v190, 1.0, v190
	v_add_f32_e32 v191, 1.0, v191
	v_add_f32_e32 v192, 1.0, v192
	v_add_f32_e32 v193, 1.0, v193
	v_rcp_f32_e32 v178, v178
	v_rcp_f32_e32 v179, v179
	v_rcp_f32_e32 v180, v180
	v_rcp_f32_e32 v181, v181
	v_rcp_f32_e32 v182, v182
	v_rcp_f32_e32 v183, v183
	v_rcp_f32_e32 v184, v184
	v_rcp_f32_e32 v185, v185
	v_rcp_f32_e32 v186, v186
	v_rcp_f32_e32 v187, v187
	v_rcp_f32_e32 v188, v188
	v_rcp_f32_e32 v189, v189
	v_rcp_f32_e32 v190, v190
	v_rcp_f32_e32 v191, v191
	v_rcp_f32_e32 v192, v192
	v_rcp_f32_e32 v193, v193
	v_mul_f32_e32 v178, v175, v178
	v_mul_f32_e32 v179, v175, v179
	v_mul_f32_e32 v180, v175, v180
	v_mul_f32_e32 v181, v175, v181
	v_mul_f32_e32 v182, v175, v182
	v_mul_f32_e32 v183, v175, v183
	v_mul_f32_e32 v184, v175, v184
	v_mul_f32_e32 v185, v175, v185
	v_exp_f32_e32 v136, v178
	v_exp_f32_e32 v137, v179
	v_exp_f32_e32 v138, v180
	v_exp_f32_e32 v139, v181
	v_exp_f32_e32 v140, v182
	v_exp_f32_e32 v141, v183
	v_exp_f32_e32 v142, v184
	v_exp_f32_e32 v143, v185
	s_nop 0
	v_fma_f32 v194, -v136, v136, 1.0
	v_fma_f32 v195, -v137, v137, 1.0
	v_fma_f32 v196, -v138, v138, 1.0
	v_fma_f32 v197, -v139, v139, 1.0
	v_fma_f32 v198, -v140, v140, 1.0
	v_fma_f32 v199, -v141, v141, 1.0
	v_fma_f32 v200, -v142, v142, 1.0
	v_fma_f32 v201, -v143, v143, 1.0
	v_max_f32_e32 v194, 0, v194
	v_max_f32_e32 v195, 0, v195
	v_max_f32_e32 v196, 0, v196
	v_max_f32_e32 v197, 0, v197
	v_max_f32_e32 v198, 0, v198
	v_max_f32_e32 v199, 0, v199
	v_max_f32_e32 v200, 0, v200
	v_max_f32_e32 v201, 0, v201
	v_sqrt_f32_e32 v194, v194
	v_sqrt_f32_e32 v195, v195
	v_sqrt_f32_e32 v196, v196
	v_sqrt_f32_e32 v197, v197
	v_sqrt_f32_e32 v198, v198
	v_sqrt_f32_e32 v199, v199
	v_sqrt_f32_e32 v200, v200
	v_sqrt_f32_e32 v201, v201
	s_waitcnt lgkmcnt(0)
	v_lshlrev_b32_e32 v152, 16, v152
	v_lshlrev_b32_e32 v153, 16, v153
	v_lshlrev_b32_e32 v154, 16, v154
	v_lshlrev_b32_e32 v155, 16, v155
	v_lshlrev_b32_e32 v156, 16, v156
	v_lshlrev_b32_e32 v157, 16, v157
	v_lshlrev_b32_e32 v158, 16, v158
	v_lshlrev_b32_e32 v159, 16, v159
	v_mul_f32_e32 v194, v194, v186
	v_mul_f32_e32 v195, v195, v187
	v_mul_f32_e32 v196, v196, v188
	v_mul_f32_e32 v197, v197, v189
	v_mul_f32_e32 v198, v198, v190
	v_mul_f32_e32 v199, v199, v191
	v_mul_f32_e32 v200, v200, v192
	v_mul_f32_e32 v201, v201, v193
	v_mul_f32_e32 v152, v194, v152
	v_mul_f32_e32 v153, v195, v153
	v_mul_f32_e32 v154, v196, v154
	v_mul_f32_e32 v155, v197, v155
	v_mul_f32_e32 v156, v198, v156
	v_mul_f32_e32 v157, v199, v157
	v_mul_f32_e32 v158, v200, v158
	v_mul_f32_e32 v159, v201, v159
	v_fma_f32 v145, v129, v144, v145
	v_fma_f32 v149, v133, v148, v149
	v_fma_f32 v153, v137, v152, v153
	v_fma_f32 v157, v141, v156, v157
	v_mul_f32_e32 v129, v129, v128
	v_mul_f32_e32 v133, v133, v132
	v_mul_f32_e32 v137, v137, v136
	v_mul_f32_e32 v141, v141, v140
	v_fma_f32 v146, v130, v145, v146
	v_fma_f32 v150, v134, v149, v150
	v_fma_f32 v154, v138, v153, v154
	v_fma_f32 v158, v142, v157, v158
	v_mul_f32_e32 v130, v130, v129
	v_mul_f32_e32 v134, v134, v133
	v_mul_f32_e32 v138, v138, v137
	v_mul_f32_e32 v142, v142, v141
	v_fma_f32 v147, v131, v146, v147
	v_fma_f32 v151, v135, v150, v151
	v_fma_f32 v155, v139, v154, v155
	v_fma_f32 v159, v143, v158, v159
	v_mul_f32_e32 v131, v131, v130
	v_mul_f32_e32 v135, v135, v134
	v_mul_f32_e32 v139, v139, v138
	v_mul_f32_e32 v143, v143, v142
	ds_bpermute_b32 v178, v204, v131
	ds_bpermute_b32 v182, v204, v147
	ds_bpermute_b32 v179, v204, v135
	ds_bpermute_b32 v183, v204, v151
	ds_bpermute_b32 v180, v204, v139
	ds_bpermute_b32 v184, v204, v155
	ds_bpermute_b32 v181, v204, v143
	ds_bpermute_b32 v185, v204, v159
	s_waitcnt lgkmcnt(0)
	v_fma_f32 v186, v182, v131, v147
	v_cndmask_b32_e64 v178, 1.0, v178, s[34:35]
	v_fma_f32 v187, v183, v135, v151
	v_cndmask_b32_e64 v179, 1.0, v179, s[34:35]
	v_fma_f32 v188, v184, v139, v155
	v_cndmask_b32_e64 v180, 1.0, v180, s[34:35]
	v_fma_f32 v189, v185, v143, v159
	v_cndmask_b32_e64 v181, 1.0, v181, s[34:35]
	v_cndmask_b32_e64 v223, v147, v186, s[34:35]
	v_mul_f32_e32 v219, v131, v178
	v_cndmask_b32_e64 v224, v151, v187, s[34:35]
	v_mul_f32_e32 v220, v135, v179
	v_cndmask_b32_e64 v225, v155, v188, s[34:35]
	v_mul_f32_e32 v221, v139, v180
	v_cndmask_b32_e64 v226, v159, v189, s[34:35]
	v_mul_f32_e32 v222, v143, v181
	ds_bpermute_b32 v178, v205, v219
	ds_bpermute_b32 v182, v205, v223
	ds_bpermute_b32 v179, v205, v220
	ds_bpermute_b32 v183, v205, v224
	ds_bpermute_b32 v180, v205, v221
	ds_bpermute_b32 v184, v205, v225
	ds_bpermute_b32 v181, v205, v222
	ds_bpermute_b32 v185, v205, v226
	s_waitcnt lgkmcnt(0)
	v_fma_f32 v186, v182, v219, v223
	v_cndmask_b32_e64 v178, 1.0, v178, s[36:37]
	v_fma_f32 v187, v183, v220, v224
	v_cndmask_b32_e64 v179, 1.0, v179, s[36:37]
	v_fma_f32 v188, v184, v221, v225
	v_cndmask_b32_e64 v180, 1.0, v180, s[36:37]
	v_fma_f32 v189, v185, v222, v226
	v_cndmask_b32_e64 v181, 1.0, v181, s[36:37]
	v_cndmask_b32_e64 v223, v223, v186, s[36:37]
	v_mul_f32_e32 v219, v219, v178
	v_cndmask_b32_e64 v224, v224, v187, s[36:37]
	v_mul_f32_e32 v220, v220, v179
	v_cndmask_b32_e64 v225, v225, v188, s[36:37]
	v_mul_f32_e32 v221, v221, v180
	v_cndmask_b32_e64 v226, v226, v189, s[36:37]
	v_mul_f32_e32 v222, v222, v181
	ds_bpermute_b32 v227, v204, v219
	ds_bpermute_b32 v231, v204, v223
	ds_bpermute_b32 v235, v206, v219
	ds_bpermute_b32 v239, v206, v223
	ds_bpermute_b32 v228, v204, v220
	ds_bpermute_b32 v232, v204, v224
	ds_bpermute_b32 v236, v206, v220
	ds_bpermute_b32 v244, v206, v224
	ds_bpermute_b32 v229, v204, v221
	ds_bpermute_b32 v233, v204, v225
	ds_bpermute_b32 v237, v206, v221
	ds_bpermute_b32 v245, v206, v225
	ds_bpermute_b32 v230, v204, v222
	ds_bpermute_b32 v234, v204, v226
	ds_bpermute_b32 v238, v206, v222
	ds_bpermute_b32 v246, v206, v226
	s_waitcnt lgkmcnt(0)
	v_cndmask_b32_e64 v227, 1.0, v227, s[34:35]
	v_cndmask_b32_e64 v231, 0, v231, s[34:35]
	v_cndmask_b32_e64 v228, 1.0, v228, s[34:35]
	v_cndmask_b32_e64 v232, 0, v232, s[34:35]
	v_cndmask_b32_e64 v229, 1.0, v229, s[34:35]
	v_cndmask_b32_e64 v233, 0, v233, s[34:35]
	v_cndmask_b32_e64 v230, 1.0, v230, s[34:35]
	v_cndmask_b32_e64 v234, 0, v234, s[34:35]
	v_mov_b32_e32 v190, v235
	v_mov_b32_e32 v194, v239
	v_mov_b32_e32 v198, v190
	v_mov_b32_e32 v201, v194
	v_fma_f32 v194, v194, v236, v244
	v_mul_f32_e32 v190, v190, v236
	v_mov_b32_e32 v199, v190
	v_mov_b32_e32 v177, v194
	v_fma_f32 v194, v194, v237, v245
	v_mul_f32_e32 v190, v190, v237
	v_mov_b32_e32 v200, v190
	v_mov_b32_e32 v203, v194
	v_fma_f32 v194, v194, v238, v246
	v_mul_f32_e32 v190, v190, v238
	v_mov_b32_e32 v191, v194
	ds_write_b64 v207, v[190:191] offset:1024
	s_waitcnt lgkmcnt(0)
	s_barrier
	ds_read_b64 v[178:179], v208 offset:1024
	ds_read_b64 v[180:181], v208 offset:1536
	s_waitcnt lgkmcnt(0)
	v_fma_f32 v182, v176, v178, v179
	v_cndmask_b32_e64 v183, v176, v182, s[38:39]
	v_fma_f32 v176, v182, v180, v181
	s_add_i32 s13, s13, 1
	s_mov_b32 s60, 8
.Lmylru_loop_0:
	s_cmp_eq_u32 s13, 2
	s_cbranch_scc1 .Lmylru_t0_3
	s_waitcnt vmcnt(8)
	s_branch .Lmylru_t1_3

.Lmylru_t1_3:
	s_barrier
	s_add_i32 s54, s13, -2
	s_lshl_b32 s55, s54, 14
	s_lshl_b32 s56, s6, 11
	s_add_i32 s55, s55, s56
	s_add_u32 s44, s22, s55
	s_addc_u32 s45, s23, 0
	s_cmp_eq_u32 s13, 17
	s_cbranch_scc1 .Lmylru_nodma_3
	s_add_i32 s58, s13, 1
	s_cmp_lt_u32 s58, 2
	s_lshl_b32 s50, s58, 7
	s_lshl_b32 s51, s9, 8
	s_add_i32 s51, s51, 0x8000
	s_add_i32 s51, s51, s50
	s_lshl_b32 s59, s9, 11
	s_add_i32 s59, s59, s50
	s_addk_i32 s59, 0xff00
	s_cmp_lt_u32 s58, 2
	s_cselect_b32 s59, s51, s59
	s_lshl_b32 s52, s59, 11
	s_add_u32 s46, s16, s52
	s_addc_u32 s47, s17, 0
	s_lshl_b32 s52, s6, 13
	s_add_i32 s52, s52, 0x10000
	s_mov_b32 m0, s52
	s_add_i32 s52, s52, 0x400
	global_load_lds_dwordx4 v211, s[46:47]
	s_mov_b32 m0, s52
	s_add_i32 s52, s52, 0x400
	global_load_lds_dwordx4 v212, s[46:47]
	s_mov_b32 m0, s52
	s_add_i32 s52, s52, 0x400
	global_load_lds_dwordx4 v213, s[46:47]
	s_mov_b32 m0, s52
	s_add_i32 s52, s52, 0x400
	global_load_lds_dwordx4 v214, s[46:47]
	s_mov_b32 m0, s52
	s_add_i32 s52, s52, 0x400
	global_load_lds_dwordx4 v215, s[46:47]
	s_mov_b32 m0, s52
	s_add_i32 s52, s52, 0x400
	global_load_lds_dwordx4 v216, s[46:47]
	s_mov_b32 m0, s52
	s_add_i32 s52, s52, 0x400
	global_load_lds_dwordx4 v217, s[46:47]
	s_mov_b32 m0, s52
	s_nop 0
	global_load_lds_dwordx4 v218, s[46:47]
.Lmylru_nodma_3:
	v_mov_b32_e32 v163, v162
	ds_read_b128 v[96:99], v163
	ds_read_b128 v[100:103], v163 offset:8192
	ds_read_b128 v[104:107], v163 offset:16384
	ds_read_b128 v[108:111], v163 offset:24576
	v_xor_b32_e32 v164, 0x40, v163
	ds_read_b128 v[112:115], v164
	ds_read_b128 v[116:119], v164 offset:8192
	ds_read_b128 v[120:123], v164 offset:16384
	ds_read_b128 v[124:127], v164 offset:24576
	s_waitcnt lgkmcnt(7)
	v_mfma_f32_16x16x32_bf16 v[64:67], v[96:99], v[0:3], 0
	v_mfma_f32_16x16x32_bf16 v[68:71], v[96:99], v[32:35], 0
	v_xor_b32_e32 v164, 0x80, v163
	ds_read_b128 v[96:99], v164
	s_waitcnt lgkmcnt(7)
	v_mfma_f32_16x16x32_bf16 v[72:75], v[100:103], v[0:3], 0
	v_mfma_f32_16x16x32_bf16 v[76:79], v[100:103], v[32:35], 0
	ds_read_b128 v[100:103], v164 offset:8192
	s_waitcnt lgkmcnt(7)
	v_mfma_f32_16x16x32_bf16 v[80:83], v[104:107], v[0:3], 0
	v_mfma_f32_16x16x32_bf16 v[84:87], v[104:107], v[32:35], 0
	ds_read_b128 v[104:107], v164 offset:16384
	s_waitcnt lgkmcnt(7)
	v_mfma_f32_16x16x32_bf16 v[88:91], v[108:111], v[0:3], 0
	v_mfma_f32_16x16x32_bf16 v[92:95], v[108:111], v[32:35], 0
	ds_read_b128 v[108:111], v164 offset:24576
	s_waitcnt lgkmcnt(7)
	v_mfma_f32_16x16x32_bf16 v[64:67], v[112:115], v[4:7], v[64:67]
	v_mfma_f32_16x16x32_bf16 v[68:71], v[112:115], v[36:39], v[68:71]
	v_xor_b32_e32 v164, 0xc0, v163
	ds_read_b128 v[112:115], v164
	s_waitcnt lgkmcnt(7)
	v_mfma_f32_16x16x32_bf16 v[72:75], v[116:119], v[4:7], v[72:75]
	v_mfma_f32_16x16x32_bf16 v[76:79], v[116:119], v[36:39], v[76:79]
	ds_read_b128 v[116:119], v164 offset:8192
	s_waitcnt lgkmcnt(7)
	v_mfma_f32_16x16x32_bf16 v[80:83], v[120:123], v[4:7], v[80:83]
	v_mfma_f32_16x16x32_bf16 v[84:87], v[120:123], v[36:39], v[84:87]
	ds_read_b128 v[120:123], v164 offset:16384
	s_waitcnt lgkmcnt(7)
	v_mfma_f32_16x16x32_bf16 v[88:91], v[124:127], v[4:7], v[88:91]
	v_mfma_f32_16x16x32_bf16 v[92:95], v[124:127], v[36:39], v[92:95]
	ds_read_b128 v[124:127], v164 offset:24576
	s_waitcnt lgkmcnt(7)
	v_mfma_f32_16x16x32_bf16 v[64:67], v[96:99], v[8:11], v[64:67]
	v_mfma_f32_16x16x32_bf16 v[68:71], v[96:99], v[40:43], v[68:71]
	v_xor_b32_e32 v164, 0x100, v163
	ds_read_b128 v[96:99], v164
	s_waitcnt lgkmcnt(7)
	v_mfma_f32_16x16x32_bf16 v[72:75], v[100:103], v[8:11], v[72:75]
	v_mfma_f32_16x16x32_bf16 v[76:79], v[100:103], v[40:43], v[76:79]
	ds_read_b128 v[100:103], v164 offset:8192
	s_waitcnt lgkmcnt(7)
	v_mfma_f32_16x16x32_bf16 v[80:83], v[104:107], v[8:11], v[80:83]
	v_mfma_f32_16x16x32_bf16 v[84:87], v[104:107], v[40:43], v[84:87]
	ds_read_b128 v[104:107], v164 offset:16384
	s_waitcnt lgkmcnt(7)
	v_mfma_f32_16x16x32_bf16 v[88:91], v[108:111], v[8:11], v[88:91]
	v_mfma_f32_16x16x32_bf16 v[92:95], v[108:111], v[40:43], v[92:95]
	ds_read_b128 v[108:111], v164 offset:24576
	s_waitcnt lgkmcnt(7)
	v_mfma_f32_16x16x32_bf16 v[64:67], v[112:115], v[12:15], v[64:67]
	v_mfma_f32_16x16x32_bf16 v[68:71], v[112:115], v[44:47], v[68:71]
	v_xor_b32_e32 v164, 0x140, v163
	ds_read_b128 v[112:115], v164
	s_waitcnt lgkmcnt(7)
	v_mfma_f32_16x16x32_bf16 v[72:75], v[116:119], v[12:15], v[72:75]
	v_mfma_f32_16x16x32_bf16 v[76:79], v[116:119], v[44:47], v[76:79]
	ds_read_b128 v[116:119], v164 offset:8192
	s_waitcnt lgkmcnt(7)
	v_mfma_f32_16x16x32_bf16 v[80:83], v[120:123], v[12:15], v[80:83]
	v_mfma_f32_16x16x32_bf16 v[84:87], v[120:123], v[44:47], v[84:87]
	ds_read_b128 v[120:123], v164 offset:16384
	s_waitcnt lgkmcnt(7)
	v_mfma_f32_16x16x32_bf16 v[88:91], v[124:127], v[12:15], v[88:91]
	v_mfma_f32_16x16x32_bf16 v[92:95], v[124:127], v[44:47], v[92:95]
	ds_read_b128 v[124:127], v164 offset:24576
	s_waitcnt lgkmcnt(7)
	v_mfma_f32_16x16x32_bf16 v[64:67], v[96:99], v[16:19], v[64:67]
	v_mfma_f32_16x16x32_bf16 v[68:71], v[96:99], v[48:51], v[68:71]
	v_xor_b32_e32 v164, 0x180, v163
	ds_read_b128 v[96:99], v164
	s_waitcnt lgkmcnt(7)
	v_mfma_f32_16x16x32_bf16 v[72:75], v[100:103], v[16:19], v[72:75]
	v_mfma_f32_16x16x32_bf16 v[76:79], v[100:103], v[48:51], v[76:79]
	ds_read_b128 v[100:103], v164 offset:8192
	s_waitcnt lgkmcnt(7)
	v_mfma_f32_16x16x32_bf16 v[80:83], v[104:107], v[16:19], v[80:83]
	v_mfma_f32_16x16x32_bf16 v[84:87], v[104:107], v[48:51], v[84:87]
	ds_read_b128 v[104:107], v164 offset:16384
	s_waitcnt lgkmcnt(7)
	v_mfma_f32_16x16x32_bf16 v[88:91], v[108:111], v[16:19], v[88:91]
	v_mfma_f32_16x16x32_bf16 v[92:95], v[108:111], v[48:51], v[92:95]
	ds_read_b128 v[108:111], v164 offset:24576
	s_waitcnt lgkmcnt(7)
	v_mfma_f32_16x16x32_bf16 v[64:67], v[112:115], v[20:23], v[64:67]
	v_mfma_f32_16x16x32_bf16 v[68:71], v[112:115], v[52:55], v[68:71]
	v_xor_b32_e32 v164, 0x1c0, v163
	ds_read_b128 v[112:115], v164
	s_waitcnt lgkmcnt(7)
	v_mfma_f32_16x16x32_bf16 v[72:75], v[116:119], v[20:23], v[72:75]
	v_mfma_f32_16x16x32_bf16 v[76:79], v[116:119], v[52:55], v[76:79]
	ds_read_b128 v[116:119], v164 offset:8192
	s_waitcnt lgkmcnt(7)
	v_mfma_f32_16x16x32_bf16 v[80:83], v[120:123], v[20:23], v[80:83]
	v_mfma_f32_16x16x32_bf16 v[84:87], v[120:123], v[52:55], v[84:87]
	ds_read_b128 v[120:123], v164 offset:16384
	s_waitcnt lgkmcnt(7)
	v_mfma_f32_16x16x32_bf16 v[88:91], v[124:127], v[20:23], v[88:91]
	v_mfma_f32_16x16x32_bf16 v[92:95], v[124:127], v[52:55], v[92:95]
	ds_read_b128 v[124:127], v164 offset:24576
	s_waitcnt lgkmcnt(7)
	v_mfma_f32_16x16x32_bf16 v[64:67], v[96:99], v[24:27], v[64:67]
	v_mfma_f32_16x16x32_bf16 v[68:71], v[96:99], v[56:59], v[68:71]
	s_waitcnt lgkmcnt(6)
	v_mfma_f32_16x16x32_bf16 v[72:75], v[100:103], v[24:27], v[72:75]
	v_mfma_f32_16x16x32_bf16 v[76:79], v[100:103], v[56:59], v[76:79]
	s_waitcnt lgkmcnt(5)
	v_mfma_f32_16x16x32_bf16 v[80:83], v[104:107], v[24:27], v[80:83]
	v_mfma_f32_16x16x32_bf16 v[84:87], v[104:107], v[56:59], v[84:87]
	s_waitcnt lgkmcnt(4)
	v_mfma_f32_16x16x32_bf16 v[88:91], v[108:111], v[24:27], v[88:91]
	v_mfma_f32_16x16x32_bf16 v[92:95], v[108:111], v[56:59], v[92:95]
	s_waitcnt lgkmcnt(3)
	v_mfma_f32_16x16x32_bf16 v[64:67], v[112:115], v[28:31], v[64:67]
	v_mfma_f32_16x16x32_bf16 v[68:71], v[112:115], v[60:63], v[68:71]
	s_waitcnt lgkmcnt(2)
	v_mfma_f32_16x16x32_bf16 v[72:75], v[116:119], v[28:31], v[72:75]
	v_mfma_f32_16x16x32_bf16 v[76:79], v[116:119], v[60:63], v[76:79]
	s_waitcnt lgkmcnt(1)
	v_mfma_f32_16x16x32_bf16 v[80:83], v[120:123], v[28:31], v[80:83]
	v_mfma_f32_16x16x32_bf16 v[84:87], v[120:123], v[60:63], v[84:87]
	s_waitcnt lgkmcnt(0)
	v_mfma_f32_16x16x32_bf16 v[88:91], v[124:127], v[28:31], v[88:91]
	v_mfma_f32_16x16x32_bf16 v[92:95], v[124:127], v[60:63], v[92:95]
	v_mov_b32_e32 v169, v165
	v_mov_b32_e32 v170, v166
	v_mov_b32_e32 v171, v167
	v_mov_b32_e32 v172, v168
	ds_read_u16 v144, v169
	ds_read_u16 v145, v170
	ds_read_u16 v146, v171
	ds_read_u16 v147, v172
	ds_read_u16 v148, v169 offset:8192
	ds_read_u16 v149, v170 offset:8192
	ds_read_u16 v150, v171 offset:8192
	ds_read_u16 v151, v172 offset:8192
	ds_read_u16 v152, v169 offset:16384
	ds_read_u16 v153, v170 offset:16384
	ds_read_u16 v154, v171 offset:16384
	ds_read_u16 v155, v172 offset:16384
	ds_read_u16 v156, v169 offset:24576
	ds_read_u16 v157, v170 offset:24576
	ds_read_u16 v158, v171 offset:24576
	ds_read_u16 v159, v172 offset:24576
	s_nop 7
	v_fma_f32 v178, v64, s53, v173
	v_fma_f32 v179, v65, s53, v173
	v_fma_f32 v180, v66, s53, v173
	v_fma_f32 v181, v67, s53, v173
	v_fma_f32 v182, v72, s53, v173
	v_fma_f32 v183, v73, s53, v173
	v_fma_f32 v184, v74, s53, v173
	v_fma_f32 v185, v75, s53, v173
	v_fma_f32 v186, v68, s53, v174
	v_fma_f32 v187, v69, s53, v174
	v_fma_f32 v188, v70, s53, v174
	v_fma_f32 v189, v71, s53, v174
	v_fma_f32 v190, v76, s53, v174
	v_fma_f32 v191, v77, s53, v174
	v_fma_f32 v192, v78, s53, v174
	v_fma_f32 v193, v79, s53, v174
	v_exp_f32_e32 v178, v178
	v_exp_f32_e32 v179, v179
	v_exp_f32_e32 v180, v180
	v_exp_f32_e32 v181, v181
	v_exp_f32_e32 v182, v182
	v_exp_f32_e32 v183, v183
	v_exp_f32_e32 v184, v184
	v_exp_f32_e32 v185, v185
	v_exp_f32_e32 v186, v186
	v_exp_f32_e32 v187, v187
	v_exp_f32_e32 v188, v188
	v_exp_f32_e32 v189, v189
	v_exp_f32_e32 v190, v190
	v_exp_f32_e32 v191, v191
	v_exp_f32_e32 v192, v192
	v_exp_f32_e32 v193, v193
	v_add_f32_e32 v178, 1.0, v178
	v_add_f32_e32 v179, 1.0, v179
	v_add_f32_e32 v180, 1.0, v180
	v_add_f32_e32 v181, 1.0, v181
	v_add_f32_e32 v182, 1.0, v182
	v_add_f32_e32 v183, 1.0, v183
	v_add_f32_e32 v184, 1.0, v184
	v_add_f32_e32 v185, 1.0, v185
	v_add_f32_e32 v186, 1.0, v186
	v_add_f32_e32 v187, 1.0, v187
	v_add_f32_e32 v188, 1.0, v188
	v_add_f32_e32 v189, 1.0, v189
	v_add_f32_e32 v190, 1.0, v190
	v_add_f32_e32 v191, 1.0, v191
	v_add_f32_e32 v192, 1.0, v192
	v_add_f32_e32 v193, 1.0, v193
	v_rcp_f32_e32 v178, v178
	v_rcp_f32_e32 v179, v179
	v_rcp_f32_e32 v180, v180
	v_rcp_f32_e32 v181, v181
	v_rcp_f32_e32 v182, v182
	v_rcp_f32_e32 v183, v183
	v_rcp_f32_e32 v184, v184
	v_rcp_f32_e32 v185, v185
	v_rcp_f32_e32 v186, v186
	v_rcp_f32_e32 v187, v187
	v_rcp_f32_e32 v188, v188
	v_rcp_f32_e32 v189, v189
	v_rcp_f32_e32 v190, v190
	v_rcp_f32_e32 v191, v191
	v_rcp_f32_e32 v192, v192
	v_rcp_f32_e32 v193, v193
	v_mul_f32_e32 v178, v175, v178
	v_mul_f32_e32 v179, v175, v179
	v_mul_f32_e32 v180, v175, v180
	v_mul_f32_e32 v181, v175, v181
	v_mul_f32_e32 v182, v175, v182
	v_mul_f32_e32 v183, v175, v183
	v_mul_f32_e32 v184, v175, v184
	v_mul_f32_e32 v185, v175, v185
	v_exp_f32_e32 v128, v178
	v_exp_f32_e32 v129, v179
	v_exp_f32_e32 v130, v180
	v_exp_f32_e32 v131, v181
	v_exp_f32_e32 v132, v182
	v_exp_f32_e32 v133, v183
	v_exp_f32_e32 v134, v184
	v_exp_f32_e32 v135, v185
	s_nop 0
	v_fma_f32 v194, -v128, v128, 1.0
	v_fma_f32 v195, -v129, v129, 1.0
	v_fma_f32 v196, -v130, v130, 1.0
	v_fma_f32 v197, -v131, v131, 1.0
	v_fma_f32 v198, -v132, v132, 1.0
	v_fma_f32 v199, -v133, v133, 1.0
	v_fma_f32 v200, -v134, v134, 1.0
	v_fma_f32 v201, -v135, v135, 1.0
	v_max_f32_e32 v194, 0, v194
	v_max_f32_e32 v195, 0, v195
	v_max_f32_e32 v196, 0, v196
	v_max_f32_e32 v197, 0, v197
	v_max_f32_e32 v198, 0, v198
	v_max_f32_e32 v199, 0, v199
	v_max_f32_e32 v200, 0, v200
	v_max_f32_e32 v201, 0, v201
	v_sqrt_f32_e32 v194, v194
	v_sqrt_f32_e32 v195, v195
	v_sqrt_f32_e32 v196, v196
	v_sqrt_f32_e32 v197, v197
	v_sqrt_f32_e32 v198, v198
	v_sqrt_f32_e32 v199, v199
	v_sqrt_f32_e32 v200, v200
	v_sqrt_f32_e32 v201, v201
	s_waitcnt lgkmcnt(8)
	v_lshlrev_b32_e32 v144, 16, v144
	v_lshlrev_b32_e32 v145, 16, v145
	v_lshlrev_b32_e32 v146, 16, v146
	v_lshlrev_b32_e32 v147, 16, v147
	v_lshlrev_b32_e32 v148, 16, v148
	v_lshlrev_b32_e32 v149, 16, v149
	v_lshlrev_b32_e32 v150, 16, v150
	v_lshlrev_b32_e32 v151, 16, v151
	v_mul_f32_e32 v194, v194, v186
	v_mul_f32_e32 v195, v195, v187
	v_mul_f32_e32 v196, v196, v188
	v_mul_f32_e32 v197, v197, v189
	v_mul_f32_e32 v198, v198, v190
	v_mul_f32_e32 v199, v199, v191
	v_mul_f32_e32 v200, v200, v192
	v_mul_f32_e32 v201, v201, v193
	v_mul_f32_e32 v144, v194, v144
	v_mul_f32_e32 v145, v195, v145
	v_mul_f32_e32 v146, v196, v146
	v_mul_f32_e32 v147, v197, v147
	v_mul_f32_e32 v148, v198, v148
	v_mul_f32_e32 v149, v199, v149
	v_mul_f32_e32 v150, v200, v150
	v_mul_f32_e32 v151, v201, v151
	v_fma_f32 v178, v80, s53, v173
	v_fma_f32 v179, v81, s53, v173
	v_fma_f32 v180, v82, s53, v173
	v_fma_f32 v181, v83, s53, v173
	v_fma_f32 v182, v88, s53, v173
	v_fma_f32 v183, v89, s53, v173
	v_fma_f32 v184, v90, s53, v173
	v_fma_f32 v185, v91, s53, v173
	v_fma_f32 v186, v84, s53, v174
	v_fma_f32 v187, v85, s53, v174
	v_fma_f32 v188, v86, s53, v174
	v_fma_f32 v189, v87, s53, v174
	v_fma_f32 v190, v92, s53, v174
	v_fma_f32 v191, v93, s53, v174
	v_fma_f32 v192, v94, s53, v174
	v_fma_f32 v193, v95, s53, v174
	v_exp_f32_e32 v178, v178
	v_exp_f32_e32 v179, v179
	v_exp_f32_e32 v180, v180
	v_exp_f32_e32 v181, v181
	v_exp_f32_e32 v182, v182
	v_exp_f32_e32 v183, v183
	v_exp_f32_e32 v184, v184
	v_exp_f32_e32 v185, v185
	v_exp_f32_e32 v186, v186
	v_exp_f32_e32 v187, v187
	v_exp_f32_e32 v188, v188
	v_exp_f32_e32 v189, v189
	v_exp_f32_e32 v190, v190
	v_exp_f32_e32 v191, v191
	v_exp_f32_e32 v192, v192
	v_exp_f32_e32 v193, v193
	v_add_f32_e32 v178, 1.0, v178
	v_add_f32_e32 v179, 1.0, v179
	v_add_f32_e32 v180, 1.0, v180
	v_add_f32_e32 v181, 1.0, v181
	v_add_f32_e32 v182, 1.0, v182
	v_add_f32_e32 v183, 1.0, v183
	v_add_f32_e32 v184, 1.0, v184
	v_add_f32_e32 v185, 1.0, v185
	v_add_f32_e32 v186, 1.0, v186
	v_add_f32_e32 v187, 1.0, v187
	v_add_f32_e32 v188, 1.0, v188
	v_add_f32_e32 v189, 1.0, v189
	v_add_f32_e32 v190, 1.0, v190
	v_add_f32_e32 v191, 1.0, v191
	v_add_f32_e32 v192, 1.0, v192
	v_add_f32_e32 v193, 1.0, v193
	v_rcp_f32_e32 v178, v178
	v_rcp_f32_e32 v179, v179
	v_rcp_f32_e32 v180, v180
	v_rcp_f32_e32 v181, v181
	v_rcp_f32_e32 v182, v182
	v_rcp_f32_e32 v183, v183
	v_rcp_f32_e32 v184, v184
	v_rcp_f32_e32 v185, v185
	v_rcp_f32_e32 v186, v186
	v_rcp_f32_e32 v187, v187
	v_rcp_f32_e32 v188, v188
	v_rcp_f32_e32 v189, v189
	v_rcp_f32_e32 v190, v190
	v_rcp_f32_e32 v191, v191
	v_rcp_f32_e32 v192, v192
	v_rcp_f32_e32 v193, v193
	v_mul_f32_e32 v178, v175, v178
	v_mul_f32_e32 v179, v175, v179
	v_mul_f32_e32 v180, v175, v180
	v_mul_f32_e32 v181, v175, v181
	v_mul_f32_e32 v182, v175, v182
	v_mul_f32_e32 v183, v175, v183
	v_mul_f32_e32 v184, v175, v184
	v_mul_f32_e32 v185, v175, v185
	v_exp_f32_e32 v136, v178
	v_exp_f32_e32 v137, v179
	v_exp_f32_e32 v138, v180
	v_exp_f32_e32 v139, v181
	v_exp_f32_e32 v140, v182
	v_exp_f32_e32 v141, v183
	v_exp_f32_e32 v142, v184
	v_exp_f32_e32 v143, v185
	s_nop 0
	v_fma_f32 v194, -v136, v136, 1.0
	v_fma_f32 v195, -v137, v137, 1.0
	v_fma_f32 v196, -v138, v138, 1.0
	v_fma_f32 v197, -v139, v139, 1.0
	v_fma_f32 v198, -v140, v140, 1.0
	v_fma_f32 v199, -v141, v141, 1.0
	v_fma_f32 v200, -v142, v142, 1.0
	v_fma_f32 v201, -v143, v143, 1.0
	v_max_f32_e32 v194, 0, v194
	v_max_f32_e32 v195, 0, v195
	v_max_f32_e32 v196, 0, v196
	v_max_f32_e32 v197, 0, v197
	v_max_f32_e32 v198, 0, v198
	v_max_f32_e32 v199, 0, v199
	v_max_f32_e32 v200, 0, v200
	v_max_f32_e32 v201, 0, v201
	v_sqrt_f32_e32 v194, v194
	v_sqrt_f32_e32 v195, v195
	v_sqrt_f32_e32 v196, v196
	v_sqrt_f32_e32 v197, v197
	v_sqrt_f32_e32 v198, v198
	v_sqrt_f32_e32 v199, v199
	v_sqrt_f32_e32 v200, v200
	v_sqrt_f32_e32 v201, v201
	s_waitcnt lgkmcnt(0)
	v_lshlrev_b32_e32 v152, 16, v152
	v_lshlrev_b32_e32 v153, 16, v153
	v_lshlrev_b32_e32 v154, 16, v154
	v_lshlrev_b32_e32 v155, 16, v155
	v_lshlrev_b32_e32 v156, 16, v156
	v_lshlrev_b32_e32 v157, 16, v157
	v_lshlrev_b32_e32 v158, 16, v158
	v_lshlrev_b32_e32 v159, 16, v159
	v_mul_f32_e32 v194, v194, v186
	v_mul_f32_e32 v195, v195, v187
	v_mul_f32_e32 v196, v196, v188
	v_mul_f32_e32 v197, v197, v189
	v_mul_f32_e32 v198, v198, v190
	v_mul_f32_e32 v199, v199, v191
	v_mul_f32_e32 v200, v200, v192
	v_mul_f32_e32 v201, v201, v193
	v_mul_f32_e32 v152, v194, v152
	v_mul_f32_e32 v153, v195, v153
	v_mul_f32_e32 v154, v196, v154
	v_mul_f32_e32 v155, v197, v155
	v_mul_f32_e32 v156, v198, v156
	v_mul_f32_e32 v157, v199, v157
	v_mul_f32_e32 v158, v200, v158
	v_mul_f32_e32 v159, v201, v159
	v_fma_f32 v145, v129, v144, v145
	v_fma_f32 v149, v133, v148, v149
	v_fma_f32 v153, v137, v152, v153
	v_fma_f32 v157, v141, v156, v157
	v_mul_f32_e32 v129, v129, v128
	v_mul_f32_e32 v133, v133, v132
	v_mul_f32_e32 v137, v137, v136
	v_mul_f32_e32 v141, v141, v140
	v_fma_f32 v146, v130, v145, v146
	v_fma_f32 v150, v134, v149, v150
	v_fma_f32 v154, v138, v153, v154
	v_fma_f32 v158, v142, v157, v158
	v_mul_f32_e32 v130, v130, v129
	v_mul_f32_e32 v134, v134, v133
	v_mul_f32_e32 v138, v138, v137
	v_mul_f32_e32 v142, v142, v141
	v_fma_f32 v147, v131, v146, v147
	v_fma_f32 v151, v135, v150, v151
	v_fma_f32 v155, v139, v154, v155
	v_fma_f32 v159, v143, v158, v159
	v_mul_f32_e32 v131, v131, v130
	v_mul_f32_e32 v135, v135, v134
	v_mul_f32_e32 v139, v139, v138
	v_mul_f32_e32 v143, v143, v142
	ds_bpermute_b32 v178, v204, v131
	ds_bpermute_b32 v182, v204, v147
	ds_bpermute_b32 v179, v204, v135
	ds_bpermute_b32 v183, v204, v151
	ds_bpermute_b32 v180, v204, v139
	ds_bpermute_b32 v184, v204, v155
	ds_bpermute_b32 v181, v204, v143
	ds_bpermute_b32 v185, v204, v159
	s_waitcnt lgkmcnt(0)
	v_fma_f32 v186, v182, v131, v147
	v_cndmask_b32_e64 v178, 1.0, v178, s[34:35]
	v_fma_f32 v187, v183, v135, v151
	v_cndmask_b32_e64 v179, 1.0, v179, s[34:35]
	v_fma_f32 v188, v184, v139, v155
	v_cndmask_b32_e64 v180, 1.0, v180, s[34:35]
	v_fma_f32 v189, v185, v143, v159
	v_cndmask_b32_e64 v181, 1.0, v181, s[34:35]
	v_cndmask_b32_e64 v223, v147, v186, s[34:35]
	v_mul_f32_e32 v219, v131, v178
	v_cndmask_b32_e64 v224, v151, v187, s[34:35]
	v_mul_f32_e32 v220, v135, v179
	v_cndmask_b32_e64 v225, v155, v188, s[34:35]
	v_mul_f32_e32 v221, v139, v180
	v_cndmask_b32_e64 v226, v159, v189, s[34:35]
	v_mul_f32_e32 v222, v143, v181
	ds_bpermute_b32 v178, v205, v219
	ds_bpermute_b32 v182, v205, v223
	ds_bpermute_b32 v179, v205, v220
	ds_bpermute_b32 v183, v205, v224
	ds_bpermute_b32 v180, v205, v221
	ds_bpermute_b32 v184, v205, v225
	ds_bpermute_b32 v181, v205, v222
	ds_bpermute_b32 v185, v205, v226
	s_waitcnt lgkmcnt(0)
	v_fma_f32 v186, v182, v219, v223
	v_cndmask_b32_e64 v178, 1.0, v178, s[36:37]
	v_fma_f32 v187, v183, v220, v224
	v_cndmask_b32_e64 v179, 1.0, v179, s[36:37]
	v_fma_f32 v188, v184, v221, v225
	v_cndmask_b32_e64 v180, 1.0, v180, s[36:37]
	v_fma_f32 v189, v185, v222, v226
	v_cndmask_b32_e64 v181, 1.0, v181, s[36:37]
	v_cndmask_b32_e64 v223, v223, v186, s[36:37]
	v_mul_f32_e32 v219, v219, v178
	v_cndmask_b32_e64 v224, v224, v187, s[36:37]
	v_mul_f32_e32 v220, v220, v179
	v_cndmask_b32_e64 v225, v225, v188, s[36:37]
	v_mul_f32_e32 v221, v221, v180
	v_cndmask_b32_e64 v226, v226, v189, s[36:37]
	v_mul_f32_e32 v222, v222, v181
	ds_bpermute_b32 v227, v204, v219
	ds_bpermute_b32 v231, v204, v223
	ds_bpermute_b32 v235, v206, v219
	ds_bpermute_b32 v239, v206, v223
	ds_bpermute_b32 v228, v204, v220
	ds_bpermute_b32 v232, v204, v224
	ds_bpermute_b32 v236, v206, v220
	ds_bpermute_b32 v244, v206, v224
	ds_bpermute_b32 v229, v204, v221
	ds_bpermute_b32 v233, v204, v225
	ds_bpermute_b32 v237, v206, v221
	ds_bpermute_b32 v245, v206, v225
	ds_bpermute_b32 v230, v204, v222
	ds_bpermute_b32 v234, v204, v226
	ds_bpermute_b32 v238, v206, v222
	ds_bpermute_b32 v246, v206, v226
	s_waitcnt lgkmcnt(0)
	v_cndmask_b32_e64 v227, 1.0, v227, s[34:35]
	v_cndmask_b32_e64 v231, 0, v231, s[34:35]
	v_cndmask_b32_e64 v228, 1.0, v228, s[34:35]
	v_cndmask_b32_e64 v232, 0, v232, s[34:35]
	v_cndmask_b32_e64 v229, 1.0, v229, s[34:35]
	v_cndmask_b32_e64 v233, 0, v233, s[34:35]
	v_cndmask_b32_e64 v230, 1.0, v230, s[34:35]
	v_cndmask_b32_e64 v234, 0, v234, s[34:35]
	v_mov_b32_e32 v190, v235
	v_mov_b32_e32 v194, v239
	v_mov_b32_e32 v198, v190
	v_mov_b32_e32 v201, v194
	v_fma_f32 v194, v194, v236, v244
	v_mul_f32_e32 v190, v190, v236
	v_mov_b32_e32 v199, v190
	v_mov_b32_e32 v177, v194
	v_fma_f32 v194, v194, v237, v245
	v_mul_f32_e32 v190, v190, v237
	v_mov_b32_e32 v200, v190
	v_mov_b32_e32 v203, v194
	v_fma_f32 v194, v194, v238, v246
	v_mul_f32_e32 v190, v190, v238
	v_mov_b32_e32 v191, v194
	ds_write_b64 v207, v[190:191]
	s_waitcnt lgkmcnt(0)
	s_barrier
	ds_read_b64 v[178:179], v208
	ds_read_b64 v[180:181], v208 offset:512
	s_waitcnt lgkmcnt(0)
	v_fma_f32 v182, v176, v178, v179
	v_cndmask_b32_e64 v183, v176, v182, s[38:39]
	v_fma_f32 v176, v182, v180, v181
	v_mov_b32_e32 v184, v183
	v_fma_f32 v185, v183, v198, v201
	v_fma_f32 v186, v183, v199, v177
	v_fma_f32 v187, v183, v200, v203
	v_fma_f32 v184, v184, v227, v231
	v_fma_f32 v185, v185, v228, v232
	v_fma_f32 v186, v186, v229, v233
	v_fma_f32 v187, v187, v230, v234
	v_fma_f32 v144, v184, v128, v144
	v_fma_f32 v148, v185, v132, v148
	v_fma_f32 v152, v186, v136, v152
	v_fma_f32 v156, v187, v140, v156
	v_fma_f32 v145, v184, v129, v145
	v_fma_f32 v149, v185, v133, v149
	v_fma_f32 v153, v186, v137, v153
	v_fma_f32 v157, v187, v141, v157
	v_fma_f32 v146, v184, v130, v146
	v_fma_f32 v150, v185, v134, v150
	v_fma_f32 v154, v186, v138, v154
	v_fma_f32 v158, v187, v142, v158
	v_fma_f32 v147, v184, v131, v147
	v_fma_f32 v151, v185, v135, v151
	v_fma_f32 v155, v186, v139, v155
	v_fma_f32 v159, v187, v143, v159
	v_cvt_pk_bf16_f32 v178, v144, v145
	v_cvt_pk_bf16_f32 v179, v146, v147
	v_cvt_pk_bf16_f32 v180, v148, v149
	v_cvt_pk_bf16_f32 v181, v150, v151
	v_cvt_pk_bf16_f32 v182, v152, v153
	v_cvt_pk_bf16_f32 v183, v154, v155
	v_cvt_pk_bf16_f32 v184, v156, v157
	v_cvt_pk_bf16_f32 v185, v158, v159
	global_store_dword v209, v178, s[44:45]
	global_store_dword v209, v179, s[44:45] offset:256
	global_store_dword v209, v180, s[44:45] offset:512
	global_store_dword v209, v181, s[44:45] offset:768
	global_store_dword v209, v182, s[44:45] offset:1024
	global_store_dword v209, v183, s[44:45] offset:1280
	global_store_dword v209, v184, s[44:45] offset:1536
	global_store_dword v209, v185, s[44:45] offset:1792
	s_add_i32 s13, s13, 1
	s_cmp_eq_u32 s13, 2
	s_cbranch_scc1 .Lmylru_t0_4
	s_waitcnt vmcnt(8)
	s_branch .Lmylru_t1_4

.Lmylru_t1_4:
	s_barrier
	s_add_i32 s54, s13, -2
	s_lshl_b32 s55, s54, 14
	s_lshl_b32 s56, s6, 11
	s_add_i32 s55, s55, s56
	s_add_u32 s44, s22, s55
	s_addc_u32 s45, s23, 0
	s_cmp_eq_u32 s13, 17
	s_cbranch_scc1 .Lmylru_nodma_4
	s_add_i32 s58, s13, 1
	s_cmp_lt_u32 s58, 2
	s_lshl_b32 s50, s58, 7
	s_lshl_b32 s51, s9, 8
	s_add_i32 s51, s51, 0x8000
	s_add_i32 s51, s51, s50
	s_lshl_b32 s59, s9, 11
	s_add_i32 s59, s59, s50
	s_addk_i32 s59, 0xff00
	s_cmp_lt_u32 s58, 2
	s_cselect_b32 s59, s51, s59
	s_lshl_b32 s52, s59, 11
	s_add_u32 s46, s16, s52
	s_addc_u32 s47, s17, 0
	s_lshl_b32 s52, s6, 13
	s_mov_b32 m0, s52
	s_add_i32 s52, s52, 0x400
	global_load_lds_dwordx4 v211, s[46:47]
	s_mov_b32 m0, s52
	s_add_i32 s52, s52, 0x400
	global_load_lds_dwordx4 v212, s[46:47]
	s_mov_b32 m0, s52
	s_add_i32 s52, s52, 0x400
	global_load_lds_dwordx4 v213, s[46:47]
	s_mov_b32 m0, s52
	s_add_i32 s52, s52, 0x400
	global_load_lds_dwordx4 v214, s[46:47]
	s_mov_b32 m0, s52
	s_add_i32 s52, s52, 0x400
	global_load_lds_dwordx4 v215, s[46:47]
	s_mov_b32 m0, s52
	s_add_i32 s52, s52, 0x400
	global_load_lds_dwordx4 v216, s[46:47]
	s_mov_b32 m0, s52
	s_add_i32 s52, s52, 0x400
	global_load_lds_dwordx4 v217, s[46:47]
	s_mov_b32 m0, s52
	s_nop 0
	global_load_lds_dwordx4 v218, s[46:47]
.Lmylru_nodma_4:
	v_or_b32_e32 v163, 0x10000, v162
	ds_read_b128 v[96:99], v163
	ds_read_b128 v[100:103], v163 offset:8192
	ds_read_b128 v[104:107], v163 offset:16384
	ds_read_b128 v[108:111], v163 offset:24576
	v_xor_b32_e32 v164, 0x40, v163
	ds_read_b128 v[112:115], v164
	ds_read_b128 v[116:119], v164 offset:8192
	ds_read_b128 v[120:123], v164 offset:16384
	ds_read_b128 v[124:127], v164 offset:24576
	s_waitcnt lgkmcnt(7)
	v_mfma_f32_16x16x32_bf16 v[64:67], v[96:99], v[0:3], 0
	v_mfma_f32_16x16x32_bf16 v[68:71], v[96:99], v[32:35], 0
	v_xor_b32_e32 v164, 0x80, v163
	ds_read_b128 v[96:99], v164
	s_waitcnt lgkmcnt(7)
	v_mfma_f32_16x16x32_bf16 v[72:75], v[100:103], v[0:3], 0
	v_mfma_f32_16x16x32_bf16 v[76:79], v[100:103], v[32:35], 0
	ds_read_b128 v[100:103], v164 offset:8192
	s_waitcnt lgkmcnt(7)
	v_mfma_f32_16x16x32_bf16 v[80:83], v[104:107], v[0:3], 0
	v_mfma_f32_16x16x32_bf16 v[84:87], v[104:107], v[32:35], 0
	ds_read_b128 v[104:107], v164 offset:16384
	s_waitcnt lgkmcnt(7)
	v_mfma_f32_16x16x32_bf16 v[88:91], v[108:111], v[0:3], 0
	v_mfma_f32_16x16x32_bf16 v[92:95], v[108:111], v[32:35], 0
	ds_read_b128 v[108:111], v164 offset:24576
	s_waitcnt lgkmcnt(7)
	v_mfma_f32_16x16x32_bf16 v[64:67], v[112:115], v[4:7], v[64:67]
	v_mfma_f32_16x16x32_bf16 v[68:71], v[112:115], v[36:39], v[68:71]
	v_xor_b32_e32 v164, 0xc0, v163
	ds_read_b128 v[112:115], v164
	s_waitcnt lgkmcnt(7)
	v_mfma_f32_16x16x32_bf16 v[72:75], v[116:119], v[4:7], v[72:75]
	v_mfma_f32_16x16x32_bf16 v[76:79], v[116:119], v[36:39], v[76:79]
	ds_read_b128 v[116:119], v164 offset:8192
	s_waitcnt lgkmcnt(7)
	v_mfma_f32_16x16x32_bf16 v[80:83], v[120:123], v[4:7], v[80:83]
	v_mfma_f32_16x16x32_bf16 v[84:87], v[120:123], v[36:39], v[84:87]
	ds_read_b128 v[120:123], v164 offset:16384
	s_waitcnt lgkmcnt(7)
	v_mfma_f32_16x16x32_bf16 v[88:91], v[124:127], v[4:7], v[88:91]
	v_mfma_f32_16x16x32_bf16 v[92:95], v[124:127], v[36:39], v[92:95]
	ds_read_b128 v[124:127], v164 offset:24576
	s_waitcnt lgkmcnt(7)
	v_mfma_f32_16x16x32_bf16 v[64:67], v[96:99], v[8:11], v[64:67]
	v_mfma_f32_16x16x32_bf16 v[68:71], v[96:99], v[40:43], v[68:71]
	v_xor_b32_e32 v164, 0x100, v163
	ds_read_b128 v[96:99], v164
	s_waitcnt lgkmcnt(7)
	v_mfma_f32_16x16x32_bf16 v[72:75], v[100:103], v[8:11], v[72:75]
	v_mfma_f32_16x16x32_bf16 v[76:79], v[100:103], v[40:43], v[76:79]
	ds_read_b128 v[100:103], v164 offset:8192
	s_waitcnt lgkmcnt(7)
	v_mfma_f32_16x16x32_bf16 v[80:83], v[104:107], v[8:11], v[80:83]
	v_mfma_f32_16x16x32_bf16 v[84:87], v[104:107], v[40:43], v[84:87]
	ds_read_b128 v[104:107], v164 offset:16384
	s_waitcnt lgkmcnt(7)
	v_mfma_f32_16x16x32_bf16 v[88:91], v[108:111], v[8:11], v[88:91]
	v_mfma_f32_16x16x32_bf16 v[92:95], v[108:111], v[40:43], v[92:95]
	ds_read_b128 v[108:111], v164 offset:24576
	s_waitcnt lgkmcnt(7)
	v_mfma_f32_16x16x32_bf16 v[64:67], v[112:115], v[12:15], v[64:67]
	v_mfma_f32_16x16x32_bf16 v[68:71], v[112:115], v[44:47], v[68:71]
	v_xor_b32_e32 v164, 0x140, v163
	ds_read_b128 v[112:115], v164
	s_waitcnt lgkmcnt(7)
	v_mfma_f32_16x16x32_bf16 v[72:75], v[116:119], v[12:15], v[72:75]
	v_mfma_f32_16x16x32_bf16 v[76:79], v[116:119], v[44:47], v[76:79]
	ds_read_b128 v[116:119], v164 offset:8192
	s_waitcnt lgkmcnt(7)
	v_mfma_f32_16x16x32_bf16 v[80:83], v[120:123], v[12:15], v[80:83]
	v_mfma_f32_16x16x32_bf16 v[84:87], v[120:123], v[44:47], v[84:87]
	ds_read_b128 v[120:123], v164 offset:16384
	s_waitcnt lgkmcnt(7)
	v_mfma_f32_16x16x32_bf16 v[88:91], v[124:127], v[12:15], v[88:91]
	v_mfma_f32_16x16x32_bf16 v[92:95], v[124:127], v[44:47], v[92:95]
	ds_read_b128 v[124:127], v164 offset:24576
	s_waitcnt lgkmcnt(7)
	v_mfma_f32_16x16x32_bf16 v[64:67], v[96:99], v[16:19], v[64:67]
	v_mfma_f32_16x16x32_bf16 v[68:71], v[96:99], v[48:51], v[68:71]
	v_xor_b32_e32 v164, 0x180, v163
	ds_read_b128 v[96:99], v164
	s_waitcnt lgkmcnt(7)
	v_mfma_f32_16x16x32_bf16 v[72:75], v[100:103], v[16:19], v[72:75]
	v_mfma_f32_16x16x32_bf16 v[76:79], v[100:103], v[48:51], v[76:79]
	ds_read_b128 v[100:103], v164 offset:8192
	s_waitcnt lgkmcnt(7)
	v_mfma_f32_16x16x32_bf16 v[80:83], v[104:107], v[16:19], v[80:83]
	v_mfma_f32_16x16x32_bf16 v[84:87], v[104:107], v[48:51], v[84:87]
	ds_read_b128 v[104:107], v164 offset:16384
	s_waitcnt lgkmcnt(7)
	v_mfma_f32_16x16x32_bf16 v[88:91], v[108:111], v[16:19], v[88:91]
	v_mfma_f32_16x16x32_bf16 v[92:95], v[108:111], v[48:51], v[92:95]
	ds_read_b128 v[108:111], v164 offset:24576
	s_waitcnt lgkmcnt(7)
	v_mfma_f32_16x16x32_bf16 v[64:67], v[112:115], v[20:23], v[64:67]
	v_mfma_f32_16x16x32_bf16 v[68:71], v[112:115], v[52:55], v[68:71]
	v_xor_b32_e32 v164, 0x1c0, v163
	ds_read_b128 v[112:115], v164
	s_waitcnt lgkmcnt(7)
	v_mfma_f32_16x16x32_bf16 v[72:75], v[116:119], v[20:23], v[72:75]
	v_mfma_f32_16x16x32_bf16 v[76:79], v[116:119], v[52:55], v[76:79]
	ds_read_b128 v[116:119], v164 offset:8192
	s_waitcnt lgkmcnt(7)
	v_mfma_f32_16x16x32_bf16 v[80:83], v[120:123], v[20:23], v[80:83]
	v_mfma_f32_16x16x32_bf16 v[84:87], v[120:123], v[52:55], v[84:87]
	ds_read_b128 v[120:123], v164 offset:16384
	s_waitcnt lgkmcnt(7)
	v_mfma_f32_16x16x32_bf16 v[88:91], v[124:127], v[20:23], v[88:91]
	v_mfma_f32_16x16x32_bf16 v[92:95], v[124:127], v[52:55], v[92:95]
	ds_read_b128 v[124:127], v164 offset:24576
	s_waitcnt lgkmcnt(7)
	v_mfma_f32_16x16x32_bf16 v[64:67], v[96:99], v[24:27], v[64:67]
	v_mfma_f32_16x16x32_bf16 v[68:71], v[96:99], v[56:59], v[68:71]
	s_waitcnt lgkmcnt(6)
	v_mfma_f32_16x16x32_bf16 v[72:75], v[100:103], v[24:27], v[72:75]
	v_mfma_f32_16x16x32_bf16 v[76:79], v[100:103], v[56:59], v[76:79]
	s_waitcnt lgkmcnt(5)
	v_mfma_f32_16x16x32_bf16 v[80:83], v[104:107], v[24:27], v[80:83]
	v_mfma_f32_16x16x32_bf16 v[84:87], v[104:107], v[56:59], v[84:87]
	s_waitcnt lgkmcnt(4)
	v_mfma_f32_16x16x32_bf16 v[88:91], v[108:111], v[24:27], v[88:91]
	v_mfma_f32_16x16x32_bf16 v[92:95], v[108:111], v[56:59], v[92:95]
	s_waitcnt lgkmcnt(3)
	v_mfma_f32_16x16x32_bf16 v[64:67], v[112:115], v[28:31], v[64:67]
	v_mfma_f32_16x16x32_bf16 v[68:71], v[112:115], v[60:63], v[68:71]
	s_waitcnt lgkmcnt(2)
	v_mfma_f32_16x16x32_bf16 v[72:75], v[116:119], v[28:31], v[72:75]
	v_mfma_f32_16x16x32_bf16 v[76:79], v[116:119], v[60:63], v[76:79]
	s_waitcnt lgkmcnt(1)
	v_mfma_f32_16x16x32_bf16 v[80:83], v[120:123], v[28:31], v[80:83]
	v_mfma_f32_16x16x32_bf16 v[84:87], v[120:123], v[60:63], v[84:87]
	s_waitcnt lgkmcnt(0)
	v_mfma_f32_16x16x32_bf16 v[88:91], v[124:127], v[28:31], v[88:91]
	v_mfma_f32_16x16x32_bf16 v[92:95], v[124:127], v[60:63], v[92:95]
	v_or_b32_e32 v169, 0x10000, v165
	v_or_b32_e32 v170, 0x10000, v166
	v_or_b32_e32 v171, 0x10000, v167
	v_or_b32_e32 v172, 0x10000, v168
	ds_read_u16 v144, v169
	ds_read_u16 v145, v170
	ds_read_u16 v146, v171
	ds_read_u16 v147, v172
	ds_read_u16 v148, v169 offset:8192
	ds_read_u16 v149, v170 offset:8192
	ds_read_u16 v150, v171 offset:8192
	ds_read_u16 v151, v172 offset:8192
	ds_read_u16 v152, v169 offset:16384
	ds_read_u16 v153, v170 offset:16384
	ds_read_u16 v154, v171 offset:16384
	ds_read_u16 v155, v172 offset:16384
	ds_read_u16 v156, v169 offset:24576
	ds_read_u16 v157, v170 offset:24576
	ds_read_u16 v158, v171 offset:24576
	ds_read_u16 v159, v172 offset:24576
	s_nop 7
	v_fma_f32 v178, v64, s53, v173
	v_fma_f32 v179, v65, s53, v173
	v_fma_f32 v180, v66, s53, v173
	v_fma_f32 v181, v67, s53, v173
	v_fma_f32 v182, v72, s53, v173
	v_fma_f32 v183, v73, s53, v173
	v_fma_f32 v184, v74, s53, v173
	v_fma_f32 v185, v75, s53, v173
	v_fma_f32 v186, v68, s53, v174
	v_fma_f32 v187, v69, s53, v174
	v_fma_f32 v188, v70, s53, v174
	v_fma_f32 v189, v71, s53, v174
	v_fma_f32 v190, v76, s53, v174
	v_fma_f32 v191, v77, s53, v174
	v_fma_f32 v192, v78, s53, v174
	v_fma_f32 v193, v79, s53, v174
	v_exp_f32_e32 v178, v178
	v_exp_f32_e32 v179, v179
	v_exp_f32_e32 v180, v180
	v_exp_f32_e32 v181, v181
	v_exp_f32_e32 v182, v182
	v_exp_f32_e32 v183, v183
	v_exp_f32_e32 v184, v184
	v_exp_f32_e32 v185, v185
	v_exp_f32_e32 v186, v186
	v_exp_f32_e32 v187, v187
	v_exp_f32_e32 v188, v188
	v_exp_f32_e32 v189, v189
	v_exp_f32_e32 v190, v190
	v_exp_f32_e32 v191, v191
	v_exp_f32_e32 v192, v192
	v_exp_f32_e32 v193, v193
	v_add_f32_e32 v178, 1.0, v178
	v_add_f32_e32 v179, 1.0, v179
	v_add_f32_e32 v180, 1.0, v180
	v_add_f32_e32 v181, 1.0, v181
	v_add_f32_e32 v182, 1.0, v182
	v_add_f32_e32 v183, 1.0, v183
	v_add_f32_e32 v184, 1.0, v184
	v_add_f32_e32 v185, 1.0, v185
	v_add_f32_e32 v186, 1.0, v186
	v_add_f32_e32 v187, 1.0, v187
	v_add_f32_e32 v188, 1.0, v188
	v_add_f32_e32 v189, 1.0, v189
	v_add_f32_e32 v190, 1.0, v190
	v_add_f32_e32 v191, 1.0, v191
	v_add_f32_e32 v192, 1.0, v192
	v_add_f32_e32 v193, 1.0, v193
	v_rcp_f32_e32 v178, v178
	v_rcp_f32_e32 v179, v179
	v_rcp_f32_e32 v180, v180
	v_rcp_f32_e32 v181, v181
	v_rcp_f32_e32 v182, v182
	v_rcp_f32_e32 v183, v183
	v_rcp_f32_e32 v184, v184
	v_rcp_f32_e32 v185, v185
	v_rcp_f32_e32 v186, v186
	v_rcp_f32_e32 v187, v187
	v_rcp_f32_e32 v188, v188
	v_rcp_f32_e32 v189, v189
	v_rcp_f32_e32 v190, v190
	v_rcp_f32_e32 v191, v191
	v_rcp_f32_e32 v192, v192
	v_rcp_f32_e32 v193, v193
	v_mul_f32_e32 v178, v175, v178
	v_mul_f32_e32 v179, v175, v179
	v_mul_f32_e32 v180, v175, v180
	v_mul_f32_e32 v181, v175, v181
	v_mul_f32_e32 v182, v175, v182
	v_mul_f32_e32 v183, v175, v183
	v_mul_f32_e32 v184, v175, v184
	v_mul_f32_e32 v185, v175, v185
	v_exp_f32_e32 v128, v178
	v_exp_f32_e32 v129, v179
	v_exp_f32_e32 v130, v180
	v_exp_f32_e32 v131, v181
	v_exp_f32_e32 v132, v182
	v_exp_f32_e32 v133, v183
	v_exp_f32_e32 v134, v184
	v_exp_f32_e32 v135, v185
	s_nop 0
	v_fma_f32 v194, -v128, v128, 1.0
	v_fma_f32 v195, -v129, v129, 1.0
	v_fma_f32 v196, -v130, v130, 1.0
	v_fma_f32 v197, -v131, v131, 1.0
	v_fma_f32 v198, -v132, v132, 1.0
	v_fma_f32 v199, -v133, v133, 1.0
	v_fma_f32 v200, -v134, v134, 1.0
	v_fma_f32 v201, -v135, v135, 1.0
	v_max_f32_e32 v194, 0, v194
	v_max_f32_e32 v195, 0, v195
	v_max_f32_e32 v196, 0, v196
	v_max_f32_e32 v197, 0, v197
	v_max_f32_e32 v198, 0, v198
	v_max_f32_e32 v199, 0, v199
	v_max_f32_e32 v200, 0, v200
	v_max_f32_e32 v201, 0, v201
	v_sqrt_f32_e32 v194, v194
	v_sqrt_f32_e32 v195, v195
	v_sqrt_f32_e32 v196, v196
	v_sqrt_f32_e32 v197, v197
	v_sqrt_f32_e32 v198, v198
	v_sqrt_f32_e32 v199, v199
	v_sqrt_f32_e32 v200, v200
	v_sqrt_f32_e32 v201, v201
	s_waitcnt lgkmcnt(8)
	v_lshlrev_b32_e32 v144, 16, v144
	v_lshlrev_b32_e32 v145, 16, v145
	v_lshlrev_b32_e32 v146, 16, v146
	v_lshlrev_b32_e32 v147, 16, v147
	v_lshlrev_b32_e32 v148, 16, v148
	v_lshlrev_b32_e32 v149, 16, v149
	v_lshlrev_b32_e32 v150, 16, v150
	v_lshlrev_b32_e32 v151, 16, v151
	v_mul_f32_e32 v194, v194, v186
	v_mul_f32_e32 v195, v195, v187
	v_mul_f32_e32 v196, v196, v188
	v_mul_f32_e32 v197, v197, v189
	v_mul_f32_e32 v198, v198, v190
	v_mul_f32_e32 v199, v199, v191
	v_mul_f32_e32 v200, v200, v192
	v_mul_f32_e32 v201, v201, v193
	v_mul_f32_e32 v144, v194, v144
	v_mul_f32_e32 v145, v195, v145
	v_mul_f32_e32 v146, v196, v146
	v_mul_f32_e32 v147, v197, v147
	v_mul_f32_e32 v148, v198, v148
	v_mul_f32_e32 v149, v199, v149
	v_mul_f32_e32 v150, v200, v150
	v_mul_f32_e32 v151, v201, v151
	v_fma_f32 v178, v80, s53, v173
	v_fma_f32 v179, v81, s53, v173
	v_fma_f32 v180, v82, s53, v173
	v_fma_f32 v181, v83, s53, v173
	v_fma_f32 v182, v88, s53, v173
	v_fma_f32 v183, v89, s53, v173
	v_fma_f32 v184, v90, s53, v173
	v_fma_f32 v185, v91, s53, v173
	v_fma_f32 v186, v84, s53, v174
	v_fma_f32 v187, v85, s53, v174
	v_fma_f32 v188, v86, s53, v174
	v_fma_f32 v189, v87, s53, v174
	v_fma_f32 v190, v92, s53, v174
	v_fma_f32 v191, v93, s53, v174
	v_fma_f32 v192, v94, s53, v174
	v_fma_f32 v193, v95, s53, v174
	v_exp_f32_e32 v178, v178
	v_exp_f32_e32 v179, v179
	v_exp_f32_e32 v180, v180
	v_exp_f32_e32 v181, v181
	v_exp_f32_e32 v182, v182
	v_exp_f32_e32 v183, v183
	v_exp_f32_e32 v184, v184
	v_exp_f32_e32 v185, v185
	v_exp_f32_e32 v186, v186
	v_exp_f32_e32 v187, v187
	v_exp_f32_e32 v188, v188
	v_exp_f32_e32 v189, v189
	v_exp_f32_e32 v190, v190
	v_exp_f32_e32 v191, v191
	v_exp_f32_e32 v192, v192
	v_exp_f32_e32 v193, v193
	v_add_f32_e32 v178, 1.0, v178
	v_add_f32_e32 v179, 1.0, v179
	v_add_f32_e32 v180, 1.0, v180
	v_add_f32_e32 v181, 1.0, v181
	v_add_f32_e32 v182, 1.0, v182
	v_add_f32_e32 v183, 1.0, v183
	v_add_f32_e32 v184, 1.0, v184
	v_add_f32_e32 v185, 1.0, v185
	v_add_f32_e32 v186, 1.0, v186
	v_add_f32_e32 v187, 1.0, v187
	v_add_f32_e32 v188, 1.0, v188
	v_add_f32_e32 v189, 1.0, v189
	v_add_f32_e32 v190, 1.0, v190
	v_add_f32_e32 v191, 1.0, v191
	v_add_f32_e32 v192, 1.0, v192
	v_add_f32_e32 v193, 1.0, v193
	v_rcp_f32_e32 v178, v178
	v_rcp_f32_e32 v179, v179
	v_rcp_f32_e32 v180, v180
	v_rcp_f32_e32 v181, v181
	v_rcp_f32_e32 v182, v182
	v_rcp_f32_e32 v183, v183
	v_rcp_f32_e32 v184, v184
	v_rcp_f32_e32 v185, v185
	v_rcp_f32_e32 v186, v186
	v_rcp_f32_e32 v187, v187
	v_rcp_f32_e32 v188, v188
	v_rcp_f32_e32 v189, v189
	v_rcp_f32_e32 v190, v190
	v_rcp_f32_e32 v191, v191
	v_rcp_f32_e32 v192, v192
	v_rcp_f32_e32 v193, v193
	v_mul_f32_e32 v178, v175, v178
	v_mul_f32_e32 v179, v175, v179
	v_mul_f32_e32 v180, v175, v180
	v_mul_f32_e32 v181, v175, v181
	v_mul_f32_e32 v182, v175, v182
	v_mul_f32_e32 v183, v175, v183
	v_mul_f32_e32 v184, v175, v184
	v_mul_f32_e32 v185, v175, v185
	v_exp_f32_e32 v136, v178
	v_exp_f32_e32 v137, v179
	v_exp_f32_e32 v138, v180
	v_exp_f32_e32 v139, v181
	v_exp_f32_e32 v140, v182
	v_exp_f32_e32 v141, v183
	v_exp_f32_e32 v142, v184
	v_exp_f32_e32 v143, v185
	s_nop 0
	v_fma_f32 v194, -v136, v136, 1.0
	v_fma_f32 v195, -v137, v137, 1.0
	v_fma_f32 v196, -v138, v138, 1.0
	v_fma_f32 v197, -v139, v139, 1.0
	v_fma_f32 v198, -v140, v140, 1.0
	v_fma_f32 v199, -v141, v141, 1.0
	v_fma_f32 v200, -v142, v142, 1.0
	v_fma_f32 v201, -v143, v143, 1.0
	v_max_f32_e32 v194, 0, v194
	v_max_f32_e32 v195, 0, v195
	v_max_f32_e32 v196, 0, v196
	v_max_f32_e32 v197, 0, v197
	v_max_f32_e32 v198, 0, v198
	v_max_f32_e32 v199, 0, v199
	v_max_f32_e32 v200, 0, v200
	v_max_f32_e32 v201, 0, v201
	v_sqrt_f32_e32 v194, v194
	v_sqrt_f32_e32 v195, v195
	v_sqrt_f32_e32 v196, v196
	v_sqrt_f32_e32 v197, v197
	v_sqrt_f32_e32 v198, v198
	v_sqrt_f32_e32 v199, v199
	v_sqrt_f32_e32 v200, v200
	v_sqrt_f32_e32 v201, v201
	s_waitcnt lgkmcnt(0)
	v_lshlrev_b32_e32 v152, 16, v152
	v_lshlrev_b32_e32 v153, 16, v153
	v_lshlrev_b32_e32 v154, 16, v154
	v_lshlrev_b32_e32 v155, 16, v155
	v_lshlrev_b32_e32 v156, 16, v156
	v_lshlrev_b32_e32 v157, 16, v157
	v_lshlrev_b32_e32 v158, 16, v158
	v_lshlrev_b32_e32 v159, 16, v159
	v_mul_f32_e32 v194, v194, v186
	v_mul_f32_e32 v195, v195, v187
	v_mul_f32_e32 v196, v196, v188
	v_mul_f32_e32 v197, v197, v189
	v_mul_f32_e32 v198, v198, v190
	v_mul_f32_e32 v199, v199, v191
	v_mul_f32_e32 v200, v200, v192
	v_mul_f32_e32 v201, v201, v193
	v_mul_f32_e32 v152, v194, v152
	v_mul_f32_e32 v153, v195, v153
	v_mul_f32_e32 v154, v196, v154
	v_mul_f32_e32 v155, v197, v155
	v_mul_f32_e32 v156, v198, v156
	v_mul_f32_e32 v157, v199, v157
	v_mul_f32_e32 v158, v200, v158
	v_mul_f32_e32 v159, v201, v159
	v_fma_f32 v145, v129, v144, v145
	v_fma_f32 v149, v133, v148, v149
	v_fma_f32 v153, v137, v152, v153
	v_fma_f32 v157, v141, v156, v157
	v_mul_f32_e32 v129, v129, v128
	v_mul_f32_e32 v133, v133, v132
	v_mul_f32_e32 v137, v137, v136
	v_mul_f32_e32 v141, v141, v140
	v_fma_f32 v146, v130, v145, v146
	v_fma_f32 v150, v134, v149, v150
	v_fma_f32 v154, v138, v153, v154
	v_fma_f32 v158, v142, v157, v158
	v_mul_f32_e32 v130, v130, v129
	v_mul_f32_e32 v134, v134, v133
	v_mul_f32_e32 v138, v138, v137
	v_mul_f32_e32 v142, v142, v141
	v_fma_f32 v147, v131, v146, v147
	v_fma_f32 v151, v135, v150, v151
	v_fma_f32 v155, v139, v154, v155
	v_fma_f32 v159, v143, v158, v159
	v_mul_f32_e32 v131, v131, v130
	v_mul_f32_e32 v135, v135, v134
	v_mul_f32_e32 v139, v139, v138
	v_mul_f32_e32 v143, v143, v142
	ds_bpermute_b32 v178, v204, v131
	ds_bpermute_b32 v182, v204, v147
	ds_bpermute_b32 v179, v204, v135
	ds_bpermute_b32 v183, v204, v151
	ds_bpermute_b32 v180, v204, v139
	ds_bpermute_b32 v184, v204, v155
	ds_bpermute_b32 v181, v204, v143
	ds_bpermute_b32 v185, v204, v159
	s_waitcnt lgkmcnt(0)
	v_fma_f32 v186, v182, v131, v147
	v_cndmask_b32_e64 v178, 1.0, v178, s[34:35]
	v_fma_f32 v187, v183, v135, v151
	v_cndmask_b32_e64 v179, 1.0, v179, s[34:35]
	v_fma_f32 v188, v184, v139, v155
	v_cndmask_b32_e64 v180, 1.0, v180, s[34:35]
	v_fma_f32 v189, v185, v143, v159
	v_cndmask_b32_e64 v181, 1.0, v181, s[34:35]
	v_cndmask_b32_e64 v223, v147, v186, s[34:35]
	v_mul_f32_e32 v219, v131, v178
	v_cndmask_b32_e64 v224, v151, v187, s[34:35]
	v_mul_f32_e32 v220, v135, v179
	v_cndmask_b32_e64 v225, v155, v188, s[34:35]
	v_mul_f32_e32 v221, v139, v180
	v_cndmask_b32_e64 v226, v159, v189, s[34:35]
	v_mul_f32_e32 v222, v143, v181
	ds_bpermute_b32 v178, v205, v219
	ds_bpermute_b32 v182, v205, v223
	ds_bpermute_b32 v179, v205, v220
	ds_bpermute_b32 v183, v205, v224
	ds_bpermute_b32 v180, v205, v221
	ds_bpermute_b32 v184, v205, v225
	ds_bpermute_b32 v181, v205, v222
	ds_bpermute_b32 v185, v205, v226
	s_waitcnt lgkmcnt(0)
	v_fma_f32 v186, v182, v219, v223
	v_cndmask_b32_e64 v178, 1.0, v178, s[36:37]
	v_fma_f32 v187, v183, v220, v224
	v_cndmask_b32_e64 v179, 1.0, v179, s[36:37]
	v_fma_f32 v188, v184, v221, v225
	v_cndmask_b32_e64 v180, 1.0, v180, s[36:37]
	v_fma_f32 v189, v185, v222, v226
	v_cndmask_b32_e64 v181, 1.0, v181, s[36:37]
	v_cndmask_b32_e64 v223, v223, v186, s[36:37]
	v_mul_f32_e32 v219, v219, v178
	v_cndmask_b32_e64 v224, v224, v187, s[36:37]
	v_mul_f32_e32 v220, v220, v179
	v_cndmask_b32_e64 v225, v225, v188, s[36:37]
	v_mul_f32_e32 v221, v221, v180
	v_cndmask_b32_e64 v226, v226, v189, s[36:37]
	v_mul_f32_e32 v222, v222, v181
	ds_bpermute_b32 v227, v204, v219
	ds_bpermute_b32 v231, v204, v223
	ds_bpermute_b32 v235, v206, v219
	ds_bpermute_b32 v239, v206, v223
	ds_bpermute_b32 v228, v204, v220
	ds_bpermute_b32 v232, v204, v224
	ds_bpermute_b32 v236, v206, v220
	ds_bpermute_b32 v244, v206, v224
	ds_bpermute_b32 v229, v204, v221
	ds_bpermute_b32 v233, v204, v225
	ds_bpermute_b32 v237, v206, v221
	ds_bpermute_b32 v245, v206, v225
	ds_bpermute_b32 v230, v204, v222
	ds_bpermute_b32 v234, v204, v226
	ds_bpermute_b32 v238, v206, v222
	ds_bpermute_b32 v246, v206, v226
	s_waitcnt lgkmcnt(0)
	v_cndmask_b32_e64 v227, 1.0, v227, s[34:35]
	v_cndmask_b32_e64 v231, 0, v231, s[34:35]
	v_cndmask_b32_e64 v228, 1.0, v228, s[34:35]
	v_cndmask_b32_e64 v232, 0, v232, s[34:35]
	v_cndmask_b32_e64 v229, 1.0, v229, s[34:35]
	v_cndmask_b32_e64 v233, 0, v233, s[34:35]
	v_cndmask_b32_e64 v230, 1.0, v230, s[34:35]
	v_cndmask_b32_e64 v234, 0, v234, s[34:35]
	v_mov_b32_e32 v190, v235
	v_mov_b32_e32 v194, v239
	v_mov_b32_e32 v198, v190
	v_mov_b32_e32 v201, v194
	v_fma_f32 v194, v194, v236, v244
	v_mul_f32_e32 v190, v190, v236
	v_mov_b32_e32 v199, v190
	v_mov_b32_e32 v177, v194
	v_fma_f32 v194, v194, v237, v245
	v_mul_f32_e32 v190, v190, v237
	v_mov_b32_e32 v200, v190
	v_mov_b32_e32 v203, v194
	v_fma_f32 v194, v194, v238, v246
	v_mul_f32_e32 v190, v190, v238
	v_mov_b32_e32 v191, v194
	ds_write_b64 v207, v[190:191] offset:1024
	s_waitcnt lgkmcnt(0)
	s_barrier
	ds_read_b64 v[178:179], v208 offset:1024
	ds_read_b64 v[180:181], v208 offset:1536
	s_waitcnt lgkmcnt(0)
	v_fma_f32 v182, v176, v178, v179
	v_cndmask_b32_e64 v183, v176, v182, s[38:39]
	v_fma_f32 v176, v182, v180, v181
	v_mov_b32_e32 v184, v183
	v_fma_f32 v185, v183, v198, v201
	v_fma_f32 v186, v183, v199, v177
	v_fma_f32 v187, v183, v200, v203
	v_fma_f32 v184, v184, v227, v231
	v_fma_f32 v185, v185, v228, v232
	v_fma_f32 v186, v186, v229, v233
	v_fma_f32 v187, v187, v230, v234
	v_fma_f32 v144, v184, v128, v144
	v_fma_f32 v148, v185, v132, v148
	v_fma_f32 v152, v186, v136, v152
	v_fma_f32 v156, v187, v140, v156
	v_fma_f32 v145, v184, v129, v145
	v_fma_f32 v149, v185, v133, v149
	v_fma_f32 v153, v186, v137, v153
	v_fma_f32 v157, v187, v141, v157
	v_fma_f32 v146, v184, v130, v146
	v_fma_f32 v150, v185, v134, v150
	v_fma_f32 v154, v186, v138, v154
	v_fma_f32 v158, v187, v142, v158
	v_fma_f32 v147, v184, v131, v147
	v_fma_f32 v151, v185, v135, v151
	v_fma_f32 v155, v186, v139, v155
	v_fma_f32 v159, v187, v143, v159
	v_cvt_pk_bf16_f32 v178, v144, v145
	v_cvt_pk_bf16_f32 v179, v146, v147
	v_cvt_pk_bf16_f32 v180, v148, v149
	v_cvt_pk_bf16_f32 v181, v150, v151
	v_cvt_pk_bf16_f32 v182, v152, v153
	v_cvt_pk_bf16_f32 v183, v154, v155
	v_cvt_pk_bf16_f32 v184, v156, v157
	v_cvt_pk_bf16_f32 v185, v158, v159
	global_store_dword v209, v178, s[44:45]
	global_store_dword v209, v179, s[44:45] offset:256
	global_store_dword v209, v180, s[44:45] offset:512
	global_store_dword v209, v181, s[44:45] offset:768
	global_store_dword v209, v182, s[44:45] offset:1024
	global_store_dword v209, v183, s[44:45] offset:1280
	global_store_dword v209, v184, s[44:45] offset:1536
	global_store_dword v209, v185, s[44:45] offset:1792
	s_add_i32 s13, s13, 1
	s_add_i32 s60, s60, -1
	s_cmp_lg_u32 s60, 0
	s_cbranch_scc1 .Lmylru_loop_0
	s_lshl_b32 s50, s10, 10
	s_lshl_b32 s51, s11, 6
	s_add_i32 s50, s50, s51
	s_lshl_b32 s51, s8, 4
	s_add_i32 s50, s50, s51
	s_add_i32 s50, s50, 512
	s_lshl_b32 s50, s50, 9
	s_add_u32 s46, s2, s50
	s_addc_u32 s47, s3, 0
	s_add_u32 s46, s46, 0x1000000
	s_addc_u32 s47, s47, 0
	s_add_u32 s48, s46, 0x20000
	s_addc_u32 s49, s47, 0
	v_lshlrev_b32_e32 v178, 9, v160
	v_lshl_add_u32 v178, v161, 4, v178
	global_load_dwordx4 v[0:3], v178, s[46:47]
	global_load_dwordx4 v[4:7], v178, s[46:47] offset:64
	global_load_dwordx4 v[8:11], v178, s[46:47] offset:128
	global_load_dwordx4 v[12:15], v178, s[46:47] offset:192
	global_load_dwordx4 v[16:19], v178, s[46:47] offset:256
	global_load_dwordx4 v[20:23], v178, s[46:47] offset:320
	global_load_dwordx4 v[24:27], v178, s[46:47] offset:384
	global_load_dwordx4 v[28:31], v178, s[46:47] offset:448
	global_load_dwordx4 v[32:35], v178, s[48:49]
	global_load_dwordx4 v[36:39], v178, s[48:49] offset:64
	global_load_dwordx4 v[40:43], v178, s[48:49] offset:128
	global_load_dwordx4 v[44:47], v178, s[48:49] offset:192
	global_load_dwordx4 v[48:51], v178, s[48:49] offset:256
	global_load_dwordx4 v[52:55], v178, s[48:49] offset:320
	global_load_dwordx4 v[56:59], v178, s[48:49] offset:384
	global_load_dwordx4 v[60:63], v178, s[48:49] offset:448
	s_load_dwordx2 s[46:47], s[0:1], 0xc8
	s_load_dwordx2 s[48:49], s[0:1], 0xd8
	s_load_dwordx2 s[40:41], s[0:1], 0xe0
	s_lshl_b32 s50, s10, 8
	s_lshl_b32 s51, s11, 6
	s_add_i32 s50, s50, s51
	s_lshl_b32 s51, s8, 4
	s_add_i32 s50, s50, s51
	v_add_u32_e32 v179, s50, v160
	v_lshlrev_b32_e32 v179, 2, v179
	s_waitcnt lgkmcnt(0)
	global_load_dword v173, v179, s[46:47]
	global_load_dword v174, v179, s[48:49]
	global_load_dword v175, v179, s[40:41]
	v_cmp_gt_u32_e64 s[34:35], 48, v202
	v_cmp_gt_u32_e64 s[36:37], 32, v202
	v_add_u32_e32 v204, 16, v202
	v_add_u32_e32 v205, 32, v202
	v_mov_b32_e32 v206, v160
	s_cmp_eq_u32 s7, 0
	s_cselect_b64 s[38:39], -1, 0
	v_and_b32_e32 v204, 63, v204
	v_lshlrev_b32_e32 v204, 2, v204
	v_and_b32_e32 v205, 63, v205
	v_lshlrev_b32_e32 v205, 2, v205
	v_and_b32_e32 v206, 63, v206
	v_lshlrev_b32_e32 v206, 2, v206
	v_mov_b32_e32 v176, 0
	s_mov_b32 s53, 0xbfb8aa3b
	s_waitcnt vmcnt(0)
	v_mul_f32_e32 v173, s53, v173
	v_mul_f32_e32 v174, s53, v174
	v_mul_f32_e32 v175, s53, v175
	v_exp_f32_e32 v175, v175
	s_nop 0
	v_add_f32_e32 v180, 1.0, v175
	v_log_f32_e32 v180, v180
	v_mov_b32_e32 v181, 0x3eaaaaab
	v_fma_f32 v181, v175, v181, -0.5
	v_fma_f32 v181, v175, v181, 1.0
	v_mul_f32_e32 v181, v175, v181
	v_mul_f32_e32 v181, 0x3fb8aa3b, v181
	v_cmp_gt_f32_e32 vcc, 0x3cf5c28f, v175
	s_nop 1
	v_cndmask_b32_e32 v175, v180, v181, vcc
	v_mul_f32_e32 v175, 0xc1000000, v175
	s_mov_b32 s13, 0
	s_barrier
	s_cmp_lt_u32 s13, 2
	s_sub_i32 s50, 1, s13
	s_lshl_b32 s50, s50, 7
	s_lshl_b32 s51, s9, 8
	s_add_i32 s51, s51, 0x8000
	s_add_i32 s51, s51, s50
	s_sub_i32 s50, 17, s13
	s_lshl_b32 s50, s50, 7
	s_lshl_b32 s59, s9, 11
	s_add_i32 s59, s59, s50
	s_cmp_lt_u32 s13, 2
	s_cselect_b32 s59, s51, s59
	s_lshl_b32 s52, s59, 11
	s_add_u32 s46, s16, s52
	s_addc_u32 s47, s17, 0
	s_lshl_b32 s52, s6, 13
	s_mov_b32 m0, s52
	s_add_i32 s52, s52, 0x400
	global_load_lds_dwordx4 v211, s[46:47]
	s_mov_b32 m0, s52
	s_add_i32 s52, s52, 0x400
	global_load_lds_dwordx4 v212, s[46:47]
	s_mov_b32 m0, s52
	s_add_i32 s52, s52, 0x400
	global_load_lds_dwordx4 v213, s[46:47]
	s_mov_b32 m0, s52
	s_add_i32 s52, s52, 0x400
	global_load_lds_dwordx4 v214, s[46:47]
	s_mov_b32 m0, s52
	s_add_i32 s52, s52, 0x400
	global_load_lds_dwordx4 v215, s[46:47]
	s_mov_b32 m0, s52
	s_add_i32 s52, s52, 0x400
	global_load_lds_dwordx4 v216, s[46:47]
	s_mov_b32 m0, s52
	s_add_i32 s52, s52, 0x400
	global_load_lds_dwordx4 v217, s[46:47]
	s_mov_b32 m0, s52
	s_nop 0
	global_load_lds_dwordx4 v218, s[46:47]
	s_waitcnt vmcnt(0)
	s_barrier
	s_cmp_eq_u32 s13, 17
	s_cbranch_scc1 .Lmylru_nodma_5
	s_add_i32 s58, s13, 1
	s_cmp_lt_u32 s58, 2
	s_sub_i32 s50, 1, s58
	s_lshl_b32 s50, s50, 7
	s_lshl_b32 s51, s9, 8
	s_add_i32 s51, s51, 0x8000
	s_add_i32 s51, s51, s50
	s_sub_i32 s50, 17, s58
	s_lshl_b32 s50, s50, 7
	s_lshl_b32 s59, s9, 11
	s_add_i32 s59, s59, s50
	s_cmp_lt_u32 s58, 2
	s_cselect_b32 s59, s51, s59
	s_lshl_b32 s52, s59, 11
	s_add_u32 s46, s16, s52
	s_addc_u32 s47, s17, 0
	s_lshl_b32 s52, s6, 13
	s_add_i32 s52, s52, 0x10000
	s_mov_b32 m0, s52
	s_add_i32 s52, s52, 0x400
	global_load_lds_dwordx4 v211, s[46:47]
	s_mov_b32 m0, s52
	s_add_i32 s52, s52, 0x400
	global_load_lds_dwordx4 v212, s[46:47]
	s_mov_b32 m0, s52
	s_add_i32 s52, s52, 0x400
	global_load_lds_dwordx4 v213, s[46:47]
	s_mov_b32 m0, s52
	s_add_i32 s52, s52, 0x400
	global_load_lds_dwordx4 v214, s[46:47]
	s_mov_b32 m0, s52
	s_add_i32 s52, s52, 0x400
	global_load_lds_dwordx4 v215, s[46:47]
	s_mov_b32 m0, s52
	s_add_i32 s52, s52, 0x400
	global_load_lds_dwordx4 v216, s[46:47]
	s_mov_b32 m0, s52
	s_add_i32 s52, s52, 0x400
	global_load_lds_dwordx4 v217, s[46:47]
	s_mov_b32 m0, s52
	s_nop 0
	global_load_lds_dwordx4 v218, s[46:47]
.Lmylru_nodma_5:
	v_mov_b32_e32 v163, v162
	ds_read_b128 v[96:99], v163
	ds_read_b128 v[100:103], v163 offset:8192
	ds_read_b128 v[104:107], v163 offset:16384
	ds_read_b128 v[108:111], v163 offset:24576
	v_xor_b32_e32 v164, 0x40, v163
	ds_read_b128 v[112:115], v164
	ds_read_b128 v[116:119], v164 offset:8192
	ds_read_b128 v[120:123], v164 offset:16384
	ds_read_b128 v[124:127], v164 offset:24576
	s_waitcnt lgkmcnt(7)
	v_mfma_f32_16x16x32_bf16 v[64:67], v[96:99], v[0:3], 0
	v_mfma_f32_16x16x32_bf16 v[68:71], v[96:99], v[32:35], 0
	v_xor_b32_e32 v164, 0x80, v163
	ds_read_b128 v[96:99], v164
	s_waitcnt lgkmcnt(7)
	v_mfma_f32_16x16x32_bf16 v[72:75], v[100:103], v[0:3], 0
	v_mfma_f32_16x16x32_bf16 v[76:79], v[100:103], v[32:35], 0
	ds_read_b128 v[100:103], v164 offset:8192
	s_waitcnt lgkmcnt(7)
	v_mfma_f32_16x16x32_bf16 v[80:83], v[104:107], v[0:3], 0
	v_mfma_f32_16x16x32_bf16 v[84:87], v[104:107], v[32:35], 0
	ds_read_b128 v[104:107], v164 offset:16384
	s_waitcnt lgkmcnt(7)
	v_mfma_f32_16x16x32_bf16 v[88:91], v[108:111], v[0:3], 0
	v_mfma_f32_16x16x32_bf16 v[92:95], v[108:111], v[32:35], 0
	ds_read_b128 v[108:111], v164 offset:24576
	s_waitcnt lgkmcnt(7)
	v_mfma_f32_16x16x32_bf16 v[64:67], v[112:115], v[4:7], v[64:67]
	v_mfma_f32_16x16x32_bf16 v[68:71], v[112:115], v[36:39], v[68:71]
	v_xor_b32_e32 v164, 0xc0, v163
	ds_read_b128 v[112:115], v164
	s_waitcnt lgkmcnt(7)
	v_mfma_f32_16x16x32_bf16 v[72:75], v[116:119], v[4:7], v[72:75]
	v_mfma_f32_16x16x32_bf16 v[76:79], v[116:119], v[36:39], v[76:79]
	ds_read_b128 v[116:119], v164 offset:8192
	s_waitcnt lgkmcnt(7)
	v_mfma_f32_16x16x32_bf16 v[80:83], v[120:123], v[4:7], v[80:83]
	v_mfma_f32_16x16x32_bf16 v[84:87], v[120:123], v[36:39], v[84:87]
	ds_read_b128 v[120:123], v164 offset:16384
	s_waitcnt lgkmcnt(7)
	v_mfma_f32_16x16x32_bf16 v[88:91], v[124:127], v[4:7], v[88:91]
	v_mfma_f32_16x16x32_bf16 v[92:95], v[124:127], v[36:39], v[92:95]
	ds_read_b128 v[124:127], v164 offset:24576
	s_waitcnt lgkmcnt(7)
	v_mfma_f32_16x16x32_bf16 v[64:67], v[96:99], v[8:11], v[64:67]
	v_mfma_f32_16x16x32_bf16 v[68:71], v[96:99], v[40:43], v[68:71]
	v_xor_b32_e32 v164, 0x100, v163
	ds_read_b128 v[96:99], v164
	s_waitcnt lgkmcnt(7)
	v_mfma_f32_16x16x32_bf16 v[72:75], v[100:103], v[8:11], v[72:75]
	v_mfma_f32_16x16x32_bf16 v[76:79], v[100:103], v[40:43], v[76:79]
	ds_read_b128 v[100:103], v164 offset:8192
	s_waitcnt lgkmcnt(7)
	v_mfma_f32_16x16x32_bf16 v[80:83], v[104:107], v[8:11], v[80:83]
	v_mfma_f32_16x16x32_bf16 v[84:87], v[104:107], v[40:43], v[84:87]
	ds_read_b128 v[104:107], v164 offset:16384
	s_waitcnt lgkmcnt(7)
	v_mfma_f32_16x16x32_bf16 v[88:91], v[108:111], v[8:11], v[88:91]
	v_mfma_f32_16x16x32_bf16 v[92:95], v[108:111], v[40:43], v[92:95]
	ds_read_b128 v[108:111], v164 offset:24576
	s_waitcnt lgkmcnt(7)
	v_mfma_f32_16x16x32_bf16 v[64:67], v[112:115], v[12:15], v[64:67]
	v_mfma_f32_16x16x32_bf16 v[68:71], v[112:115], v[44:47], v[68:71]
	v_xor_b32_e32 v164, 0x140, v163
	ds_read_b128 v[112:115], v164
	s_waitcnt lgkmcnt(7)
	v_mfma_f32_16x16x32_bf16 v[72:75], v[116:119], v[12:15], v[72:75]
	v_mfma_f32_16x16x32_bf16 v[76:79], v[116:119], v[44:47], v[76:79]
	ds_read_b128 v[116:119], v164 offset:8192
	s_waitcnt lgkmcnt(7)
	v_mfma_f32_16x16x32_bf16 v[80:83], v[120:123], v[12:15], v[80:83]
	v_mfma_f32_16x16x32_bf16 v[84:87], v[120:123], v[44:47], v[84:87]
	ds_read_b128 v[120:123], v164 offset:16384
	s_waitcnt lgkmcnt(7)
	v_mfma_f32_16x16x32_bf16 v[88:91], v[124:127], v[12:15], v[88:91]
	v_mfma_f32_16x16x32_bf16 v[92:95], v[124:127], v[44:47], v[92:95]
	ds_read_b128 v[124:127], v164 offset:24576
	s_waitcnt lgkmcnt(7)
	v_mfma_f32_16x16x32_bf16 v[64:67], v[96:99], v[16:19], v[64:67]
	v_mfma_f32_16x16x32_bf16 v[68:71], v[96:99], v[48:51], v[68:71]
	v_xor_b32_e32 v164, 0x180, v163
	ds_read_b128 v[96:99], v164
	s_waitcnt lgkmcnt(7)
	v_mfma_f32_16x16x32_bf16 v[72:75], v[100:103], v[16:19], v[72:75]
	v_mfma_f32_16x16x32_bf16 v[76:79], v[100:103], v[48:51], v[76:79]
	ds_read_b128 v[100:103], v164 offset:8192
	s_waitcnt lgkmcnt(7)
	v_mfma_f32_16x16x32_bf16 v[80:83], v[104:107], v[16:19], v[80:83]
	v_mfma_f32_16x16x32_bf16 v[84:87], v[104:107], v[48:51], v[84:87]
	ds_read_b128 v[104:107], v164 offset:16384
	s_waitcnt lgkmcnt(7)
	v_mfma_f32_16x16x32_bf16 v[88:91], v[108:111], v[16:19], v[88:91]
	v_mfma_f32_16x16x32_bf16 v[92:95], v[108:111], v[48:51], v[92:95]
	ds_read_b128 v[108:111], v164 offset:24576
	s_waitcnt lgkmcnt(7)
	v_mfma_f32_16x16x32_bf16 v[64:67], v[112:115], v[20:23], v[64:67]
	v_mfma_f32_16x16x32_bf16 v[68:71], v[112:115], v[52:55], v[68:71]
	v_xor_b32_e32 v164, 0x1c0, v163
	ds_read_b128 v[112:115], v164
	s_waitcnt lgkmcnt(7)
	v_mfma_f32_16x16x32_bf16 v[72:75], v[116:119], v[20:23], v[72:75]
	v_mfma_f32_16x16x32_bf16 v[76:79], v[116:119], v[52:55], v[76:79]
	ds_read_b128 v[116:119], v164 offset:8192
	s_waitcnt lgkmcnt(7)
	v_mfma_f32_16x16x32_bf16 v[80:83], v[120:123], v[20:23], v[80:83]
	v_mfma_f32_16x16x32_bf16 v[84:87], v[120:123], v[52:55], v[84:87]
	ds_read_b128 v[120:123], v164 offset:16384
	s_waitcnt lgkmcnt(7)
	v_mfma_f32_16x16x32_bf16 v[88:91], v[124:127], v[20:23], v[88:91]
	v_mfma_f32_16x16x32_bf16 v[92:95], v[124:127], v[52:55], v[92:95]
	ds_read_b128 v[124:127], v164 offset:24576
	s_waitcnt lgkmcnt(7)
	v_mfma_f32_16x16x32_bf16 v[64:67], v[96:99], v[24:27], v[64:67]
	v_mfma_f32_16x16x32_bf16 v[68:71], v[96:99], v[56:59], v[68:71]
	s_waitcnt lgkmcnt(6)
	v_mfma_f32_16x16x32_bf16 v[72:75], v[100:103], v[24:27], v[72:75]
	v_mfma_f32_16x16x32_bf16 v[76:79], v[100:103], v[56:59], v[76:79]
	s_waitcnt lgkmcnt(5)
	v_mfma_f32_16x16x32_bf16 v[80:83], v[104:107], v[24:27], v[80:83]
	v_mfma_f32_16x16x32_bf16 v[84:87], v[104:107], v[56:59], v[84:87]
	s_waitcnt lgkmcnt(4)
	v_mfma_f32_16x16x32_bf16 v[88:91], v[108:111], v[24:27], v[88:91]
	v_mfma_f32_16x16x32_bf16 v[92:95], v[108:111], v[56:59], v[92:95]
	s_waitcnt lgkmcnt(3)
	v_mfma_f32_16x16x32_bf16 v[64:67], v[112:115], v[28:31], v[64:67]
	v_mfma_f32_16x16x32_bf16 v[68:71], v[112:115], v[60:63], v[68:71]
	s_waitcnt lgkmcnt(2)
	v_mfma_f32_16x16x32_bf16 v[72:75], v[116:119], v[28:31], v[72:75]
	v_mfma_f32_16x16x32_bf16 v[76:79], v[116:119], v[60:63], v[76:79]
	s_waitcnt lgkmcnt(1)
	v_mfma_f32_16x16x32_bf16 v[80:83], v[120:123], v[28:31], v[80:83]
	v_mfma_f32_16x16x32_bf16 v[84:87], v[120:123], v[60:63], v[84:87]
	s_waitcnt lgkmcnt(0)
	v_mfma_f32_16x16x32_bf16 v[88:91], v[124:127], v[28:31], v[88:91]
	v_mfma_f32_16x16x32_bf16 v[92:95], v[124:127], v[60:63], v[92:95]
	v_mov_b32_e32 v169, v165
	v_mov_b32_e32 v170, v166
	v_mov_b32_e32 v171, v167
	v_mov_b32_e32 v172, v168
	ds_read_u16 v144, v169
	ds_read_u16 v145, v170
	ds_read_u16 v146, v171
	ds_read_u16 v147, v172
	ds_read_u16 v148, v169 offset:8192
	ds_read_u16 v149, v170 offset:8192
	ds_read_u16 v150, v171 offset:8192
	ds_read_u16 v151, v172 offset:8192
	ds_read_u16 v152, v169 offset:16384
	ds_read_u16 v153, v170 offset:16384
	ds_read_u16 v154, v171 offset:16384
	ds_read_u16 v155, v172 offset:16384
	ds_read_u16 v156, v169 offset:24576
	ds_read_u16 v157, v170 offset:24576
	ds_read_u16 v158, v171 offset:24576
	ds_read_u16 v159, v172 offset:24576
	s_nop 7
	v_fma_f32 v178, v64, s53, v173
	v_fma_f32 v179, v65, s53, v173
	v_fma_f32 v180, v66, s53, v173
	v_fma_f32 v181, v67, s53, v173
	v_fma_f32 v182, v72, s53, v173
	v_fma_f32 v183, v73, s53, v173
	v_fma_f32 v184, v74, s53, v173
	v_fma_f32 v185, v75, s53, v173
	v_fma_f32 v186, v68, s53, v174
	v_fma_f32 v187, v69, s53, v174
	v_fma_f32 v188, v70, s53, v174
	v_fma_f32 v189, v71, s53, v174
	v_fma_f32 v190, v76, s53, v174
	v_fma_f32 v191, v77, s53, v174
	v_fma_f32 v192, v78, s53, v174
	v_fma_f32 v193, v79, s53, v174
	v_exp_f32_e32 v178, v178
	v_exp_f32_e32 v179, v179
	v_exp_f32_e32 v180, v180
	v_exp_f32_e32 v181, v181
	v_exp_f32_e32 v182, v182
	v_exp_f32_e32 v183, v183
	v_exp_f32_e32 v184, v184
	v_exp_f32_e32 v185, v185
	v_exp_f32_e32 v186, v186
	v_exp_f32_e32 v187, v187
	v_exp_f32_e32 v188, v188
	v_exp_f32_e32 v189, v189
	v_exp_f32_e32 v190, v190
	v_exp_f32_e32 v191, v191
	v_exp_f32_e32 v192, v192
	v_exp_f32_e32 v193, v193
	v_add_f32_e32 v178, 1.0, v178
	v_add_f32_e32 v179, 1.0, v179
	v_add_f32_e32 v180, 1.0, v180
	v_add_f32_e32 v181, 1.0, v181
	v_add_f32_e32 v182, 1.0, v182
	v_add_f32_e32 v183, 1.0, v183
	v_add_f32_e32 v184, 1.0, v184
	v_add_f32_e32 v185, 1.0, v185
	v_add_f32_e32 v186, 1.0, v186
	v_add_f32_e32 v187, 1.0, v187
	v_add_f32_e32 v188, 1.0, v188
	v_add_f32_e32 v189, 1.0, v189
	v_add_f32_e32 v190, 1.0, v190
	v_add_f32_e32 v191, 1.0, v191
	v_add_f32_e32 v192, 1.0, v192
	v_add_f32_e32 v193, 1.0, v193
	v_rcp_f32_e32 v178, v178
	v_rcp_f32_e32 v179, v179
	v_rcp_f32_e32 v180, v180
	v_rcp_f32_e32 v181, v181
	v_rcp_f32_e32 v182, v182
	v_rcp_f32_e32 v183, v183
	v_rcp_f32_e32 v184, v184
	v_rcp_f32_e32 v185, v185
	v_rcp_f32_e32 v186, v186
	v_rcp_f32_e32 v187, v187
	v_rcp_f32_e32 v188, v188
	v_rcp_f32_e32 v189, v189
	v_rcp_f32_e32 v190, v190
	v_rcp_f32_e32 v191, v191
	v_rcp_f32_e32 v192, v192
	v_rcp_f32_e32 v193, v193
	v_mul_f32_e32 v178, v175, v178
	v_mul_f32_e32 v179, v175, v179
	v_mul_f32_e32 v180, v175, v180
	v_mul_f32_e32 v181, v175, v181
	v_mul_f32_e32 v182, v175, v182
	v_mul_f32_e32 v183, v175, v183
	v_mul_f32_e32 v184, v175, v184
	v_mul_f32_e32 v185, v175, v185
	v_exp_f32_e32 v128, v178
	v_exp_f32_e32 v129, v179
	v_exp_f32_e32 v130, v180
	v_exp_f32_e32 v131, v181
	v_exp_f32_e32 v132, v182
	v_exp_f32_e32 v133, v183
	v_exp_f32_e32 v134, v184
	v_exp_f32_e32 v135, v185
	s_nop 0
	v_fma_f32 v194, -v128, v128, 1.0
	v_fma_f32 v195, -v129, v129, 1.0
	v_fma_f32 v196, -v130, v130, 1.0
	v_fma_f32 v197, -v131, v131, 1.0
	v_fma_f32 v198, -v132, v132, 1.0
	v_fma_f32 v199, -v133, v133, 1.0
	v_fma_f32 v200, -v134, v134, 1.0
	v_fma_f32 v201, -v135, v135, 1.0
	v_max_f32_e32 v194, 0, v194
	v_max_f32_e32 v195, 0, v195
	v_max_f32_e32 v196, 0, v196
	v_max_f32_e32 v197, 0, v197
	v_max_f32_e32 v198, 0, v198
	v_max_f32_e32 v199, 0, v199
	v_max_f32_e32 v200, 0, v200
	v_max_f32_e32 v201, 0, v201
	v_sqrt_f32_e32 v194, v194
	v_sqrt_f32_e32 v195, v195
	v_sqrt_f32_e32 v196, v196
	v_sqrt_f32_e32 v197, v197
	v_sqrt_f32_e32 v198, v198
	v_sqrt_f32_e32 v199, v199
	v_sqrt_f32_e32 v200, v200
	v_sqrt_f32_e32 v201, v201
	s_waitcnt lgkmcnt(8)
	v_lshlrev_b32_e32 v144, 16, v144
	v_lshlrev_b32_e32 v145, 16, v145
	v_lshlrev_b32_e32 v146, 16, v146
	v_lshlrev_b32_e32 v147, 16, v147
	v_lshlrev_b32_e32 v148, 16, v148
	v_lshlrev_b32_e32 v149, 16, v149
	v_lshlrev_b32_e32 v150, 16, v150
	v_lshlrev_b32_e32 v151, 16, v151
	v_mul_f32_e32 v194, v194, v186
	v_mul_f32_e32 v195, v195, v187
	v_mul_f32_e32 v196, v196, v188
	v_mul_f32_e32 v197, v197, v189
	v_mul_f32_e32 v198, v198, v190
	v_mul_f32_e32 v199, v199, v191
	v_mul_f32_e32 v200, v200, v192
	v_mul_f32_e32 v201, v201, v193
	v_mul_f32_e32 v144, v194, v144
	v_mul_f32_e32 v145, v195, v145
	v_mul_f32_e32 v146, v196, v146
	v_mul_f32_e32 v147, v197, v147
	v_mul_f32_e32 v148, v198, v148
	v_mul_f32_e32 v149, v199, v149
	v_mul_f32_e32 v150, v200, v150
	v_mul_f32_e32 v151, v201, v151
	v_fma_f32 v178, v80, s53, v173
	v_fma_f32 v179, v81, s53, v173
	v_fma_f32 v180, v82, s53, v173
	v_fma_f32 v181, v83, s53, v173
	v_fma_f32 v182, v88, s53, v173
	v_fma_f32 v183, v89, s53, v173
	v_fma_f32 v184, v90, s53, v173
	v_fma_f32 v185, v91, s53, v173
	v_fma_f32 v186, v84, s53, v174
	v_fma_f32 v187, v85, s53, v174
	v_fma_f32 v188, v86, s53, v174
	v_fma_f32 v189, v87, s53, v174
	v_fma_f32 v190, v92, s53, v174
	v_fma_f32 v191, v93, s53, v174
	v_fma_f32 v192, v94, s53, v174
	v_fma_f32 v193, v95, s53, v174
	v_exp_f32_e32 v178, v178
	v_exp_f32_e32 v179, v179
	v_exp_f32_e32 v180, v180
	v_exp_f32_e32 v181, v181
	v_exp_f32_e32 v182, v182
	v_exp_f32_e32 v183, v183
	v_exp_f32_e32 v184, v184
	v_exp_f32_e32 v185, v185
	v_exp_f32_e32 v186, v186
	v_exp_f32_e32 v187, v187
	v_exp_f32_e32 v188, v188
	v_exp_f32_e32 v189, v189
	v_exp_f32_e32 v190, v190
	v_exp_f32_e32 v191, v191
	v_exp_f32_e32 v192, v192
	v_exp_f32_e32 v193, v193
	v_add_f32_e32 v178, 1.0, v178
	v_add_f32_e32 v179, 1.0, v179
	v_add_f32_e32 v180, 1.0, v180
	v_add_f32_e32 v181, 1.0, v181
	v_add_f32_e32 v182, 1.0, v182
	v_add_f32_e32 v183, 1.0, v183
	v_add_f32_e32 v184, 1.0, v184
	v_add_f32_e32 v185, 1.0, v185
	v_add_f32_e32 v186, 1.0, v186
	v_add_f32_e32 v187, 1.0, v187
	v_add_f32_e32 v188, 1.0, v188
	v_add_f32_e32 v189, 1.0, v189
	v_add_f32_e32 v190, 1.0, v190
	v_add_f32_e32 v191, 1.0, v191
	v_add_f32_e32 v192, 1.0, v192
	v_add_f32_e32 v193, 1.0, v193
	v_rcp_f32_e32 v178, v178
	v_rcp_f32_e32 v179, v179
	v_rcp_f32_e32 v180, v180
	v_rcp_f32_e32 v181, v181
	v_rcp_f32_e32 v182, v182
	v_rcp_f32_e32 v183, v183
	v_rcp_f32_e32 v184, v184
	v_rcp_f32_e32 v185, v185
	v_rcp_f32_e32 v186, v186
	v_rcp_f32_e32 v187, v187
	v_rcp_f32_e32 v188, v188
	v_rcp_f32_e32 v189, v189
	v_rcp_f32_e32 v190, v190
	v_rcp_f32_e32 v191, v191
	v_rcp_f32_e32 v192, v192
	v_rcp_f32_e32 v193, v193
	v_mul_f32_e32 v178, v175, v178
	v_mul_f32_e32 v179, v175, v179
	v_mul_f32_e32 v180, v175, v180
	v_mul_f32_e32 v181, v175, v181
	v_mul_f32_e32 v182, v175, v182
	v_mul_f32_e32 v183, v175, v183
	v_mul_f32_e32 v184, v175, v184
	v_mul_f32_e32 v185, v175, v185
	v_exp_f32_e32 v136, v178
	v_exp_f32_e32 v137, v179
	v_exp_f32_e32 v138, v180
	v_exp_f32_e32 v139, v181
	v_exp_f32_e32 v140, v182
	v_exp_f32_e32 v141, v183
	v_exp_f32_e32 v142, v184
	v_exp_f32_e32 v143, v185
	s_nop 0
	v_fma_f32 v194, -v136, v136, 1.0
	v_fma_f32 v195, -v137, v137, 1.0
	v_fma_f32 v196, -v138, v138, 1.0
	v_fma_f32 v197, -v139, v139, 1.0
	v_fma_f32 v198, -v140, v140, 1.0
	v_fma_f32 v199, -v141, v141, 1.0
	v_fma_f32 v200, -v142, v142, 1.0
	v_fma_f32 v201, -v143, v143, 1.0
	v_max_f32_e32 v194, 0, v194
	v_max_f32_e32 v195, 0, v195
	v_max_f32_e32 v196, 0, v196
	v_max_f32_e32 v197, 0, v197
	v_max_f32_e32 v198, 0, v198
	v_max_f32_e32 v199, 0, v199
	v_max_f32_e32 v200, 0, v200
	v_max_f32_e32 v201, 0, v201
	v_sqrt_f32_e32 v194, v194
	v_sqrt_f32_e32 v195, v195
	v_sqrt_f32_e32 v196, v196
	v_sqrt_f32_e32 v197, v197
	v_sqrt_f32_e32 v198, v198
	v_sqrt_f32_e32 v199, v199
	v_sqrt_f32_e32 v200, v200
	v_sqrt_f32_e32 v201, v201
	s_waitcnt lgkmcnt(0)
	v_lshlrev_b32_e32 v152, 16, v152
	v_lshlrev_b32_e32 v153, 16, v153
	v_lshlrev_b32_e32 v154, 16, v154
	v_lshlrev_b32_e32 v155, 16, v155
	v_lshlrev_b32_e32 v156, 16, v156
	v_lshlrev_b32_e32 v157, 16, v157
	v_lshlrev_b32_e32 v158, 16, v158
	v_lshlrev_b32_e32 v159, 16, v159
	v_mul_f32_e32 v194, v194, v186
	v_mul_f32_e32 v195, v195, v187
	v_mul_f32_e32 v196, v196, v188
	v_mul_f32_e32 v197, v197, v189
	v_mul_f32_e32 v198, v198, v190
	v_mul_f32_e32 v199, v199, v191
	v_mul_f32_e32 v200, v200, v192
	v_mul_f32_e32 v201, v201, v193
	v_mul_f32_e32 v152, v194, v152
	v_mul_f32_e32 v153, v195, v153
	v_mul_f32_e32 v154, v196, v154
	v_mul_f32_e32 v155, v197, v155
	v_mul_f32_e32 v156, v198, v156
	v_mul_f32_e32 v157, v199, v157
	v_mul_f32_e32 v158, v200, v158
	v_mul_f32_e32 v159, v201, v159
	v_fma_f32 v146, v130, v147, v146
	v_fma_f32 v150, v134, v151, v150
	v_fma_f32 v154, v138, v155, v154
	v_fma_f32 v158, v142, v159, v158
	v_mul_f32_e32 v130, v130, v131
	v_mul_f32_e32 v134, v134, v135
	v_mul_f32_e32 v138, v138, v139
	v_mul_f32_e32 v142, v142, v143
	v_fma_f32 v145, v129, v146, v145
	v_fma_f32 v149, v133, v150, v149
	v_fma_f32 v153, v137, v154, v153
	v_fma_f32 v157, v141, v158, v157
	v_mul_f32_e32 v129, v129, v130
	v_mul_f32_e32 v133, v133, v134
	v_mul_f32_e32 v137, v137, v138
	v_mul_f32_e32 v141, v141, v142
	v_fma_f32 v144, v128, v145, v144
	v_fma_f32 v148, v132, v149, v148
	v_fma_f32 v152, v136, v153, v152
	v_fma_f32 v156, v140, v157, v156
	v_mul_f32_e32 v128, v128, v129
	v_mul_f32_e32 v132, v132, v133
	v_mul_f32_e32 v136, v136, v137
	v_mul_f32_e32 v140, v140, v141
	ds_bpermute_b32 v178, v204, v128
	ds_bpermute_b32 v182, v204, v144
	ds_bpermute_b32 v179, v204, v132
	ds_bpermute_b32 v183, v204, v148
	ds_bpermute_b32 v180, v204, v136
	ds_bpermute_b32 v184, v204, v152
	ds_bpermute_b32 v181, v204, v140
	ds_bpermute_b32 v185, v204, v156
	s_waitcnt lgkmcnt(0)
	v_fma_f32 v186, v182, v128, v144
	v_cndmask_b32_e64 v178, 1.0, v178, s[34:35]
	v_fma_f32 v187, v183, v132, v148
	v_cndmask_b32_e64 v179, 1.0, v179, s[34:35]
	v_fma_f32 v188, v184, v136, v152
	v_cndmask_b32_e64 v180, 1.0, v180, s[34:35]
	v_fma_f32 v189, v185, v140, v156
	v_cndmask_b32_e64 v181, 1.0, v181, s[34:35]
	v_cndmask_b32_e64 v223, v144, v186, s[34:35]
	v_mul_f32_e32 v219, v128, v178
	v_cndmask_b32_e64 v224, v148, v187, s[34:35]
	v_mul_f32_e32 v220, v132, v179
	v_cndmask_b32_e64 v225, v152, v188, s[34:35]
	v_mul_f32_e32 v221, v136, v180
	v_cndmask_b32_e64 v226, v156, v189, s[34:35]
	v_mul_f32_e32 v222, v140, v181
	ds_bpermute_b32 v178, v205, v219
	ds_bpermute_b32 v182, v205, v223
	ds_bpermute_b32 v179, v205, v220
	ds_bpermute_b32 v183, v205, v224
	ds_bpermute_b32 v180, v205, v221
	ds_bpermute_b32 v184, v205, v225
	ds_bpermute_b32 v181, v205, v222
	ds_bpermute_b32 v185, v205, v226
	s_waitcnt lgkmcnt(0)
	v_fma_f32 v186, v182, v219, v223
	v_cndmask_b32_e64 v178, 1.0, v178, s[36:37]
	v_fma_f32 v187, v183, v220, v224
	v_cndmask_b32_e64 v179, 1.0, v179, s[36:37]
	v_fma_f32 v188, v184, v221, v225
	v_cndmask_b32_e64 v180, 1.0, v180, s[36:37]
	v_fma_f32 v189, v185, v222, v226
	v_cndmask_b32_e64 v181, 1.0, v181, s[36:37]
	v_cndmask_b32_e64 v223, v223, v186, s[36:37]
	v_mul_f32_e32 v219, v219, v178
	v_cndmask_b32_e64 v224, v224, v187, s[36:37]
	v_mul_f32_e32 v220, v220, v179
	v_cndmask_b32_e64 v225, v225, v188, s[36:37]
	v_mul_f32_e32 v221, v221, v180
	v_cndmask_b32_e64 v226, v226, v189, s[36:37]
	v_mul_f32_e32 v222, v222, v181
	ds_bpermute_b32 v227, v204, v219
	ds_bpermute_b32 v231, v204, v223
	ds_bpermute_b32 v235, v206, v219
	ds_bpermute_b32 v239, v206, v223
	ds_bpermute_b32 v228, v204, v220
	ds_bpermute_b32 v232, v204, v224
	ds_bpermute_b32 v236, v206, v220
	ds_bpermute_b32 v244, v206, v224
	ds_bpermute_b32 v229, v204, v221
	ds_bpermute_b32 v233, v204, v225
	ds_bpermute_b32 v237, v206, v221
	ds_bpermute_b32 v245, v206, v225
	ds_bpermute_b32 v230, v204, v222
	ds_bpermute_b32 v234, v204, v226
	ds_bpermute_b32 v238, v206, v222
	ds_bpermute_b32 v246, v206, v226
	s_waitcnt lgkmcnt(0)
	v_cndmask_b32_e64 v227, 1.0, v227, s[34:35]
	v_cndmask_b32_e64 v231, 0, v231, s[34:35]
	v_cndmask_b32_e64 v228, 1.0, v228, s[34:35]
	v_cndmask_b32_e64 v232, 0, v232, s[34:35]
	v_cndmask_b32_e64 v229, 1.0, v229, s[34:35]
	v_cndmask_b32_e64 v233, 0, v233, s[34:35]
	v_cndmask_b32_e64 v230, 1.0, v230, s[34:35]
	v_cndmask_b32_e64 v234, 0, v234, s[34:35]
	v_mov_b32_e32 v190, v238
	v_mov_b32_e32 v194, v246
	v_mov_b32_e32 v198, v190
	v_mov_b32_e32 v201, v194
	v_fma_f32 v194, v194, v237, v245
	v_mul_f32_e32 v190, v190, v237
	v_mov_b32_e32 v199, v190
	v_mov_b32_e32 v177, v194
	v_fma_f32 v194, v194, v236, v244
	v_mul_f32_e32 v190, v190, v236
	v_mov_b32_e32 v200, v190
	v_mov_b32_e32 v203, v194
	v_fma_f32 v194, v194, v235, v239
	v_mul_f32_e32 v190, v190, v235
	v_mov_b32_e32 v191, v194
	ds_write_b64 v207, v[190:191]
	s_waitcnt lgkmcnt(0)
	s_barrier
	ds_read_b64 v[178:179], v208 offset:512
	ds_read_b64 v[180:181], v208
	s_waitcnt lgkmcnt(0)
	v_fma_f32 v182, v176, v178, v179
	v_cndmask_b32_e64 v183, v176, v182, s[38:39]
	v_fma_f32 v176, v182, v180, v181
	s_add_i32 s13, s13, 1
	s_waitcnt vmcnt(0)
	s_barrier
	s_cmp_eq_u32 s13, 17
	s_cbranch_scc1 .Lmylru_nodma_6
	s_add_i32 s58, s13, 1
	s_cmp_lt_u32 s58, 2
	s_sub_i32 s50, 1, s58
	s_lshl_b32 s50, s50, 7
	s_lshl_b32 s51, s9, 8
	s_add_i32 s51, s51, 0x8000
	s_add_i32 s51, s51, s50
	s_sub_i32 s50, 17, s58
	s_lshl_b32 s50, s50, 7
	s_lshl_b32 s59, s9, 11
	s_add_i32 s59, s59, s50
	s_cmp_lt_u32 s58, 2
	s_cselect_b32 s59, s51, s59
	s_lshl_b32 s52, s59, 11
	s_add_u32 s46, s16, s52
	s_addc_u32 s47, s17, 0
	s_lshl_b32 s52, s6, 13
	s_mov_b32 m0, s52
	s_add_i32 s52, s52, 0x400
	global_load_lds_dwordx4 v211, s[46:47]
	s_mov_b32 m0, s52
	s_add_i32 s52, s52, 0x400
	global_load_lds_dwordx4 v212, s[46:47]
	s_mov_b32 m0, s52
	s_add_i32 s52, s52, 0x400
	global_load_lds_dwordx4 v213, s[46:47]
	s_mov_b32 m0, s52
	s_add_i32 s52, s52, 0x400
	global_load_lds_dwordx4 v214, s[46:47]
	s_mov_b32 m0, s52
	s_add_i32 s52, s52, 0x400
	global_load_lds_dwordx4 v215, s[46:47]
	s_mov_b32 m0, s52
	s_add_i32 s52, s52, 0x400
	global_load_lds_dwordx4 v216, s[46:47]
	s_mov_b32 m0, s52
	s_add_i32 s52, s52, 0x400
	global_load_lds_dwordx4 v217, s[46:47]
	s_mov_b32 m0, s52
	s_nop 0
	global_load_lds_dwordx4 v218, s[46:47]
.Lmylru_nodma_6:
	v_or_b32_e32 v163, 0x10000, v162
	ds_read_b128 v[96:99], v163
	ds_read_b128 v[100:103], v163 offset:8192
	ds_read_b128 v[104:107], v163 offset:16384
	ds_read_b128 v[108:111], v163 offset:24576
	v_xor_b32_e32 v164, 0x40, v163
	ds_read_b128 v[112:115], v164
	ds_read_b128 v[116:119], v164 offset:8192
	ds_read_b128 v[120:123], v164 offset:16384
	ds_read_b128 v[124:127], v164 offset:24576
	s_waitcnt lgkmcnt(7)
	v_mfma_f32_16x16x32_bf16 v[64:67], v[96:99], v[0:3], 0
	v_mfma_f32_16x16x32_bf16 v[68:71], v[96:99], v[32:35], 0
	v_xor_b32_e32 v164, 0x80, v163
	ds_read_b128 v[96:99], v164
	s_waitcnt lgkmcnt(7)
	v_mfma_f32_16x16x32_bf16 v[72:75], v[100:103], v[0:3], 0
	v_mfma_f32_16x16x32_bf16 v[76:79], v[100:103], v[32:35], 0
	ds_read_b128 v[100:103], v164 offset:8192
	s_waitcnt lgkmcnt(7)
	v_mfma_f32_16x16x32_bf16 v[80:83], v[104:107], v[0:3], 0
	v_mfma_f32_16x16x32_bf16 v[84:87], v[104:107], v[32:35], 0
	ds_read_b128 v[104:107], v164 offset:16384
	s_waitcnt lgkmcnt(7)
	v_mfma_f32_16x16x32_bf16 v[88:91], v[108:111], v[0:3], 0
	v_mfma_f32_16x16x32_bf16 v[92:95], v[108:111], v[32:35], 0
	ds_read_b128 v[108:111], v164 offset:24576
	s_waitcnt lgkmcnt(7)
	v_mfma_f32_16x16x32_bf16 v[64:67], v[112:115], v[4:7], v[64:67]
	v_mfma_f32_16x16x32_bf16 v[68:71], v[112:115], v[36:39], v[68:71]
	v_xor_b32_e32 v164, 0xc0, v163
	ds_read_b128 v[112:115], v164
	s_waitcnt lgkmcnt(7)
	v_mfma_f32_16x16x32_bf16 v[72:75], v[116:119], v[4:7], v[72:75]
	v_mfma_f32_16x16x32_bf16 v[76:79], v[116:119], v[36:39], v[76:79]
	ds_read_b128 v[116:119], v164 offset:8192
	s_waitcnt lgkmcnt(7)
	v_mfma_f32_16x16x32_bf16 v[80:83], v[120:123], v[4:7], v[80:83]
	v_mfma_f32_16x16x32_bf16 v[84:87], v[120:123], v[36:39], v[84:87]
	ds_read_b128 v[120:123], v164 offset:16384
	s_waitcnt lgkmcnt(7)
	v_mfma_f32_16x16x32_bf16 v[88:91], v[124:127], v[4:7], v[88:91]
	v_mfma_f32_16x16x32_bf16 v[92:95], v[124:127], v[36:39], v[92:95]
	ds_read_b128 v[124:127], v164 offset:24576
	s_waitcnt lgkmcnt(7)
	v_mfma_f32_16x16x32_bf16 v[64:67], v[96:99], v[8:11], v[64:67]
	v_mfma_f32_16x16x32_bf16 v[68:71], v[96:99], v[40:43], v[68:71]
	v_xor_b32_e32 v164, 0x100, v163
	ds_read_b128 v[96:99], v164
	s_waitcnt lgkmcnt(7)
	v_mfma_f32_16x16x32_bf16 v[72:75], v[100:103], v[8:11], v[72:75]
	v_mfma_f32_16x16x32_bf16 v[76:79], v[100:103], v[40:43], v[76:79]
	ds_read_b128 v[100:103], v164 offset:8192
	s_waitcnt lgkmcnt(7)
	v_mfma_f32_16x16x32_bf16 v[80:83], v[104:107], v[8:11], v[80:83]
	v_mfma_f32_16x16x32_bf16 v[84:87], v[104:107], v[40:43], v[84:87]
	ds_read_b128 v[104:107], v164 offset:16384
	s_waitcnt lgkmcnt(7)
	v_mfma_f32_16x16x32_bf16 v[88:91], v[108:111], v[8:11], v[88:91]
	v_mfma_f32_16x16x32_bf16 v[92:95], v[108:111], v[40:43], v[92:95]
	ds_read_b128 v[108:111], v164 offset:24576
	s_waitcnt lgkmcnt(7)
	v_mfma_f32_16x16x32_bf16 v[64:67], v[112:115], v[12:15], v[64:67]
	v_mfma_f32_16x16x32_bf16 v[68:71], v[112:115], v[44:47], v[68:71]
	v_xor_b32_e32 v164, 0x140, v163
	ds_read_b128 v[112:115], v164
	s_waitcnt lgkmcnt(7)
	v_mfma_f32_16x16x32_bf16 v[72:75], v[116:119], v[12:15], v[72:75]
	v_mfma_f32_16x16x32_bf16 v[76:79], v[116:119], v[44:47], v[76:79]
	ds_read_b128 v[116:119], v164 offset:8192
	s_waitcnt lgkmcnt(7)
	v_mfma_f32_16x16x32_bf16 v[80:83], v[120:123], v[12:15], v[80:83]
	v_mfma_f32_16x16x32_bf16 v[84:87], v[120:123], v[44:47], v[84:87]
	ds_read_b128 v[120:123], v164 offset:16384
	s_waitcnt lgkmcnt(7)
	v_mfma_f32_16x16x32_bf16 v[88:91], v[124:127], v[12:15], v[88:91]
	v_mfma_f32_16x16x32_bf16 v[92:95], v[124:127], v[44:47], v[92:95]
	ds_read_b128 v[124:127], v164 offset:24576
	s_waitcnt lgkmcnt(7)
	v_mfma_f32_16x16x32_bf16 v[64:67], v[96:99], v[16:19], v[64:67]
	v_mfma_f32_16x16x32_bf16 v[68:71], v[96:99], v[48:51], v[68:71]
	v_xor_b32_e32 v164, 0x180, v163
	ds_read_b128 v[96:99], v164
	s_waitcnt lgkmcnt(7)
	v_mfma_f32_16x16x32_bf16 v[72:75], v[100:103], v[16:19], v[72:75]
	v_mfma_f32_16x16x32_bf16 v[76:79], v[100:103], v[48:51], v[76:79]
	ds_read_b128 v[100:103], v164 offset:8192
	s_waitcnt lgkmcnt(7)
	v_mfma_f32_16x16x32_bf16 v[80:83], v[104:107], v[16:19], v[80:83]
	v_mfma_f32_16x16x32_bf16 v[84:87], v[104:107], v[48:51], v[84:87]
	ds_read_b128 v[104:107], v164 offset:16384
	s_waitcnt lgkmcnt(7)
	v_mfma_f32_16x16x32_bf16 v[88:91], v[108:111], v[16:19], v[88:91]
	v_mfma_f32_16x16x32_bf16 v[92:95], v[108:111], v[48:51], v[92:95]
	ds_read_b128 v[108:111], v164 offset:24576
	s_waitcnt lgkmcnt(7)
	v_mfma_f32_16x16x32_bf16 v[64:67], v[112:115], v[20:23], v[64:67]
	v_mfma_f32_16x16x32_bf16 v[68:71], v[112:115], v[52:55], v[68:71]
	v_xor_b32_e32 v164, 0x1c0, v163
	ds_read_b128 v[112:115], v164
	s_waitcnt lgkmcnt(7)
	v_mfma_f32_16x16x32_bf16 v[72:75], v[116:119], v[20:23], v[72:75]
	v_mfma_f32_16x16x32_bf16 v[76:79], v[116:119], v[52:55], v[76:79]
	ds_read_b128 v[116:119], v164 offset:8192
	s_waitcnt lgkmcnt(7)
	v_mfma_f32_16x16x32_bf16 v[80:83], v[120:123], v[20:23], v[80:83]
	v_mfma_f32_16x16x32_bf16 v[84:87], v[120:123], v[52:55], v[84:87]
	ds_read_b128 v[120:123], v164 offset:16384
	s_waitcnt lgkmcnt(7)
	v_mfma_f32_16x16x32_bf16 v[88:91], v[124:127], v[20:23], v[88:91]
	v_mfma_f32_16x16x32_bf16 v[92:95], v[124:127], v[52:55], v[92:95]
	ds_read_b128 v[124:127], v164 offset:24576
	s_waitcnt lgkmcnt(7)
	v_mfma_f32_16x16x32_bf16 v[64:67], v[96:99], v[24:27], v[64:67]
	v_mfma_f32_16x16x32_bf16 v[68:71], v[96:99], v[56:59], v[68:71]
	s_waitcnt lgkmcnt(6)
	v_mfma_f32_16x16x32_bf16 v[72:75], v[100:103], v[24:27], v[72:75]
	v_mfma_f32_16x16x32_bf16 v[76:79], v[100:103], v[56:59], v[76:79]
	s_waitcnt lgkmcnt(5)
	v_mfma_f32_16x16x32_bf16 v[80:83], v[104:107], v[24:27], v[80:83]
	v_mfma_f32_16x16x32_bf16 v[84:87], v[104:107], v[56:59], v[84:87]
	s_waitcnt lgkmcnt(4)
	v_mfma_f32_16x16x32_bf16 v[88:91], v[108:111], v[24:27], v[88:91]
	v_mfma_f32_16x16x32_bf16 v[92:95], v[108:111], v[56:59], v[92:95]
	s_waitcnt lgkmcnt(3)
	v_mfma_f32_16x16x32_bf16 v[64:67], v[112:115], v[28:31], v[64:67]
	v_mfma_f32_16x16x32_bf16 v[68:71], v[112:115], v[60:63], v[68:71]
	s_waitcnt lgkmcnt(2)
	v_mfma_f32_16x16x32_bf16 v[72:75], v[116:119], v[28:31], v[72:75]
	v_mfma_f32_16x16x32_bf16 v[76:79], v[116:119], v[60:63], v[76:79]
	s_waitcnt lgkmcnt(1)
	v_mfma_f32_16x16x32_bf16 v[80:83], v[120:123], v[28:31], v[80:83]
	v_mfma_f32_16x16x32_bf16 v[84:87], v[120:123], v[60:63], v[84:87]
	s_waitcnt lgkmcnt(0)
	v_mfma_f32_16x16x32_bf16 v[88:91], v[124:127], v[28:31], v[88:91]
	v_mfma_f32_16x16x32_bf16 v[92:95], v[124:127], v[60:63], v[92:95]
	v_or_b32_e32 v169, 0x10000, v165
	v_or_b32_e32 v170, 0x10000, v166
	v_or_b32_e32 v171, 0x10000, v167
	v_or_b32_e32 v172, 0x10000, v168
	ds_read_u16 v144, v169
	ds_read_u16 v145, v170
	ds_read_u16 v146, v171
	ds_read_u16 v147, v172
	ds_read_u16 v148, v169 offset:8192
	ds_read_u16 v149, v170 offset:8192
	ds_read_u16 v150, v171 offset:8192
	ds_read_u16 v151, v172 offset:8192
	ds_read_u16 v152, v169 offset:16384
	ds_read_u16 v153, v170 offset:16384
	ds_read_u16 v154, v171 offset:16384
	ds_read_u16 v155, v172 offset:16384
	ds_read_u16 v156, v169 offset:24576
	ds_read_u16 v157, v170 offset:24576
	ds_read_u16 v158, v171 offset:24576
	ds_read_u16 v159, v172 offset:24576
	s_nop 7
	v_fma_f32 v178, v64, s53, v173
	v_fma_f32 v179, v65, s53, v173
	v_fma_f32 v180, v66, s53, v173
	v_fma_f32 v181, v67, s53, v173
	v_fma_f32 v182, v72, s53, v173
	v_fma_f32 v183, v73, s53, v173
	v_fma_f32 v184, v74, s53, v173
	v_fma_f32 v185, v75, s53, v173
	v_fma_f32 v186, v68, s53, v174
	v_fma_f32 v187, v69, s53, v174
	v_fma_f32 v188, v70, s53, v174
	v_fma_f32 v189, v71, s53, v174
	v_fma_f32 v190, v76, s53, v174
	v_fma_f32 v191, v77, s53, v174
	v_fma_f32 v192, v78, s53, v174
	v_fma_f32 v193, v79, s53, v174
	v_exp_f32_e32 v178, v178
	v_exp_f32_e32 v179, v179
	v_exp_f32_e32 v180, v180
	v_exp_f32_e32 v181, v181
	v_exp_f32_e32 v182, v182
	v_exp_f32_e32 v183, v183
	v_exp_f32_e32 v184, v184
	v_exp_f32_e32 v185, v185
	v_exp_f32_e32 v186, v186
	v_exp_f32_e32 v187, v187
	v_exp_f32_e32 v188, v188
	v_exp_f32_e32 v189, v189
	v_exp_f32_e32 v190, v190
	v_exp_f32_e32 v191, v191
	v_exp_f32_e32 v192, v192
	v_exp_f32_e32 v193, v193
	v_add_f32_e32 v178, 1.0, v178
	v_add_f32_e32 v179, 1.0, v179
	v_add_f32_e32 v180, 1.0, v180
	v_add_f32_e32 v181, 1.0, v181
	v_add_f32_e32 v182, 1.0, v182
	v_add_f32_e32 v183, 1.0, v183
	v_add_f32_e32 v184, 1.0, v184
	v_add_f32_e32 v185, 1.0, v185
	v_add_f32_e32 v186, 1.0, v186
	v_add_f32_e32 v187, 1.0, v187
	v_add_f32_e32 v188, 1.0, v188
	v_add_f32_e32 v189, 1.0, v189
	v_add_f32_e32 v190, 1.0, v190
	v_add_f32_e32 v191, 1.0, v191
	v_add_f32_e32 v192, 1.0, v192
	v_add_f32_e32 v193, 1.0, v193
	v_rcp_f32_e32 v178, v178
	v_rcp_f32_e32 v179, v179
	v_rcp_f32_e32 v180, v180
	v_rcp_f32_e32 v181, v181
	v_rcp_f32_e32 v182, v182
	v_rcp_f32_e32 v183, v183
	v_rcp_f32_e32 v184, v184
	v_rcp_f32_e32 v185, v185
	v_rcp_f32_e32 v186, v186
	v_rcp_f32_e32 v187, v187
	v_rcp_f32_e32 v188, v188
	v_rcp_f32_e32 v189, v189
	v_rcp_f32_e32 v190, v190
	v_rcp_f32_e32 v191, v191
	v_rcp_f32_e32 v192, v192
	v_rcp_f32_e32 v193, v193
	v_mul_f32_e32 v178, v175, v178
	v_mul_f32_e32 v179, v175, v179
	v_mul_f32_e32 v180, v175, v180
	v_mul_f32_e32 v181, v175, v181
	v_mul_f32_e32 v182, v175, v182
	v_mul_f32_e32 v183, v175, v183
	v_mul_f32_e32 v184, v175, v184
	v_mul_f32_e32 v185, v175, v185
	v_exp_f32_e32 v128, v178
	v_exp_f32_e32 v129, v179
	v_exp_f32_e32 v130, v180
	v_exp_f32_e32 v131, v181
	v_exp_f32_e32 v132, v182
	v_exp_f32_e32 v133, v183
	v_exp_f32_e32 v134, v184
	v_exp_f32_e32 v135, v185
	s_nop 0
	v_fma_f32 v194, -v128, v128, 1.0
	v_fma_f32 v195, -v129, v129, 1.0
	v_fma_f32 v196, -v130, v130, 1.0
	v_fma_f32 v197, -v131, v131, 1.0
	v_fma_f32 v198, -v132, v132, 1.0
	v_fma_f32 v199, -v133, v133, 1.0
	v_fma_f32 v200, -v134, v134, 1.0
	v_fma_f32 v201, -v135, v135, 1.0
	v_max_f32_e32 v194, 0, v194
	v_max_f32_e32 v195, 0, v195
	v_max_f32_e32 v196, 0, v196
	v_max_f32_e32 v197, 0, v197
	v_max_f32_e32 v198, 0, v198
	v_max_f32_e32 v199, 0, v199
	v_max_f32_e32 v200, 0, v200
	v_max_f32_e32 v201, 0, v201
	v_sqrt_f32_e32 v194, v194
	v_sqrt_f32_e32 v195, v195
	v_sqrt_f32_e32 v196, v196
	v_sqrt_f32_e32 v197, v197
	v_sqrt_f32_e32 v198, v198
	v_sqrt_f32_e32 v199, v199
	v_sqrt_f32_e32 v200, v200
	v_sqrt_f32_e32 v201, v201
	s_waitcnt lgkmcnt(8)
	v_lshlrev_b32_e32 v144, 16, v144
	v_lshlrev_b32_e32 v145, 16, v145
	v_lshlrev_b32_e32 v146, 16, v146
	v_lshlrev_b32_e32 v147, 16, v147
	v_lshlrev_b32_e32 v148, 16, v148
	v_lshlrev_b32_e32 v149, 16, v149
	v_lshlrev_b32_e32 v150, 16, v150
	v_lshlrev_b32_e32 v151, 16, v151
	v_mul_f32_e32 v194, v194, v186
	v_mul_f32_e32 v195, v195, v187
	v_mul_f32_e32 v196, v196, v188
	v_mul_f32_e32 v197, v197, v189
	v_mul_f32_e32 v198, v198, v190
	v_mul_f32_e32 v199, v199, v191
	v_mul_f32_e32 v200, v200, v192
	v_mul_f32_e32 v201, v201, v193
	v_mul_f32_e32 v144, v194, v144
	v_mul_f32_e32 v145, v195, v145
	v_mul_f32_e32 v146, v196, v146
	v_mul_f32_e32 v147, v197, v147
	v_mul_f32_e32 v148, v198, v148
	v_mul_f32_e32 v149, v199, v149
	v_mul_f32_e32 v150, v200, v150
	v_mul_f32_e32 v151, v201, v151
	v_fma_f32 v178, v80, s53, v173
	v_fma_f32 v179, v81, s53, v173
	v_fma_f32 v180, v82, s53, v173
	v_fma_f32 v181, v83, s53, v173
	v_fma_f32 v182, v88, s53, v173
	v_fma_f32 v183, v89, s53, v173
	v_fma_f32 v184, v90, s53, v173
	v_fma_f32 v185, v91, s53, v173
	v_fma_f32 v186, v84, s53, v174
	v_fma_f32 v187, v85, s53, v174
	v_fma_f32 v188, v86, s53, v174
	v_fma_f32 v189, v87, s53, v174
	v_fma_f32 v190, v92, s53, v174
	v_fma_f32 v191, v93, s53, v174
	v_fma_f32 v192, v94, s53, v174
	v_fma_f32 v193, v95, s53, v174
	v_exp_f32_e32 v178, v178
	v_exp_f32_e32 v179, v179
	v_exp_f32_e32 v180, v180
	v_exp_f32_e32 v181, v181
	v_exp_f32_e32 v182, v182
	v_exp_f32_e32 v183, v183
	v_exp_f32_e32 v184, v184
	v_exp_f32_e32 v185, v185
	v_exp_f32_e32 v186, v186
	v_exp_f32_e32 v187, v187
	v_exp_f32_e32 v188, v188
	v_exp_f32_e32 v189, v189
	v_exp_f32_e32 v190, v190
	v_exp_f32_e32 v191, v191
	v_exp_f32_e32 v192, v192
	v_exp_f32_e32 v193, v193
	v_add_f32_e32 v178, 1.0, v178
	v_add_f32_e32 v179, 1.0, v179
	v_add_f32_e32 v180, 1.0, v180
	v_add_f32_e32 v181, 1.0, v181
	v_add_f32_e32 v182, 1.0, v182
	v_add_f32_e32 v183, 1.0, v183
	v_add_f32_e32 v184, 1.0, v184
	v_add_f32_e32 v185, 1.0, v185
	v_add_f32_e32 v186, 1.0, v186
	v_add_f32_e32 v187, 1.0, v187
	v_add_f32_e32 v188, 1.0, v188
	v_add_f32_e32 v189, 1.0, v189
	v_add_f32_e32 v190, 1.0, v190
	v_add_f32_e32 v191, 1.0, v191
	v_add_f32_e32 v192, 1.0, v192
	v_add_f32_e32 v193, 1.0, v193
	v_rcp_f32_e32 v178, v178
	v_rcp_f32_e32 v179, v179
	v_rcp_f32_e32 v180, v180
	v_rcp_f32_e32 v181, v181
	v_rcp_f32_e32 v182, v182
	v_rcp_f32_e32 v183, v183
	v_rcp_f32_e32 v184, v184
	v_rcp_f32_e32 v185, v185
	v_rcp_f32_e32 v186, v186
	v_rcp_f32_e32 v187, v187
	v_rcp_f32_e32 v188, v188
	v_rcp_f32_e32 v189, v189
	v_rcp_f32_e32 v190, v190
	v_rcp_f32_e32 v191, v191
	v_rcp_f32_e32 v192, v192
	v_rcp_f32_e32 v193, v193
	v_mul_f32_e32 v178, v175, v178
	v_mul_f32_e32 v179, v175, v179
	v_mul_f32_e32 v180, v175, v180
	v_mul_f32_e32 v181, v175, v181
	v_mul_f32_e32 v182, v175, v182
	v_mul_f32_e32 v183, v175, v183
	v_mul_f32_e32 v184, v175, v184
	v_mul_f32_e32 v185, v175, v185
	v_exp_f32_e32 v136, v178
	v_exp_f32_e32 v137, v179
	v_exp_f32_e32 v138, v180
	v_exp_f32_e32 v139, v181
	v_exp_f32_e32 v140, v182
	v_exp_f32_e32 v141, v183
	v_exp_f32_e32 v142, v184
	v_exp_f32_e32 v143, v185
	s_nop 0
	v_fma_f32 v194, -v136, v136, 1.0
	v_fma_f32 v195, -v137, v137, 1.0
	v_fma_f32 v196, -v138, v138, 1.0
	v_fma_f32 v197, -v139, v139, 1.0
	v_fma_f32 v198, -v140, v140, 1.0
	v_fma_f32 v199, -v141, v141, 1.0
	v_fma_f32 v200, -v142, v142, 1.0
	v_fma_f32 v201, -v143, v143, 1.0
	v_max_f32_e32 v194, 0, v194
	v_max_f32_e32 v195, 0, v195
	v_max_f32_e32 v196, 0, v196
	v_max_f32_e32 v197, 0, v197
	v_max_f32_e32 v198, 0, v198
	v_max_f32_e32 v199, 0, v199
	v_max_f32_e32 v200, 0, v200
	v_max_f32_e32 v201, 0, v201
	v_sqrt_f32_e32 v194, v194
	v_sqrt_f32_e32 v195, v195
	v_sqrt_f32_e32 v196, v196
	v_sqrt_f32_e32 v197, v197
	v_sqrt_f32_e32 v198, v198
	v_sqrt_f32_e32 v199, v199
	v_sqrt_f32_e32 v200, v200
	v_sqrt_f32_e32 v201, v201
	s_waitcnt lgkmcnt(0)
	v_lshlrev_b32_e32 v152, 16, v152
	v_lshlrev_b32_e32 v153, 16, v153
	v_lshlrev_b32_e32 v154, 16, v154
	v_lshlrev_b32_e32 v155, 16, v155
	v_lshlrev_b32_e32 v156, 16, v156
	v_lshlrev_b32_e32 v157, 16, v157
	v_lshlrev_b32_e32 v158, 16, v158
	v_lshlrev_b32_e32 v159, 16, v159
	v_mul_f32_e32 v194, v194, v186
	v_mul_f32_e32 v195, v195, v187
	v_mul_f32_e32 v196, v196, v188
	v_mul_f32_e32 v197, v197, v189
	v_mul_f32_e32 v198, v198, v190
	v_mul_f32_e32 v199, v199, v191
	v_mul_f32_e32 v200, v200, v192
	v_mul_f32_e32 v201, v201, v193
	v_mul_f32_e32 v152, v194, v152
	v_mul_f32_e32 v153, v195, v153
	v_mul_f32_e32 v154, v196, v154
	v_mul_f32_e32 v155, v197, v155
	v_mul_f32_e32 v156, v198, v156
	v_mul_f32_e32 v157, v199, v157
	v_mul_f32_e32 v158, v200, v158
	v_mul_f32_e32 v159, v201, v159
	v_fma_f32 v146, v130, v147, v146
	v_fma_f32 v150, v134, v151, v150
	v_fma_f32 v154, v138, v155, v154
	v_fma_f32 v158, v142, v159, v158
	v_mul_f32_e32 v130, v130, v131
	v_mul_f32_e32 v134, v134, v135
	v_mul_f32_e32 v138, v138, v139
	v_mul_f32_e32 v142, v142, v143
	v_fma_f32 v145, v129, v146, v145
	v_fma_f32 v149, v133, v150, v149
	v_fma_f32 v153, v137, v154, v153
	v_fma_f32 v157, v141, v158, v157
	v_mul_f32_e32 v129, v129, v130
	v_mul_f32_e32 v133, v133, v134
	v_mul_f32_e32 v137, v137, v138
	v_mul_f32_e32 v141, v141, v142
	v_fma_f32 v144, v128, v145, v144
	v_fma_f32 v148, v132, v149, v148
	v_fma_f32 v152, v136, v153, v152
	v_fma_f32 v156, v140, v157, v156
	v_mul_f32_e32 v128, v128, v129
	v_mul_f32_e32 v132, v132, v133
	v_mul_f32_e32 v136, v136, v137
	v_mul_f32_e32 v140, v140, v141
	ds_bpermute_b32 v178, v204, v128
	ds_bpermute_b32 v182, v204, v144
	ds_bpermute_b32 v179, v204, v132
	ds_bpermute_b32 v183, v204, v148
	ds_bpermute_b32 v180, v204, v136
	ds_bpermute_b32 v184, v204, v152
	ds_bpermute_b32 v181, v204, v140
	ds_bpermute_b32 v185, v204, v156
	s_waitcnt lgkmcnt(0)
	v_fma_f32 v186, v182, v128, v144
	v_cndmask_b32_e64 v178, 1.0, v178, s[34:35]
	v_fma_f32 v187, v183, v132, v148
	v_cndmask_b32_e64 v179, 1.0, v179, s[34:35]
	v_fma_f32 v188, v184, v136, v152
	v_cndmask_b32_e64 v180, 1.0, v180, s[34:35]
	v_fma_f32 v189, v185, v140, v156
	v_cndmask_b32_e64 v181, 1.0, v181, s[34:35]
	v_cndmask_b32_e64 v223, v144, v186, s[34:35]
	v_mul_f32_e32 v219, v128, v178
	v_cndmask_b32_e64 v224, v148, v187, s[34:35]
	v_mul_f32_e32 v220, v132, v179
	v_cndmask_b32_e64 v225, v152, v188, s[34:35]
	v_mul_f32_e32 v221, v136, v180
	v_cndmask_b32_e64 v226, v156, v189, s[34:35]
	v_mul_f32_e32 v222, v140, v181
	ds_bpermute_b32 v178, v205, v219
	ds_bpermute_b32 v182, v205, v223
	ds_bpermute_b32 v179, v205, v220
	ds_bpermute_b32 v183, v205, v224
	ds_bpermute_b32 v180, v205, v221
	ds_bpermute_b32 v184, v205, v225
	ds_bpermute_b32 v181, v205, v222
	ds_bpermute_b32 v185, v205, v226
	s_waitcnt lgkmcnt(0)
	v_fma_f32 v186, v182, v219, v223
	v_cndmask_b32_e64 v178, 1.0, v178, s[36:37]
	v_fma_f32 v187, v183, v220, v224
	v_cndmask_b32_e64 v179, 1.0, v179, s[36:37]
	v_fma_f32 v188, v184, v221, v225
	v_cndmask_b32_e64 v180, 1.0, v180, s[36:37]
	v_fma_f32 v189, v185, v222, v226
	v_cndmask_b32_e64 v181, 1.0, v181, s[36:37]
	v_cndmask_b32_e64 v223, v223, v186, s[36:37]
	v_mul_f32_e32 v219, v219, v178
	v_cndmask_b32_e64 v224, v224, v187, s[36:37]
	v_mul_f32_e32 v220, v220, v179
	v_cndmask_b32_e64 v225, v225, v188, s[36:37]
	v_mul_f32_e32 v221, v221, v180
	v_cndmask_b32_e64 v226, v226, v189, s[36:37]
	v_mul_f32_e32 v222, v222, v181
	ds_bpermute_b32 v227, v204, v219
	ds_bpermute_b32 v231, v204, v223
	ds_bpermute_b32 v235, v206, v219
	ds_bpermute_b32 v239, v206, v223
	ds_bpermute_b32 v228, v204, v220
	ds_bpermute_b32 v232, v204, v224
	ds_bpermute_b32 v236, v206, v220
	ds_bpermute_b32 v244, v206, v224
	ds_bpermute_b32 v229, v204, v221
	ds_bpermute_b32 v233, v204, v225
	ds_bpermute_b32 v237, v206, v221
	ds_bpermute_b32 v245, v206, v225
	ds_bpermute_b32 v230, v204, v222
	ds_bpermute_b32 v234, v204, v226
	ds_bpermute_b32 v238, v206, v222
	ds_bpermute_b32 v246, v206, v226
	s_waitcnt lgkmcnt(0)
	v_cndmask_b32_e64 v227, 1.0, v227, s[34:35]
	v_cndmask_b32_e64 v231, 0, v231, s[34:35]
	v_cndmask_b32_e64 v228, 1.0, v228, s[34:35]
	v_cndmask_b32_e64 v232, 0, v232, s[34:35]
	v_cndmask_b32_e64 v229, 1.0, v229, s[34:35]
	v_cndmask_b32_e64 v233, 0, v233, s[34:35]
	v_cndmask_b32_e64 v230, 1.0, v230, s[34:35]
	v_cndmask_b32_e64 v234, 0, v234, s[34:35]
	v_mov_b32_e32 v190, v238
	v_mov_b32_e32 v194, v246
	v_mov_b32_e32 v198, v190
	v_mov_b32_e32 v201, v194
	v_fma_f32 v194, v194, v237, v245
	v_mul_f32_e32 v190, v190, v237
	v_mov_b32_e32 v199, v190
	v_mov_b32_e32 v177, v194
	v_fma_f32 v194, v194, v236, v244
	v_mul_f32_e32 v190, v190, v236
	v_mov_b32_e32 v200, v190
	v_mov_b32_e32 v203, v194
	v_fma_f32 v194, v194, v235, v239
	v_mul_f32_e32 v190, v190, v235
	v_mov_b32_e32 v191, v194
	ds_write_b64 v207, v[190:191] offset:1024
	s_waitcnt lgkmcnt(0)
	s_barrier
	ds_read_b64 v[178:179], v208 offset:1536
	ds_read_b64 v[180:181], v208 offset:1024
	s_waitcnt lgkmcnt(0)
	v_fma_f32 v182, v176, v178, v179
	v_cndmask_b32_e64 v183, v176, v182, s[38:39]
	v_fma_f32 v176, v182, v180, v181
	s_add_i32 s13, s13, 1
	s_mov_b32 s60, 8
.Lmylru_loop_1:
	s_cmp_eq_u32 s13, 2
	s_cbranch_scc1 .Lmylru_t0_7
	s_waitcnt vmcnt(16)
	s_branch .Lmylru_t1_7

.Lmylru_t1_7:
	s_barrier
	s_sub_i32 s54, 17, s13
	s_lshl_b32 s55, s54, 14
	s_lshl_b32 s56, s6, 11
	s_add_i32 s55, s55, s56
	s_add_u32 s44, s22, s55
	s_addc_u32 s45, s23, 0
	s_cmp_lt_u32 s13, 2
	s_sub_i32 s50, 1, s13
	s_lshl_b32 s50, s50, 7
	s_lshl_b32 s51, s9, 8
	s_add_i32 s51, s51, 0x8000
	s_add_i32 s51, s51, s50
	s_sub_i32 s50, 17, s13
	s_lshl_b32 s50, s50, 7
	s_lshl_b32 s57, s9, 11
	s_add_i32 s57, s57, s50
	s_cmp_lt_u32 s13, 2
	s_cselect_b32 s57, s51, s57
	s_lshl_b32 s57, s57, 11
	s_add_u32 s40, s18, s57
	s_addc_u32 s41, s19, 0
	s_add_u32 s42, s20, s57
	s_addc_u32 s43, s21, 0
	global_load_dword v247, v209, s[44:45]
	global_load_dword v248, v209, s[44:45] offset:256
	global_load_dword v249, v209, s[44:45] offset:512
	global_load_dword v250, v209, s[44:45] offset:768
	global_load_dword v251, v209, s[44:45] offset:1024
	global_load_dword v252, v209, s[44:45] offset:1280
	global_load_dword v253, v209, s[44:45] offset:1536
	global_load_dword v254, v209, s[44:45] offset:1792
	s_cmp_eq_u32 s13, 17
	s_cbranch_scc1 .Lmylru_nodma_7
	s_add_i32 s58, s13, 1
	s_cmp_lt_u32 s58, 2
	s_sub_i32 s50, 1, s58
	s_lshl_b32 s50, s50, 7
	s_lshl_b32 s51, s9, 8
	s_add_i32 s51, s51, 0x8000
	s_add_i32 s51, s51, s50
	s_sub_i32 s50, 17, s58
	s_lshl_b32 s50, s50, 7
	s_lshl_b32 s59, s9, 11
	s_add_i32 s59, s59, s50
	s_cmp_lt_u32 s58, 2
	s_cselect_b32 s59, s51, s59
	s_lshl_b32 s52, s59, 11
	s_add_u32 s46, s16, s52
	s_addc_u32 s47, s17, 0
	s_lshl_b32 s52, s6, 13
	s_add_i32 s52, s52, 0x10000
	s_mov_b32 m0, s52
	s_add_i32 s52, s52, 0x400
	global_load_lds_dwordx4 v211, s[46:47]
	s_mov_b32 m0, s52
	s_add_i32 s52, s52, 0x400
	global_load_lds_dwordx4 v212, s[46:47]
	s_mov_b32 m0, s52
	s_add_i32 s52, s52, 0x400
	global_load_lds_dwordx4 v213, s[46:47]
	s_mov_b32 m0, s52
	s_add_i32 s52, s52, 0x400
	global_load_lds_dwordx4 v214, s[46:47]
	s_mov_b32 m0, s52
	s_add_i32 s52, s52, 0x400
	global_load_lds_dwordx4 v215, s[46:47]
	s_mov_b32 m0, s52
	s_add_i32 s52, s52, 0x400
	global_load_lds_dwordx4 v216, s[46:47]
	s_mov_b32 m0, s52
	s_add_i32 s52, s52, 0x400
	global_load_lds_dwordx4 v217, s[46:47]
	s_mov_b32 m0, s52
	s_nop 0
	global_load_lds_dwordx4 v218, s[46:47]
.Lmylru_nodma_7:
	v_mov_b32_e32 v163, v162
	ds_read_b128 v[96:99], v163
	ds_read_b128 v[100:103], v163 offset:8192
	ds_read_b128 v[104:107], v163 offset:16384
	ds_read_b128 v[108:111], v163 offset:24576
	v_xor_b32_e32 v164, 0x40, v163
	ds_read_b128 v[112:115], v164
	ds_read_b128 v[116:119], v164 offset:8192
	ds_read_b128 v[120:123], v164 offset:16384
	ds_read_b128 v[124:127], v164 offset:24576
	s_waitcnt lgkmcnt(7)
	v_mfma_f32_16x16x32_bf16 v[64:67], v[96:99], v[0:3], 0
	v_mfma_f32_16x16x32_bf16 v[68:71], v[96:99], v[32:35], 0
	v_xor_b32_e32 v164, 0x80, v163
	ds_read_b128 v[96:99], v164
	s_waitcnt lgkmcnt(7)
	v_mfma_f32_16x16x32_bf16 v[72:75], v[100:103], v[0:3], 0
	v_mfma_f32_16x16x32_bf16 v[76:79], v[100:103], v[32:35], 0
	ds_read_b128 v[100:103], v164 offset:8192
	s_waitcnt lgkmcnt(7)
	v_mfma_f32_16x16x32_bf16 v[80:83], v[104:107], v[0:3], 0
	v_mfma_f32_16x16x32_bf16 v[84:87], v[104:107], v[32:35], 0
	ds_read_b128 v[104:107], v164 offset:16384
	s_waitcnt lgkmcnt(7)
	v_mfma_f32_16x16x32_bf16 v[88:91], v[108:111], v[0:3], 0
	v_mfma_f32_16x16x32_bf16 v[92:95], v[108:111], v[32:35], 0
	ds_read_b128 v[108:111], v164 offset:24576
	s_waitcnt lgkmcnt(7)
	v_mfma_f32_16x16x32_bf16 v[64:67], v[112:115], v[4:7], v[64:67]
	v_mfma_f32_16x16x32_bf16 v[68:71], v[112:115], v[36:39], v[68:71]
	v_xor_b32_e32 v164, 0xc0, v163
	ds_read_b128 v[112:115], v164
	s_waitcnt lgkmcnt(7)
	v_mfma_f32_16x16x32_bf16 v[72:75], v[116:119], v[4:7], v[72:75]
	v_mfma_f32_16x16x32_bf16 v[76:79], v[116:119], v[36:39], v[76:79]
	ds_read_b128 v[116:119], v164 offset:8192
	s_waitcnt lgkmcnt(7)
	v_mfma_f32_16x16x32_bf16 v[80:83], v[120:123], v[4:7], v[80:83]
	v_mfma_f32_16x16x32_bf16 v[84:87], v[120:123], v[36:39], v[84:87]
	ds_read_b128 v[120:123], v164 offset:16384
	s_waitcnt lgkmcnt(7)
	v_mfma_f32_16x16x32_bf16 v[88:91], v[124:127], v[4:7], v[88:91]
	v_mfma_f32_16x16x32_bf16 v[92:95], v[124:127], v[36:39], v[92:95]
	ds_read_b128 v[124:127], v164 offset:24576
	s_waitcnt lgkmcnt(7)
	v_mfma_f32_16x16x32_bf16 v[64:67], v[96:99], v[8:11], v[64:67]
	v_mfma_f32_16x16x32_bf16 v[68:71], v[96:99], v[40:43], v[68:71]
	v_xor_b32_e32 v164, 0x100, v163
	ds_read_b128 v[96:99], v164
	s_waitcnt lgkmcnt(7)
	v_mfma_f32_16x16x32_bf16 v[72:75], v[100:103], v[8:11], v[72:75]
	v_mfma_f32_16x16x32_bf16 v[76:79], v[100:103], v[40:43], v[76:79]
	ds_read_b128 v[100:103], v164 offset:8192
	s_waitcnt lgkmcnt(7)
	v_mfma_f32_16x16x32_bf16 v[80:83], v[104:107], v[8:11], v[80:83]
	v_mfma_f32_16x16x32_bf16 v[84:87], v[104:107], v[40:43], v[84:87]
	ds_read_b128 v[104:107], v164 offset:16384
	s_waitcnt lgkmcnt(7)
	v_mfma_f32_16x16x32_bf16 v[88:91], v[108:111], v[8:11], v[88:91]
	v_mfma_f32_16x16x32_bf16 v[92:95], v[108:111], v[40:43], v[92:95]
	ds_read_b128 v[108:111], v164 offset:24576
	s_waitcnt lgkmcnt(7)
	v_mfma_f32_16x16x32_bf16 v[64:67], v[112:115], v[12:15], v[64:67]
	v_mfma_f32_16x16x32_bf16 v[68:71], v[112:115], v[44:47], v[68:71]
	v_xor_b32_e32 v164, 0x140, v163
	ds_read_b128 v[112:115], v164
	s_waitcnt lgkmcnt(7)
	v_mfma_f32_16x16x32_bf16 v[72:75], v[116:119], v[12:15], v[72:75]
	v_mfma_f32_16x16x32_bf16 v[76:79], v[116:119], v[44:47], v[76:79]
	ds_read_b128 v[116:119], v164 offset:8192
	s_waitcnt lgkmcnt(7)
	v_mfma_f32_16x16x32_bf16 v[80:83], v[120:123], v[12:15], v[80:83]
	v_mfma_f32_16x16x32_bf16 v[84:87], v[120:123], v[44:47], v[84:87]
	ds_read_b128 v[120:123], v164 offset:16384
	s_waitcnt lgkmcnt(7)
	v_mfma_f32_16x16x32_bf16 v[88:91], v[124:127], v[12:15], v[88:91]
	v_mfma_f32_16x16x32_bf16 v[92:95], v[124:127], v[44:47], v[92:95]
	ds_read_b128 v[124:127], v164 offset:24576
	s_waitcnt lgkmcnt(7)
	v_mfma_f32_16x16x32_bf16 v[64:67], v[96:99], v[16:19], v[64:67]
	v_mfma_f32_16x16x32_bf16 v[68:71], v[96:99], v[48:51], v[68:71]
	v_xor_b32_e32 v164, 0x180, v163
	ds_read_b128 v[96:99], v164
	s_waitcnt lgkmcnt(7)
	v_mfma_f32_16x16x32_bf16 v[72:75], v[100:103], v[16:19], v[72:75]
	v_mfma_f32_16x16x32_bf16 v[76:79], v[100:103], v[48:51], v[76:79]
	ds_read_b128 v[100:103], v164 offset:8192
	s_waitcnt lgkmcnt(7)
	v_mfma_f32_16x16x32_bf16 v[80:83], v[104:107], v[16:19], v[80:83]
	v_mfma_f32_16x16x32_bf16 v[84:87], v[104:107], v[48:51], v[84:87]
	ds_read_b128 v[104:107], v164 offset:16384
	s_waitcnt lgkmcnt(7)
	v_mfma_f32_16x16x32_bf16 v[88:91], v[108:111], v[16:19], v[88:91]
	v_mfma_f32_16x16x32_bf16 v[92:95], v[108:111], v[48:51], v[92:95]
	ds_read_b128 v[108:111], v164 offset:24576
	s_waitcnt lgkmcnt(7)
	v_mfma_f32_16x16x32_bf16 v[64:67], v[112:115], v[20:23], v[64:67]
	v_mfma_f32_16x16x32_bf16 v[68:71], v[112:115], v[52:55], v[68:71]
	v_xor_b32_e32 v164, 0x1c0, v163
	ds_read_b128 v[112:115], v164
	s_waitcnt lgkmcnt(7)
	v_mfma_f32_16x16x32_bf16 v[72:75], v[116:119], v[20:23], v[72:75]
	v_mfma_f32_16x16x32_bf16 v[76:79], v[116:119], v[52:55], v[76:79]
	ds_read_b128 v[116:119], v164 offset:8192
	s_waitcnt lgkmcnt(7)
	v_mfma_f32_16x16x32_bf16 v[80:83], v[120:123], v[20:23], v[80:83]
	v_mfma_f32_16x16x32_bf16 v[84:87], v[120:123], v[52:55], v[84:87]
	ds_read_b128 v[120:123], v164 offset:16384
	s_waitcnt lgkmcnt(7)
	v_mfma_f32_16x16x32_bf16 v[88:91], v[124:127], v[20:23], v[88:91]
	v_mfma_f32_16x16x32_bf16 v[92:95], v[124:127], v[52:55], v[92:95]
	ds_read_b128 v[124:127], v164 offset:24576
	s_waitcnt lgkmcnt(7)
	v_mfma_f32_16x16x32_bf16 v[64:67], v[96:99], v[24:27], v[64:67]
	v_mfma_f32_16x16x32_bf16 v[68:71], v[96:99], v[56:59], v[68:71]
	s_waitcnt lgkmcnt(6)
	v_mfma_f32_16x16x32_bf16 v[72:75], v[100:103], v[24:27], v[72:75]
	v_mfma_f32_16x16x32_bf16 v[76:79], v[100:103], v[56:59], v[76:79]
	s_waitcnt lgkmcnt(5)
	v_mfma_f32_16x16x32_bf16 v[80:83], v[104:107], v[24:27], v[80:83]
	v_mfma_f32_16x16x32_bf16 v[84:87], v[104:107], v[56:59], v[84:87]
	s_waitcnt lgkmcnt(4)
	v_mfma_f32_16x16x32_bf16 v[88:91], v[108:111], v[24:27], v[88:91]
	v_mfma_f32_16x16x32_bf16 v[92:95], v[108:111], v[56:59], v[92:95]
	s_waitcnt lgkmcnt(3)
	v_mfma_f32_16x16x32_bf16 v[64:67], v[112:115], v[28:31], v[64:67]
	v_mfma_f32_16x16x32_bf16 v[68:71], v[112:115], v[60:63], v[68:71]
	s_waitcnt lgkmcnt(2)
	v_mfma_f32_16x16x32_bf16 v[72:75], v[116:119], v[28:31], v[72:75]
	v_mfma_f32_16x16x32_bf16 v[76:79], v[116:119], v[60:63], v[76:79]
	s_waitcnt lgkmcnt(1)
	v_mfma_f32_16x16x32_bf16 v[80:83], v[120:123], v[28:31], v[80:83]
	v_mfma_f32_16x16x32_bf16 v[84:87], v[120:123], v[60:63], v[84:87]
	s_waitcnt lgkmcnt(0)
	v_mfma_f32_16x16x32_bf16 v[88:91], v[124:127], v[28:31], v[88:91]
	v_mfma_f32_16x16x32_bf16 v[92:95], v[124:127], v[60:63], v[92:95]
	v_add_u32_e32 v182, 0x0, v210
	v_add_u32_e32 v183, 0x1000, v182
	global_load_ushort v96, v182, s[40:41]
	global_load_ushort v97, v182, s[40:41] offset:2048
	global_load_ushort v98, v183, s[40:41]
	global_load_ushort v99, v183, s[40:41] offset:2048
	v_add_u32_e32 v182, 0x8000, v210
	v_add_u32_e32 v183, 0x1000, v182
	global_load_ushort v100, v182, s[40:41]
	global_load_ushort v101, v182, s[40:41] offset:2048
	global_load_ushort v102, v183, s[40:41]
	global_load_ushort v103, v183, s[40:41] offset:2048
	v_add_u32_e32 v182, 0x10000, v210
	v_add_u32_e32 v183, 0x1000, v182
	global_load_ushort v104, v182, s[40:41]
	global_load_ushort v105, v182, s[40:41] offset:2048
	global_load_ushort v106, v183, s[40:41]
	global_load_ushort v107, v183, s[40:41] offset:2048
	v_add_u32_e32 v182, 0x18000, v210
	v_add_u32_e32 v183, 0x1000, v182
	global_load_ushort v108, v182, s[40:41]
	global_load_ushort v109, v182, s[40:41] offset:2048
	global_load_ushort v110, v183, s[40:41]
	global_load_ushort v111, v183, s[40:41] offset:2048
	v_mov_b32_e32 v169, v165
	v_mov_b32_e32 v170, v166
	v_mov_b32_e32 v171, v167
	v_mov_b32_e32 v172, v168
	ds_read_u16 v144, v169
	ds_read_u16 v145, v170
	ds_read_u16 v146, v171
	ds_read_u16 v147, v172
	ds_read_u16 v148, v169 offset:8192
	ds_read_u16 v149, v170 offset:8192
	ds_read_u16 v150, v171 offset:8192
	ds_read_u16 v151, v172 offset:8192
	ds_read_u16 v152, v169 offset:16384
	ds_read_u16 v153, v170 offset:16384
	ds_read_u16 v154, v171 offset:16384
	ds_read_u16 v155, v172 offset:16384
	ds_read_u16 v156, v169 offset:24576
	ds_read_u16 v157, v170 offset:24576
	ds_read_u16 v158, v171 offset:24576
	ds_read_u16 v159, v172 offset:24576
	s_nop 7
	v_fma_f32 v178, v64, s53, v173
	v_fma_f32 v179, v65, s53, v173
	v_fma_f32 v180, v66, s53, v173
	v_fma_f32 v181, v67, s53, v173
	v_fma_f32 v182, v72, s53, v173
	v_fma_f32 v183, v73, s53, v173
	v_fma_f32 v184, v74, s53, v173
	v_fma_f32 v185, v75, s53, v173
	v_fma_f32 v186, v68, s53, v174
	v_fma_f32 v187, v69, s53, v174
	v_fma_f32 v188, v70, s53, v174
	v_fma_f32 v189, v71, s53, v174
	v_fma_f32 v190, v76, s53, v174
	v_fma_f32 v191, v77, s53, v174
	v_fma_f32 v192, v78, s53, v174
	v_fma_f32 v193, v79, s53, v174
	v_exp_f32_e32 v178, v178
	v_exp_f32_e32 v179, v179
	v_exp_f32_e32 v180, v180
	v_exp_f32_e32 v181, v181
	v_exp_f32_e32 v182, v182
	v_exp_f32_e32 v183, v183
	v_exp_f32_e32 v184, v184
	v_exp_f32_e32 v185, v185
	v_exp_f32_e32 v186, v186
	v_exp_f32_e32 v187, v187
	v_exp_f32_e32 v188, v188
	v_exp_f32_e32 v189, v189
	v_exp_f32_e32 v190, v190
	v_exp_f32_e32 v191, v191
	v_exp_f32_e32 v192, v192
	v_exp_f32_e32 v193, v193
	v_add_f32_e32 v178, 1.0, v178
	v_add_f32_e32 v179, 1.0, v179
	v_add_f32_e32 v180, 1.0, v180
	v_add_f32_e32 v181, 1.0, v181
	v_add_f32_e32 v182, 1.0, v182
	v_add_f32_e32 v183, 1.0, v183
	v_add_f32_e32 v184, 1.0, v184
	v_add_f32_e32 v185, 1.0, v185
	v_add_f32_e32 v186, 1.0, v186
	v_add_f32_e32 v187, 1.0, v187
	v_add_f32_e32 v188, 1.0, v188
	v_add_f32_e32 v189, 1.0, v189
	v_add_f32_e32 v190, 1.0, v190
	v_add_f32_e32 v191, 1.0, v191
	v_add_f32_e32 v192, 1.0, v192
	v_add_f32_e32 v193, 1.0, v193
	v_rcp_f32_e32 v178, v178
	v_rcp_f32_e32 v179, v179
	v_rcp_f32_e32 v180, v180
	v_rcp_f32_e32 v181, v181
	v_rcp_f32_e32 v182, v182
	v_rcp_f32_e32 v183, v183
	v_rcp_f32_e32 v184, v184
	v_rcp_f32_e32 v185, v185
	v_rcp_f32_e32 v186, v186
	v_rcp_f32_e32 v187, v187
	v_rcp_f32_e32 v188, v188
	v_rcp_f32_e32 v189, v189
	v_rcp_f32_e32 v190, v190
	v_rcp_f32_e32 v191, v191
	v_rcp_f32_e32 v192, v192
	v_rcp_f32_e32 v193, v193
	v_mul_f32_e32 v178, v175, v178
	v_mul_f32_e32 v179, v175, v179
	v_mul_f32_e32 v180, v175, v180
	v_mul_f32_e32 v181, v175, v181
	v_mul_f32_e32 v182, v175, v182
	v_mul_f32_e32 v183, v175, v183
	v_mul_f32_e32 v184, v175, v184
	v_mul_f32_e32 v185, v175, v185
	v_exp_f32_e32 v128, v178
	v_exp_f32_e32 v129, v179
	v_exp_f32_e32 v130, v180
	v_exp_f32_e32 v131, v181
	v_exp_f32_e32 v132, v182
	v_exp_f32_e32 v133, v183
	v_exp_f32_e32 v134, v184
	v_exp_f32_e32 v135, v185
	s_nop 0
	v_fma_f32 v194, -v128, v128, 1.0
	v_fma_f32 v195, -v129, v129, 1.0
	v_fma_f32 v196, -v130, v130, 1.0
	v_fma_f32 v197, -v131, v131, 1.0
	v_fma_f32 v198, -v132, v132, 1.0
	v_fma_f32 v199, -v133, v133, 1.0
	v_fma_f32 v200, -v134, v134, 1.0
	v_fma_f32 v201, -v135, v135, 1.0
	v_max_f32_e32 v194, 0, v194
	v_max_f32_e32 v195, 0, v195
	v_max_f32_e32 v196, 0, v196
	v_max_f32_e32 v197, 0, v197
	v_max_f32_e32 v198, 0, v198
	v_max_f32_e32 v199, 0, v199
	v_max_f32_e32 v200, 0, v200
	v_max_f32_e32 v201, 0, v201
	v_sqrt_f32_e32 v194, v194
	v_sqrt_f32_e32 v195, v195
	v_sqrt_f32_e32 v196, v196
	v_sqrt_f32_e32 v197, v197
	v_sqrt_f32_e32 v198, v198
	v_sqrt_f32_e32 v199, v199
	v_sqrt_f32_e32 v200, v200
	v_sqrt_f32_e32 v201, v201
	s_waitcnt lgkmcnt(8)
	v_lshlrev_b32_e32 v144, 16, v144
	v_lshlrev_b32_e32 v145, 16, v145
	v_lshlrev_b32_e32 v146, 16, v146
	v_lshlrev_b32_e32 v147, 16, v147
	v_lshlrev_b32_e32 v148, 16, v148
	v_lshlrev_b32_e32 v149, 16, v149
	v_lshlrev_b32_e32 v150, 16, v150
	v_lshlrev_b32_e32 v151, 16, v151
	v_mul_f32_e32 v194, v194, v186
	v_mul_f32_e32 v195, v195, v187
	v_mul_f32_e32 v196, v196, v188
	v_mul_f32_e32 v197, v197, v189
	v_mul_f32_e32 v198, v198, v190
	v_mul_f32_e32 v199, v199, v191
	v_mul_f32_e32 v200, v200, v192
	v_mul_f32_e32 v201, v201, v193
	v_mul_f32_e32 v144, v194, v144
	v_mul_f32_e32 v145, v195, v145
	v_mul_f32_e32 v146, v196, v146
	v_mul_f32_e32 v147, v197, v147
	v_mul_f32_e32 v148, v198, v148
	v_mul_f32_e32 v149, v199, v149
	v_mul_f32_e32 v150, v200, v150
	v_mul_f32_e32 v151, v201, v151
	v_fma_f32 v178, v80, s53, v173
	v_fma_f32 v179, v81, s53, v173
	v_fma_f32 v180, v82, s53, v173
	v_fma_f32 v181, v83, s53, v173
	v_fma_f32 v182, v88, s53, v173
	v_fma_f32 v183, v89, s53, v173
	v_fma_f32 v184, v90, s53, v173
	v_fma_f32 v185, v91, s53, v173
	v_fma_f32 v186, v84, s53, v174
	v_fma_f32 v187, v85, s53, v174
	v_fma_f32 v188, v86, s53, v174
	v_fma_f32 v189, v87, s53, v174
	v_fma_f32 v190, v92, s53, v174
	v_fma_f32 v191, v93, s53, v174
	v_fma_f32 v192, v94, s53, v174
	v_fma_f32 v193, v95, s53, v174
	v_exp_f32_e32 v178, v178
	v_exp_f32_e32 v179, v179
	v_exp_f32_e32 v180, v180
	v_exp_f32_e32 v181, v181
	v_exp_f32_e32 v182, v182
	v_exp_f32_e32 v183, v183
	v_exp_f32_e32 v184, v184
	v_exp_f32_e32 v185, v185
	v_exp_f32_e32 v186, v186
	v_exp_f32_e32 v187, v187
	v_exp_f32_e32 v188, v188
	v_exp_f32_e32 v189, v189
	v_exp_f32_e32 v190, v190
	v_exp_f32_e32 v191, v191
	v_exp_f32_e32 v192, v192
	v_exp_f32_e32 v193, v193
	v_add_f32_e32 v178, 1.0, v178
	v_add_f32_e32 v179, 1.0, v179
	v_add_f32_e32 v180, 1.0, v180
	v_add_f32_e32 v181, 1.0, v181
	v_add_f32_e32 v182, 1.0, v182
	v_add_f32_e32 v183, 1.0, v183
	v_add_f32_e32 v184, 1.0, v184
	v_add_f32_e32 v185, 1.0, v185
	v_add_f32_e32 v186, 1.0, v186
	v_add_f32_e32 v187, 1.0, v187
	v_add_f32_e32 v188, 1.0, v188
	v_add_f32_e32 v189, 1.0, v189
	v_add_f32_e32 v190, 1.0, v190
	v_add_f32_e32 v191, 1.0, v191
	v_add_f32_e32 v192, 1.0, v192
	v_add_f32_e32 v193, 1.0, v193
	v_rcp_f32_e32 v178, v178
	v_rcp_f32_e32 v179, v179
	v_rcp_f32_e32 v180, v180
	v_rcp_f32_e32 v181, v181
	v_rcp_f32_e32 v182, v182
	v_rcp_f32_e32 v183, v183
	v_rcp_f32_e32 v184, v184
	v_rcp_f32_e32 v185, v185
	v_rcp_f32_e32 v186, v186
	v_rcp_f32_e32 v187, v187
	v_rcp_f32_e32 v188, v188
	v_rcp_f32_e32 v189, v189
	v_rcp_f32_e32 v190, v190
	v_rcp_f32_e32 v191, v191
	v_rcp_f32_e32 v192, v192
	v_rcp_f32_e32 v193, v193
	v_mul_f32_e32 v178, v175, v178
	v_mul_f32_e32 v179, v175, v179
	v_mul_f32_e32 v180, v175, v180
	v_mul_f32_e32 v181, v175, v181
	v_mul_f32_e32 v182, v175, v182
	v_mul_f32_e32 v183, v175, v183
	v_mul_f32_e32 v184, v175, v184
	v_mul_f32_e32 v185, v175, v185
	v_exp_f32_e32 v136, v178
	v_exp_f32_e32 v137, v179
	v_exp_f32_e32 v138, v180
	v_exp_f32_e32 v139, v181
	v_exp_f32_e32 v140, v182
	v_exp_f32_e32 v141, v183
	v_exp_f32_e32 v142, v184
	v_exp_f32_e32 v143, v185
	s_nop 0
	v_fma_f32 v194, -v136, v136, 1.0
	v_fma_f32 v195, -v137, v137, 1.0
	v_fma_f32 v196, -v138, v138, 1.0
	v_fma_f32 v197, -v139, v139, 1.0
	v_fma_f32 v198, -v140, v140, 1.0
	v_fma_f32 v199, -v141, v141, 1.0
	v_fma_f32 v200, -v142, v142, 1.0
	v_fma_f32 v201, -v143, v143, 1.0
	v_max_f32_e32 v194, 0, v194
	v_max_f32_e32 v195, 0, v195
	v_max_f32_e32 v196, 0, v196
	v_max_f32_e32 v197, 0, v197
	v_max_f32_e32 v198, 0, v198
	v_max_f32_e32 v199, 0, v199
	v_max_f32_e32 v200, 0, v200
	v_max_f32_e32 v201, 0, v201
	v_sqrt_f32_e32 v194, v194
	v_sqrt_f32_e32 v195, v195
	v_sqrt_f32_e32 v196, v196
	v_sqrt_f32_e32 v197, v197
	v_sqrt_f32_e32 v198, v198
	v_sqrt_f32_e32 v199, v199
	v_sqrt_f32_e32 v200, v200
	v_sqrt_f32_e32 v201, v201
	s_waitcnt lgkmcnt(0)
	v_lshlrev_b32_e32 v152, 16, v152
	v_lshlrev_b32_e32 v153, 16, v153
	v_lshlrev_b32_e32 v154, 16, v154
	v_lshlrev_b32_e32 v155, 16, v155
	v_lshlrev_b32_e32 v156, 16, v156
	v_lshlrev_b32_e32 v157, 16, v157
	v_lshlrev_b32_e32 v158, 16, v158
	v_lshlrev_b32_e32 v159, 16, v159
	v_mul_f32_e32 v194, v194, v186
	v_mul_f32_e32 v195, v195, v187
	v_mul_f32_e32 v196, v196, v188
	v_mul_f32_e32 v197, v197, v189
	v_mul_f32_e32 v198, v198, v190
	v_mul_f32_e32 v199, v199, v191
	v_mul_f32_e32 v200, v200, v192
	v_mul_f32_e32 v201, v201, v193
	v_mul_f32_e32 v152, v194, v152
	v_mul_f32_e32 v153, v195, v153
	v_mul_f32_e32 v154, v196, v154
	v_mul_f32_e32 v155, v197, v155
	v_mul_f32_e32 v156, v198, v156
	v_mul_f32_e32 v157, v199, v157
	v_mul_f32_e32 v158, v200, v158
	v_mul_f32_e32 v159, v201, v159
	v_fma_f32 v146, v130, v147, v146
	v_fma_f32 v150, v134, v151, v150
	v_fma_f32 v154, v138, v155, v154
	v_fma_f32 v158, v142, v159, v158
	v_mul_f32_e32 v130, v130, v131
	v_mul_f32_e32 v134, v134, v135
	v_mul_f32_e32 v138, v138, v139
	v_mul_f32_e32 v142, v142, v143
	v_fma_f32 v145, v129, v146, v145
	v_fma_f32 v149, v133, v150, v149
	v_fma_f32 v153, v137, v154, v153
	v_fma_f32 v157, v141, v158, v157
	v_mul_f32_e32 v129, v129, v130
	v_mul_f32_e32 v133, v133, v134
	v_mul_f32_e32 v137, v137, v138
	v_mul_f32_e32 v141, v141, v142
	v_fma_f32 v144, v128, v145, v144
	v_fma_f32 v148, v132, v149, v148
	v_fma_f32 v152, v136, v153, v152
	v_fma_f32 v156, v140, v157, v156
	v_mul_f32_e32 v128, v128, v129
	v_mul_f32_e32 v132, v132, v133
	v_mul_f32_e32 v136, v136, v137
	v_mul_f32_e32 v140, v140, v141
	ds_bpermute_b32 v178, v204, v128
	ds_bpermute_b32 v182, v204, v144
	ds_bpermute_b32 v179, v204, v132
	ds_bpermute_b32 v183, v204, v148
	ds_bpermute_b32 v180, v204, v136
	ds_bpermute_b32 v184, v204, v152
	ds_bpermute_b32 v181, v204, v140
	ds_bpermute_b32 v185, v204, v156
	s_waitcnt lgkmcnt(0)
	v_fma_f32 v186, v182, v128, v144
	v_cndmask_b32_e64 v178, 1.0, v178, s[34:35]
	v_fma_f32 v187, v183, v132, v148
	v_cndmask_b32_e64 v179, 1.0, v179, s[34:35]
	v_fma_f32 v188, v184, v136, v152
	v_cndmask_b32_e64 v180, 1.0, v180, s[34:35]
	v_fma_f32 v189, v185, v140, v156
	v_cndmask_b32_e64 v181, 1.0, v181, s[34:35]
	v_cndmask_b32_e64 v223, v144, v186, s[34:35]
	v_mul_f32_e32 v219, v128, v178
	v_cndmask_b32_e64 v224, v148, v187, s[34:35]
	v_mul_f32_e32 v220, v132, v179
	v_cndmask_b32_e64 v225, v152, v188, s[34:35]
	v_mul_f32_e32 v221, v136, v180
	v_cndmask_b32_e64 v226, v156, v189, s[34:35]
	v_mul_f32_e32 v222, v140, v181
	ds_bpermute_b32 v178, v205, v219
	ds_bpermute_b32 v182, v205, v223
	ds_bpermute_b32 v179, v205, v220
	ds_bpermute_b32 v183, v205, v224
	ds_bpermute_b32 v180, v205, v221
	ds_bpermute_b32 v184, v205, v225
	ds_bpermute_b32 v181, v205, v222
	ds_bpermute_b32 v185, v205, v226
	s_waitcnt lgkmcnt(0)
	v_fma_f32 v186, v182, v219, v223
	v_cndmask_b32_e64 v178, 1.0, v178, s[36:37]
	v_fma_f32 v187, v183, v220, v224
	v_cndmask_b32_e64 v179, 1.0, v179, s[36:37]
	v_fma_f32 v188, v184, v221, v225
	v_cndmask_b32_e64 v180, 1.0, v180, s[36:37]
	v_fma_f32 v189, v185, v222, v226
	v_cndmask_b32_e64 v181, 1.0, v181, s[36:37]
	v_cndmask_b32_e64 v223, v223, v186, s[36:37]
	v_mul_f32_e32 v219, v219, v178
	v_cndmask_b32_e64 v224, v224, v187, s[36:37]
	v_mul_f32_e32 v220, v220, v179
	v_cndmask_b32_e64 v225, v225, v188, s[36:37]
	v_mul_f32_e32 v221, v221, v180
	v_cndmask_b32_e64 v226, v226, v189, s[36:37]
	v_mul_f32_e32 v222, v222, v181
	ds_bpermute_b32 v227, v204, v219
	ds_bpermute_b32 v231, v204, v223
	ds_bpermute_b32 v235, v206, v219
	ds_bpermute_b32 v239, v206, v223
	ds_bpermute_b32 v228, v204, v220
	ds_bpermute_b32 v232, v204, v224
	ds_bpermute_b32 v236, v206, v220
	ds_bpermute_b32 v244, v206, v224
	ds_bpermute_b32 v229, v204, v221
	ds_bpermute_b32 v233, v204, v225
	ds_bpermute_b32 v237, v206, v221
	ds_bpermute_b32 v245, v206, v225
	ds_bpermute_b32 v230, v204, v222
	ds_bpermute_b32 v234, v204, v226
	ds_bpermute_b32 v238, v206, v222
	ds_bpermute_b32 v246, v206, v226
	s_waitcnt lgkmcnt(0)
	v_cndmask_b32_e64 v227, 1.0, v227, s[34:35]
	v_cndmask_b32_e64 v231, 0, v231, s[34:35]
	v_cndmask_b32_e64 v228, 1.0, v228, s[34:35]
	v_cndmask_b32_e64 v232, 0, v232, s[34:35]
	v_cndmask_b32_e64 v229, 1.0, v229, s[34:35]
	v_cndmask_b32_e64 v233, 0, v233, s[34:35]
	v_cndmask_b32_e64 v230, 1.0, v230, s[34:35]
	v_cndmask_b32_e64 v234, 0, v234, s[34:35]
	v_mov_b32_e32 v190, v238
	v_mov_b32_e32 v194, v246
	v_mov_b32_e32 v198, v190
	v_mov_b32_e32 v201, v194
	v_fma_f32 v194, v194, v237, v245
	v_mul_f32_e32 v190, v190, v237
	v_mov_b32_e32 v199, v190
	v_mov_b32_e32 v177, v194
	v_fma_f32 v194, v194, v236, v244
	v_mul_f32_e32 v190, v190, v236
	v_mov_b32_e32 v200, v190
	v_mov_b32_e32 v203, v194
	v_fma_f32 v194, v194, v235, v239
	v_mul_f32_e32 v190, v190, v235
	v_mov_b32_e32 v191, v194
	ds_write_b64 v207, v[190:191]
	s_waitcnt lgkmcnt(0)
	s_barrier
	ds_read_b64 v[178:179], v208 offset:512
	ds_read_b64 v[180:181], v208
	s_waitcnt lgkmcnt(0)
	v_fma_f32 v182, v176, v178, v179
	v_cndmask_b32_e64 v183, v176, v182, s[38:39]
	v_fma_f32 v176, v182, v180, v181
	v_fma_f32 v184, v183, v200, v203
	v_fma_f32 v185, v183, v199, v177
	v_fma_f32 v186, v183, v198, v201
	v_mov_b32_e32 v187, v183
	v_fma_f32 v184, v184, v227, v231
	v_fma_f32 v185, v185, v228, v232
	v_fma_f32 v186, v186, v229, v233
	v_fma_f32 v187, v187, v230, v234
	v_fma_f32 v144, v184, v128, v144
	v_fma_f32 v148, v185, v132, v148
	v_fma_f32 v152, v186, v136, v152
	v_fma_f32 v156, v187, v140, v156
	v_fma_f32 v145, v184, v129, v145
	v_fma_f32 v149, v185, v133, v149
	v_fma_f32 v153, v186, v137, v153
	v_fma_f32 v157, v187, v141, v157
	v_fma_f32 v146, v184, v130, v146
	v_fma_f32 v150, v185, v134, v150
	v_fma_f32 v154, v186, v138, v154
	v_fma_f32 v158, v187, v142, v158
	v_fma_f32 v147, v184, v131, v147
	v_fma_f32 v151, v185, v135, v151
	v_fma_f32 v155, v186, v139, v155
	v_fma_f32 v159, v187, v143, v159
	s_waitcnt vmcnt(0)
	v_lshlrev_b32_e32 v178, 16, v247
	v_add_f32_e32 v144, v144, v178
	v_lshlrev_b32_e32 v96, 16, v96
	v_mul_f32_e32 v144, v144, v96
	v_cvt_pk_bf16_f32 v144, v144, v144
	v_and_b32_e32 v179, 0xffff0000, v247
	v_add_f32_e32 v145, v145, v179
	v_lshlrev_b32_e32 v97, 16, v97
	v_mul_f32_e32 v145, v145, v97
	v_cvt_pk_bf16_f32 v145, v145, v145
	v_lshlrev_b32_e32 v180, 16, v248
	v_add_f32_e32 v146, v146, v180
	v_lshlrev_b32_e32 v98, 16, v98
	v_mul_f32_e32 v146, v146, v98
	v_cvt_pk_bf16_f32 v146, v146, v146
	v_and_b32_e32 v181, 0xffff0000, v248
	v_add_f32_e32 v147, v147, v181
	v_lshlrev_b32_e32 v99, 16, v99
	v_mul_f32_e32 v147, v147, v99
	v_cvt_pk_bf16_f32 v147, v147, v147
	v_lshlrev_b32_e32 v178, 16, v249
	v_add_f32_e32 v148, v148, v178
	v_lshlrev_b32_e32 v100, 16, v100
	v_mul_f32_e32 v148, v148, v100
	v_cvt_pk_bf16_f32 v148, v148, v148
	v_and_b32_e32 v179, 0xffff0000, v249
	v_add_f32_e32 v149, v149, v179
	v_lshlrev_b32_e32 v101, 16, v101
	v_mul_f32_e32 v149, v149, v101
	v_cvt_pk_bf16_f32 v149, v149, v149
	v_lshlrev_b32_e32 v180, 16, v250
	v_add_f32_e32 v150, v150, v180
	v_lshlrev_b32_e32 v102, 16, v102
	v_mul_f32_e32 v150, v150, v102
	v_cvt_pk_bf16_f32 v150, v150, v150
	v_and_b32_e32 v181, 0xffff0000, v250
	v_add_f32_e32 v151, v151, v181
	v_lshlrev_b32_e32 v103, 16, v103
	v_mul_f32_e32 v151, v151, v103
	v_cvt_pk_bf16_f32 v151, v151, v151
	v_lshlrev_b32_e32 v178, 16, v251
	v_add_f32_e32 v152, v152, v178
	v_lshlrev_b32_e32 v104, 16, v104
	v_mul_f32_e32 v152, v152, v104
	v_cvt_pk_bf16_f32 v152, v152, v152
	v_and_b32_e32 v179, 0xffff0000, v251
	v_add_f32_e32 v153, v153, v179
	v_lshlrev_b32_e32 v105, 16, v105
	v_mul_f32_e32 v153, v153, v105
	v_cvt_pk_bf16_f32 v153, v153, v153
	v_lshlrev_b32_e32 v180, 16, v252
	v_add_f32_e32 v154, v154, v180
	v_lshlrev_b32_e32 v106, 16, v106
	v_mul_f32_e32 v154, v154, v106
	v_cvt_pk_bf16_f32 v154, v154, v154
	v_and_b32_e32 v181, 0xffff0000, v252
	v_add_f32_e32 v155, v155, v181
	v_lshlrev_b32_e32 v107, 16, v107
	v_mul_f32_e32 v155, v155, v107
	v_cvt_pk_bf16_f32 v155, v155, v155
	v_lshlrev_b32_e32 v178, 16, v253
	v_add_f32_e32 v156, v156, v178
	v_lshlrev_b32_e32 v108, 16, v108
	v_mul_f32_e32 v156, v156, v108
	v_cvt_pk_bf16_f32 v156, v156, v156
	v_and_b32_e32 v179, 0xffff0000, v253
	v_add_f32_e32 v157, v157, v179
	v_lshlrev_b32_e32 v109, 16, v109
	v_mul_f32_e32 v157, v157, v109
	v_cvt_pk_bf16_f32 v157, v157, v157
	v_lshlrev_b32_e32 v180, 16, v254
	v_add_f32_e32 v158, v158, v180
	v_lshlrev_b32_e32 v110, 16, v110
	v_mul_f32_e32 v158, v158, v110
	v_cvt_pk_bf16_f32 v158, v158, v158
	v_and_b32_e32 v181, 0xffff0000, v254
	v_add_f32_e32 v159, v159, v181
	v_lshlrev_b32_e32 v111, 16, v111
	v_mul_f32_e32 v159, v159, v111
	v_cvt_pk_bf16_f32 v159, v159, v159
	v_add_u32_e32 v182, 0x0, v210
	v_add_u32_e32 v183, 0x1000, v182
	global_store_short v182, v144, s[42:43]
	global_store_short v182, v145, s[42:43] offset:2048
	global_store_short v183, v146, s[42:43]
	global_store_short v183, v147, s[42:43] offset:2048
	v_add_u32_e32 v182, 0x8000, v210
	v_add_u32_e32 v183, 0x1000, v182
	global_store_short v182, v148, s[42:43]
	global_store_short v182, v149, s[42:43] offset:2048
	global_store_short v183, v150, s[42:43]
	global_store_short v183, v151, s[42:43] offset:2048
	v_add_u32_e32 v182, 0x10000, v210
	v_add_u32_e32 v183, 0x1000, v182
	global_store_short v182, v152, s[42:43]
	global_store_short v182, v153, s[42:43] offset:2048
	global_store_short v183, v154, s[42:43]
	global_store_short v183, v155, s[42:43] offset:2048
	v_add_u32_e32 v182, 0x18000, v210
	v_add_u32_e32 v183, 0x1000, v182
	global_store_short v182, v156, s[42:43]
	global_store_short v182, v157, s[42:43] offset:2048
	global_store_short v183, v158, s[42:43]
	global_store_short v183, v159, s[42:43] offset:2048
	s_add_i32 s13, s13, 1
	s_cmp_eq_u32 s13, 2
	s_cbranch_scc1 .Lmylru_t0_8
	s_waitcnt vmcnt(16)
	s_branch .Lmylru_t1_8

.Lmylru_t1_8:
	s_barrier
	s_sub_i32 s54, 17, s13
	s_lshl_b32 s55, s54, 14
	s_lshl_b32 s56, s6, 11
	s_add_i32 s55, s55, s56
	s_add_u32 s44, s22, s55
	s_addc_u32 s45, s23, 0
	s_cmp_lt_u32 s13, 2
	s_sub_i32 s50, 1, s13
	s_lshl_b32 s50, s50, 7
	s_lshl_b32 s51, s9, 8
	s_add_i32 s51, s51, 0x8000
	s_add_i32 s51, s51, s50
	s_sub_i32 s50, 17, s13
	s_lshl_b32 s50, s50, 7
	s_lshl_b32 s57, s9, 11
	s_add_i32 s57, s57, s50
	s_cmp_lt_u32 s13, 2
	s_cselect_b32 s57, s51, s57
	s_lshl_b32 s57, s57, 11
	s_add_u32 s40, s18, s57
	s_addc_u32 s41, s19, 0
	s_add_u32 s42, s20, s57
	s_addc_u32 s43, s21, 0
	global_load_dword v247, v209, s[44:45]
	global_load_dword v248, v209, s[44:45] offset:256
	global_load_dword v249, v209, s[44:45] offset:512
	global_load_dword v250, v209, s[44:45] offset:768
	global_load_dword v251, v209, s[44:45] offset:1024
	global_load_dword v252, v209, s[44:45] offset:1280
	global_load_dword v253, v209, s[44:45] offset:1536
	global_load_dword v254, v209, s[44:45] offset:1792
	s_cmp_eq_u32 s13, 17
	s_cbranch_scc1 .Lmylru_nodma_8
	s_add_i32 s58, s13, 1
	s_cmp_lt_u32 s58, 2
	s_sub_i32 s50, 1, s58
	s_lshl_b32 s50, s50, 7
	s_lshl_b32 s51, s9, 8
	s_add_i32 s51, s51, 0x8000
	s_add_i32 s51, s51, s50
	s_sub_i32 s50, 17, s58
	s_lshl_b32 s50, s50, 7
	s_lshl_b32 s59, s9, 11
	s_add_i32 s59, s59, s50
	s_cmp_lt_u32 s58, 2
	s_cselect_b32 s59, s51, s59
	s_lshl_b32 s52, s59, 11
	s_add_u32 s46, s16, s52
	s_addc_u32 s47, s17, 0
	s_lshl_b32 s52, s6, 13
	s_mov_b32 m0, s52
	s_add_i32 s52, s52, 0x400
	global_load_lds_dwordx4 v211, s[46:47]
	s_mov_b32 m0, s52
	s_add_i32 s52, s52, 0x400
	global_load_lds_dwordx4 v212, s[46:47]
	s_mov_b32 m0, s52
	s_add_i32 s52, s52, 0x400
	global_load_lds_dwordx4 v213, s[46:47]
	s_mov_b32 m0, s52
	s_add_i32 s52, s52, 0x400
	global_load_lds_dwordx4 v214, s[46:47]
	s_mov_b32 m0, s52
	s_add_i32 s52, s52, 0x400
	global_load_lds_dwordx4 v215, s[46:47]
	s_mov_b32 m0, s52
	s_add_i32 s52, s52, 0x400
	global_load_lds_dwordx4 v216, s[46:47]
	s_mov_b32 m0, s52
	s_add_i32 s52, s52, 0x400
	global_load_lds_dwordx4 v217, s[46:47]
	s_mov_b32 m0, s52
	s_nop 0
	global_load_lds_dwordx4 v218, s[46:47]
.Lmylru_nodma_8:
	v_or_b32_e32 v163, 0x10000, v162
	ds_read_b128 v[96:99], v163
	ds_read_b128 v[100:103], v163 offset:8192
	ds_read_b128 v[104:107], v163 offset:16384
	ds_read_b128 v[108:111], v163 offset:24576
	v_xor_b32_e32 v164, 0x40, v163
	ds_read_b128 v[112:115], v164
	ds_read_b128 v[116:119], v164 offset:8192
	ds_read_b128 v[120:123], v164 offset:16384
	ds_read_b128 v[124:127], v164 offset:24576
	s_waitcnt lgkmcnt(7)
	v_mfma_f32_16x16x32_bf16 v[64:67], v[96:99], v[0:3], 0
	v_mfma_f32_16x16x32_bf16 v[68:71], v[96:99], v[32:35], 0
	v_xor_b32_e32 v164, 0x80, v163
	ds_read_b128 v[96:99], v164
	s_waitcnt lgkmcnt(7)
	v_mfma_f32_16x16x32_bf16 v[72:75], v[100:103], v[0:3], 0
	v_mfma_f32_16x16x32_bf16 v[76:79], v[100:103], v[32:35], 0
	ds_read_b128 v[100:103], v164 offset:8192
	s_waitcnt lgkmcnt(7)
	v_mfma_f32_16x16x32_bf16 v[80:83], v[104:107], v[0:3], 0
	v_mfma_f32_16x16x32_bf16 v[84:87], v[104:107], v[32:35], 0
	ds_read_b128 v[104:107], v164 offset:16384
	s_waitcnt lgkmcnt(7)
	v_mfma_f32_16x16x32_bf16 v[88:91], v[108:111], v[0:3], 0
	v_mfma_f32_16x16x32_bf16 v[92:95], v[108:111], v[32:35], 0
	ds_read_b128 v[108:111], v164 offset:24576
	s_waitcnt lgkmcnt(7)
	v_mfma_f32_16x16x32_bf16 v[64:67], v[112:115], v[4:7], v[64:67]
	v_mfma_f32_16x16x32_bf16 v[68:71], v[112:115], v[36:39], v[68:71]
	v_xor_b32_e32 v164, 0xc0, v163
	ds_read_b128 v[112:115], v164
	s_waitcnt lgkmcnt(7)
	v_mfma_f32_16x16x32_bf16 v[72:75], v[116:119], v[4:7], v[72:75]
	v_mfma_f32_16x16x32_bf16 v[76:79], v[116:119], v[36:39], v[76:79]
	ds_read_b128 v[116:119], v164 offset:8192
	s_waitcnt lgkmcnt(7)
	v_mfma_f32_16x16x32_bf16 v[80:83], v[120:123], v[4:7], v[80:83]
	v_mfma_f32_16x16x32_bf16 v[84:87], v[120:123], v[36:39], v[84:87]
	ds_read_b128 v[120:123], v164 offset:16384
	s_waitcnt lgkmcnt(7)
	v_mfma_f32_16x16x32_bf16 v[88:91], v[124:127], v[4:7], v[88:91]
	v_mfma_f32_16x16x32_bf16 v[92:95], v[124:127], v[36:39], v[92:95]
	ds_read_b128 v[124:127], v164 offset:24576
	s_waitcnt lgkmcnt(7)
	v_mfma_f32_16x16x32_bf16 v[64:67], v[96:99], v[8:11], v[64:67]
	v_mfma_f32_16x16x32_bf16 v[68:71], v[96:99], v[40:43], v[68:71]
	v_xor_b32_e32 v164, 0x100, v163
	ds_read_b128 v[96:99], v164
	s_waitcnt lgkmcnt(7)
	v_mfma_f32_16x16x32_bf16 v[72:75], v[100:103], v[8:11], v[72:75]
	v_mfma_f32_16x16x32_bf16 v[76:79], v[100:103], v[40:43], v[76:79]
	ds_read_b128 v[100:103], v164 offset:8192
	s_waitcnt lgkmcnt(7)
	v_mfma_f32_16x16x32_bf16 v[80:83], v[104:107], v[8:11], v[80:83]
	v_mfma_f32_16x16x32_bf16 v[84:87], v[104:107], v[40:43], v[84:87]
	ds_read_b128 v[104:107], v164 offset:16384
	s_waitcnt lgkmcnt(7)
	v_mfma_f32_16x16x32_bf16 v[88:91], v[108:111], v[8:11], v[88:91]
	v_mfma_f32_16x16x32_bf16 v[92:95], v[108:111], v[40:43], v[92:95]
	ds_read_b128 v[108:111], v164 offset:24576
	s_waitcnt lgkmcnt(7)
	v_mfma_f32_16x16x32_bf16 v[64:67], v[112:115], v[12:15], v[64:67]
	v_mfma_f32_16x16x32_bf16 v[68:71], v[112:115], v[44:47], v[68:71]
	v_xor_b32_e32 v164, 0x140, v163
	ds_read_b128 v[112:115], v164
	s_waitcnt lgkmcnt(7)
	v_mfma_f32_16x16x32_bf16 v[72:75], v[116:119], v[12:15], v[72:75]
	v_mfma_f32_16x16x32_bf16 v[76:79], v[116:119], v[44:47], v[76:79]
	ds_read_b128 v[116:119], v164 offset:8192
	s_waitcnt lgkmcnt(7)
	v_mfma_f32_16x16x32_bf16 v[80:83], v[120:123], v[12:15], v[80:83]
	v_mfma_f32_16x16x32_bf16 v[84:87], v[120:123], v[44:47], v[84:87]
	ds_read_b128 v[120:123], v164 offset:16384
	s_waitcnt lgkmcnt(7)
	v_mfma_f32_16x16x32_bf16 v[88:91], v[124:127], v[12:15], v[88:91]
	v_mfma_f32_16x16x32_bf16 v[92:95], v[124:127], v[44:47], v[92:95]
	ds_read_b128 v[124:127], v164 offset:24576
	s_waitcnt lgkmcnt(7)
	v_mfma_f32_16x16x32_bf16 v[64:67], v[96:99], v[16:19], v[64:67]
	v_mfma_f32_16x16x32_bf16 v[68:71], v[96:99], v[48:51], v[68:71]
	v_xor_b32_e32 v164, 0x180, v163
	ds_read_b128 v[96:99], v164
	s_waitcnt lgkmcnt(7)
	v_mfma_f32_16x16x32_bf16 v[72:75], v[100:103], v[16:19], v[72:75]
	v_mfma_f32_16x16x32_bf16 v[76:79], v[100:103], v[48:51], v[76:79]
	ds_read_b128 v[100:103], v164 offset:8192
	s_waitcnt lgkmcnt(7)
	v_mfma_f32_16x16x32_bf16 v[80:83], v[104:107], v[16:19], v[80:83]
	v_mfma_f32_16x16x32_bf16 v[84:87], v[104:107], v[48:51], v[84:87]
	ds_read_b128 v[104:107], v164 offset:16384
	s_waitcnt lgkmcnt(7)
	v_mfma_f32_16x16x32_bf16 v[88:91], v[108:111], v[16:19], v[88:91]
	v_mfma_f32_16x16x32_bf16 v[92:95], v[108:111], v[48:51], v[92:95]
	ds_read_b128 v[108:111], v164 offset:24576
	s_waitcnt lgkmcnt(7)
	v_mfma_f32_16x16x32_bf16 v[64:67], v[112:115], v[20:23], v[64:67]
	v_mfma_f32_16x16x32_bf16 v[68:71], v[112:115], v[52:55], v[68:71]
	v_xor_b32_e32 v164, 0x1c0, v163
	ds_read_b128 v[112:115], v164
	s_waitcnt lgkmcnt(7)
	v_mfma_f32_16x16x32_bf16 v[72:75], v[116:119], v[20:23], v[72:75]
	v_mfma_f32_16x16x32_bf16 v[76:79], v[116:119], v[52:55], v[76:79]
	ds_read_b128 v[116:119], v164 offset:8192
	s_waitcnt lgkmcnt(7)
	v_mfma_f32_16x16x32_bf16 v[80:83], v[120:123], v[20:23], v[80:83]
	v_mfma_f32_16x16x32_bf16 v[84:87], v[120:123], v[52:55], v[84:87]
	ds_read_b128 v[120:123], v164 offset:16384
	s_waitcnt lgkmcnt(7)
	v_mfma_f32_16x16x32_bf16 v[88:91], v[124:127], v[20:23], v[88:91]
	v_mfma_f32_16x16x32_bf16 v[92:95], v[124:127], v[52:55], v[92:95]
	ds_read_b128 v[124:127], v164 offset:24576
	s_waitcnt lgkmcnt(7)
	v_mfma_f32_16x16x32_bf16 v[64:67], v[96:99], v[24:27], v[64:67]
	v_mfma_f32_16x16x32_bf16 v[68:71], v[96:99], v[56:59], v[68:71]
	s_waitcnt lgkmcnt(6)
	v_mfma_f32_16x16x32_bf16 v[72:75], v[100:103], v[24:27], v[72:75]
	v_mfma_f32_16x16x32_bf16 v[76:79], v[100:103], v[56:59], v[76:79]
	s_waitcnt lgkmcnt(5)
	v_mfma_f32_16x16x32_bf16 v[80:83], v[104:107], v[24:27], v[80:83]
	v_mfma_f32_16x16x32_bf16 v[84:87], v[104:107], v[56:59], v[84:87]
	s_waitcnt lgkmcnt(4)
	v_mfma_f32_16x16x32_bf16 v[88:91], v[108:111], v[24:27], v[88:91]
	v_mfma_f32_16x16x32_bf16 v[92:95], v[108:111], v[56:59], v[92:95]
	s_waitcnt lgkmcnt(3)
	v_mfma_f32_16x16x32_bf16 v[64:67], v[112:115], v[28:31], v[64:67]
	v_mfma_f32_16x16x32_bf16 v[68:71], v[112:115], v[60:63], v[68:71]
	s_waitcnt lgkmcnt(2)
	v_mfma_f32_16x16x32_bf16 v[72:75], v[116:119], v[28:31], v[72:75]
	v_mfma_f32_16x16x32_bf16 v[76:79], v[116:119], v[60:63], v[76:79]
	s_waitcnt lgkmcnt(1)
	v_mfma_f32_16x16x32_bf16 v[80:83], v[120:123], v[28:31], v[80:83]
	v_mfma_f32_16x16x32_bf16 v[84:87], v[120:123], v[60:63], v[84:87]
	s_waitcnt lgkmcnt(0)
	v_mfma_f32_16x16x32_bf16 v[88:91], v[124:127], v[28:31], v[88:91]
	v_mfma_f32_16x16x32_bf16 v[92:95], v[124:127], v[60:63], v[92:95]
	v_add_u32_e32 v182, 0x0, v210
	v_add_u32_e32 v183, 0x1000, v182
	global_load_ushort v96, v182, s[40:41]
	global_load_ushort v97, v182, s[40:41] offset:2048
	global_load_ushort v98, v183, s[40:41]
	global_load_ushort v99, v183, s[40:41] offset:2048
	v_add_u32_e32 v182, 0x8000, v210
	v_add_u32_e32 v183, 0x1000, v182
	global_load_ushort v100, v182, s[40:41]
	global_load_ushort v101, v182, s[40:41] offset:2048
	global_load_ushort v102, v183, s[40:41]
	global_load_ushort v103, v183, s[40:41] offset:2048
	v_add_u32_e32 v182, 0x10000, v210
	v_add_u32_e32 v183, 0x1000, v182
	global_load_ushort v104, v182, s[40:41]
	global_load_ushort v105, v182, s[40:41] offset:2048
	global_load_ushort v106, v183, s[40:41]
	global_load_ushort v107, v183, s[40:41] offset:2048
	v_add_u32_e32 v182, 0x18000, v210
	v_add_u32_e32 v183, 0x1000, v182
	global_load_ushort v108, v182, s[40:41]
	global_load_ushort v109, v182, s[40:41] offset:2048
	global_load_ushort v110, v183, s[40:41]
	global_load_ushort v111, v183, s[40:41] offset:2048
	v_or_b32_e32 v169, 0x10000, v165
	v_or_b32_e32 v170, 0x10000, v166
	v_or_b32_e32 v171, 0x10000, v167
	v_or_b32_e32 v172, 0x10000, v168
	ds_read_u16 v144, v169
	ds_read_u16 v145, v170
	ds_read_u16 v146, v171
	ds_read_u16 v147, v172
	ds_read_u16 v148, v169 offset:8192
	ds_read_u16 v149, v170 offset:8192
	ds_read_u16 v150, v171 offset:8192
	ds_read_u16 v151, v172 offset:8192
	ds_read_u16 v152, v169 offset:16384
	ds_read_u16 v153, v170 offset:16384
	ds_read_u16 v154, v171 offset:16384
	ds_read_u16 v155, v172 offset:16384
	ds_read_u16 v156, v169 offset:24576
	ds_read_u16 v157, v170 offset:24576
	ds_read_u16 v158, v171 offset:24576
	ds_read_u16 v159, v172 offset:24576
	s_nop 7
	v_fma_f32 v178, v64, s53, v173
	v_fma_f32 v179, v65, s53, v173
	v_fma_f32 v180, v66, s53, v173
	v_fma_f32 v181, v67, s53, v173
	v_fma_f32 v182, v72, s53, v173
	v_fma_f32 v183, v73, s53, v173
	v_fma_f32 v184, v74, s53, v173
	v_fma_f32 v185, v75, s53, v173
	v_fma_f32 v186, v68, s53, v174
	v_fma_f32 v187, v69, s53, v174
	v_fma_f32 v188, v70, s53, v174
	v_fma_f32 v189, v71, s53, v174
	v_fma_f32 v190, v76, s53, v174
	v_fma_f32 v191, v77, s53, v174
	v_fma_f32 v192, v78, s53, v174
	v_fma_f32 v193, v79, s53, v174
	v_exp_f32_e32 v178, v178
	v_exp_f32_e32 v179, v179
	v_exp_f32_e32 v180, v180
	v_exp_f32_e32 v181, v181
	v_exp_f32_e32 v182, v182
	v_exp_f32_e32 v183, v183
	v_exp_f32_e32 v184, v184
	v_exp_f32_e32 v185, v185
	v_exp_f32_e32 v186, v186
	v_exp_f32_e32 v187, v187
	v_exp_f32_e32 v188, v188
	v_exp_f32_e32 v189, v189
	v_exp_f32_e32 v190, v190
	v_exp_f32_e32 v191, v191
	v_exp_f32_e32 v192, v192
	v_exp_f32_e32 v193, v193
	v_add_f32_e32 v178, 1.0, v178
	v_add_f32_e32 v179, 1.0, v179
	v_add_f32_e32 v180, 1.0, v180
	v_add_f32_e32 v181, 1.0, v181
	v_add_f32_e32 v182, 1.0, v182
	v_add_f32_e32 v183, 1.0, v183
	v_add_f32_e32 v184, 1.0, v184
	v_add_f32_e32 v185, 1.0, v185
	v_add_f32_e32 v186, 1.0, v186
	v_add_f32_e32 v187, 1.0, v187
	v_add_f32_e32 v188, 1.0, v188
	v_add_f32_e32 v189, 1.0, v189
	v_add_f32_e32 v190, 1.0, v190
	v_add_f32_e32 v191, 1.0, v191
	v_add_f32_e32 v192, 1.0, v192
	v_add_f32_e32 v193, 1.0, v193
	v_rcp_f32_e32 v178, v178
	v_rcp_f32_e32 v179, v179
	v_rcp_f32_e32 v180, v180
	v_rcp_f32_e32 v181, v181
	v_rcp_f32_e32 v182, v182
	v_rcp_f32_e32 v183, v183
	v_rcp_f32_e32 v184, v184
	v_rcp_f32_e32 v185, v185
	v_rcp_f32_e32 v186, v186
	v_rcp_f32_e32 v187, v187
	v_rcp_f32_e32 v188, v188
	v_rcp_f32_e32 v189, v189
	v_rcp_f32_e32 v190, v190
	v_rcp_f32_e32 v191, v191
	v_rcp_f32_e32 v192, v192
	v_rcp_f32_e32 v193, v193
	v_mul_f32_e32 v178, v175, v178
	v_mul_f32_e32 v179, v175, v179
	v_mul_f32_e32 v180, v175, v180
	v_mul_f32_e32 v181, v175, v181
	v_mul_f32_e32 v182, v175, v182
	v_mul_f32_e32 v183, v175, v183
	v_mul_f32_e32 v184, v175, v184
	v_mul_f32_e32 v185, v175, v185
	v_exp_f32_e32 v128, v178
	v_exp_f32_e32 v129, v179
	v_exp_f32_e32 v130, v180
	v_exp_f32_e32 v131, v181
	v_exp_f32_e32 v132, v182
	v_exp_f32_e32 v133, v183
	v_exp_f32_e32 v134, v184
	v_exp_f32_e32 v135, v185
	s_nop 0
	v_fma_f32 v194, -v128, v128, 1.0
	v_fma_f32 v195, -v129, v129, 1.0
	v_fma_f32 v196, -v130, v130, 1.0
	v_fma_f32 v197, -v131, v131, 1.0
	v_fma_f32 v198, -v132, v132, 1.0
	v_fma_f32 v199, -v133, v133, 1.0
	v_fma_f32 v200, -v134, v134, 1.0
	v_fma_f32 v201, -v135, v135, 1.0
	v_max_f32_e32 v194, 0, v194
	v_max_f32_e32 v195, 0, v195
	v_max_f32_e32 v196, 0, v196
	v_max_f32_e32 v197, 0, v197
	v_max_f32_e32 v198, 0, v198
	v_max_f32_e32 v199, 0, v199
	v_max_f32_e32 v200, 0, v200
	v_max_f32_e32 v201, 0, v201
	v_sqrt_f32_e32 v194, v194
	v_sqrt_f32_e32 v195, v195
	v_sqrt_f32_e32 v196, v196
	v_sqrt_f32_e32 v197, v197
	v_sqrt_f32_e32 v198, v198
	v_sqrt_f32_e32 v199, v199
	v_sqrt_f32_e32 v200, v200
	v_sqrt_f32_e32 v201, v201
	s_waitcnt lgkmcnt(8)
	v_lshlrev_b32_e32 v144, 16, v144
	v_lshlrev_b32_e32 v145, 16, v145
	v_lshlrev_b32_e32 v146, 16, v146
	v_lshlrev_b32_e32 v147, 16, v147
	v_lshlrev_b32_e32 v148, 16, v148
	v_lshlrev_b32_e32 v149, 16, v149
	v_lshlrev_b32_e32 v150, 16, v150
	v_lshlrev_b32_e32 v151, 16, v151
	v_mul_f32_e32 v194, v194, v186
	v_mul_f32_e32 v195, v195, v187
	v_mul_f32_e32 v196, v196, v188
	v_mul_f32_e32 v197, v197, v189
	v_mul_f32_e32 v198, v198, v190
	v_mul_f32_e32 v199, v199, v191
	v_mul_f32_e32 v200, v200, v192
	v_mul_f32_e32 v201, v201, v193
	v_mul_f32_e32 v144, v194, v144
	v_mul_f32_e32 v145, v195, v145
	v_mul_f32_e32 v146, v196, v146
	v_mul_f32_e32 v147, v197, v147
	v_mul_f32_e32 v148, v198, v148
	v_mul_f32_e32 v149, v199, v149
	v_mul_f32_e32 v150, v200, v150
	v_mul_f32_e32 v151, v201, v151
	v_fma_f32 v178, v80, s53, v173
	v_fma_f32 v179, v81, s53, v173
	v_fma_f32 v180, v82, s53, v173
	v_fma_f32 v181, v83, s53, v173
	v_fma_f32 v182, v88, s53, v173
	v_fma_f32 v183, v89, s53, v173
	v_fma_f32 v184, v90, s53, v173
	v_fma_f32 v185, v91, s53, v173
	v_fma_f32 v186, v84, s53, v174
	v_fma_f32 v187, v85, s53, v174
	v_fma_f32 v188, v86, s53, v174
	v_fma_f32 v189, v87, s53, v174
	v_fma_f32 v190, v92, s53, v174
	v_fma_f32 v191, v93, s53, v174
	v_fma_f32 v192, v94, s53, v174
	v_fma_f32 v193, v95, s53, v174
	v_exp_f32_e32 v178, v178
	v_exp_f32_e32 v179, v179
	v_exp_f32_e32 v180, v180
	v_exp_f32_e32 v181, v181
	v_exp_f32_e32 v182, v182
	v_exp_f32_e32 v183, v183
	v_exp_f32_e32 v184, v184
	v_exp_f32_e32 v185, v185
	v_exp_f32_e32 v186, v186
	v_exp_f32_e32 v187, v187
	v_exp_f32_e32 v188, v188
	v_exp_f32_e32 v189, v189
	v_exp_f32_e32 v190, v190
	v_exp_f32_e32 v191, v191
	v_exp_f32_e32 v192, v192
	v_exp_f32_e32 v193, v193
	v_add_f32_e32 v178, 1.0, v178
	v_add_f32_e32 v179, 1.0, v179
	v_add_f32_e32 v180, 1.0, v180
	v_add_f32_e32 v181, 1.0, v181
	v_add_f32_e32 v182, 1.0, v182
	v_add_f32_e32 v183, 1.0, v183
	v_add_f32_e32 v184, 1.0, v184
	v_add_f32_e32 v185, 1.0, v185
	v_add_f32_e32 v186, 1.0, v186
	v_add_f32_e32 v187, 1.0, v187
	v_add_f32_e32 v188, 1.0, v188
	v_add_f32_e32 v189, 1.0, v189
	v_add_f32_e32 v190, 1.0, v190
	v_add_f32_e32 v191, 1.0, v191
	v_add_f32_e32 v192, 1.0, v192
	v_add_f32_e32 v193, 1.0, v193
	v_rcp_f32_e32 v178, v178
	v_rcp_f32_e32 v179, v179
	v_rcp_f32_e32 v180, v180
	v_rcp_f32_e32 v181, v181
	v_rcp_f32_e32 v182, v182
	v_rcp_f32_e32 v183, v183
	v_rcp_f32_e32 v184, v184
	v_rcp_f32_e32 v185, v185
	v_rcp_f32_e32 v186, v186
	v_rcp_f32_e32 v187, v187
	v_rcp_f32_e32 v188, v188
	v_rcp_f32_e32 v189, v189
	v_rcp_f32_e32 v190, v190
	v_rcp_f32_e32 v191, v191
	v_rcp_f32_e32 v192, v192
	v_rcp_f32_e32 v193, v193
	v_mul_f32_e32 v178, v175, v178
	v_mul_f32_e32 v179, v175, v179
	v_mul_f32_e32 v180, v175, v180
	v_mul_f32_e32 v181, v175, v181
	v_mul_f32_e32 v182, v175, v182
	v_mul_f32_e32 v183, v175, v183
	v_mul_f32_e32 v184, v175, v184
	v_mul_f32_e32 v185, v175, v185
	v_exp_f32_e32 v136, v178
	v_exp_f32_e32 v137, v179
	v_exp_f32_e32 v138, v180
	v_exp_f32_e32 v139, v181
	v_exp_f32_e32 v140, v182
	v_exp_f32_e32 v141, v183
	v_exp_f32_e32 v142, v184
	v_exp_f32_e32 v143, v185
	s_nop 0
	v_fma_f32 v194, -v136, v136, 1.0
	v_fma_f32 v195, -v137, v137, 1.0
	v_fma_f32 v196, -v138, v138, 1.0
	v_fma_f32 v197, -v139, v139, 1.0
	v_fma_f32 v198, -v140, v140, 1.0
	v_fma_f32 v199, -v141, v141, 1.0
	v_fma_f32 v200, -v142, v142, 1.0
	v_fma_f32 v201, -v143, v143, 1.0
	v_max_f32_e32 v194, 0, v194
	v_max_f32_e32 v195, 0, v195
	v_max_f32_e32 v196, 0, v196
	v_max_f32_e32 v197, 0, v197
	v_max_f32_e32 v198, 0, v198
	v_max_f32_e32 v199, 0, v199
	v_max_f32_e32 v200, 0, v200
	v_max_f32_e32 v201, 0, v201
	v_sqrt_f32_e32 v194, v194
	v_sqrt_f32_e32 v195, v195
	v_sqrt_f32_e32 v196, v196
	v_sqrt_f32_e32 v197, v197
	v_sqrt_f32_e32 v198, v198
	v_sqrt_f32_e32 v199, v199
	v_sqrt_f32_e32 v200, v200
	v_sqrt_f32_e32 v201, v201
	s_waitcnt lgkmcnt(0)
	v_lshlrev_b32_e32 v152, 16, v152
	v_lshlrev_b32_e32 v153, 16, v153
	v_lshlrev_b32_e32 v154, 16, v154
	v_lshlrev_b32_e32 v155, 16, v155
	v_lshlrev_b32_e32 v156, 16, v156
	v_lshlrev_b32_e32 v157, 16, v157
	v_lshlrev_b32_e32 v158, 16, v158
	v_lshlrev_b32_e32 v159, 16, v159
	v_mul_f32_e32 v194, v194, v186
	v_mul_f32_e32 v195, v195, v187
	v_mul_f32_e32 v196, v196, v188
	v_mul_f32_e32 v197, v197, v189
	v_mul_f32_e32 v198, v198, v190
	v_mul_f32_e32 v199, v199, v191
	v_mul_f32_e32 v200, v200, v192
	v_mul_f32_e32 v201, v201, v193
	v_mul_f32_e32 v152, v194, v152
	v_mul_f32_e32 v153, v195, v153
	v_mul_f32_e32 v154, v196, v154
	v_mul_f32_e32 v155, v197, v155
	v_mul_f32_e32 v156, v198, v156
	v_mul_f32_e32 v157, v199, v157
	v_mul_f32_e32 v158, v200, v158
	v_mul_f32_e32 v159, v201, v159
	v_fma_f32 v146, v130, v147, v146
	v_fma_f32 v150, v134, v151, v150
	v_fma_f32 v154, v138, v155, v154
	v_fma_f32 v158, v142, v159, v158
	v_mul_f32_e32 v130, v130, v131
	v_mul_f32_e32 v134, v134, v135
	v_mul_f32_e32 v138, v138, v139
	v_mul_f32_e32 v142, v142, v143
	v_fma_f32 v145, v129, v146, v145
	v_fma_f32 v149, v133, v150, v149
	v_fma_f32 v153, v137, v154, v153
	v_fma_f32 v157, v141, v158, v157
	v_mul_f32_e32 v129, v129, v130
	v_mul_f32_e32 v133, v133, v134
	v_mul_f32_e32 v137, v137, v138
	v_mul_f32_e32 v141, v141, v142
	v_fma_f32 v144, v128, v145, v144
	v_fma_f32 v148, v132, v149, v148
	v_fma_f32 v152, v136, v153, v152
	v_fma_f32 v156, v140, v157, v156
	v_mul_f32_e32 v128, v128, v129
	v_mul_f32_e32 v132, v132, v133
	v_mul_f32_e32 v136, v136, v137
	v_mul_f32_e32 v140, v140, v141
	ds_bpermute_b32 v178, v204, v128
	ds_bpermute_b32 v182, v204, v144
	ds_bpermute_b32 v179, v204, v132
	ds_bpermute_b32 v183, v204, v148
	ds_bpermute_b32 v180, v204, v136
	ds_bpermute_b32 v184, v204, v152
	ds_bpermute_b32 v181, v204, v140
	ds_bpermute_b32 v185, v204, v156
	s_waitcnt lgkmcnt(0)
	v_fma_f32 v186, v182, v128, v144
	v_cndmask_b32_e64 v178, 1.0, v178, s[34:35]
	v_fma_f32 v187, v183, v132, v148
	v_cndmask_b32_e64 v179, 1.0, v179, s[34:35]
	v_fma_f32 v188, v184, v136, v152
	v_cndmask_b32_e64 v180, 1.0, v180, s[34:35]
	v_fma_f32 v189, v185, v140, v156
	v_cndmask_b32_e64 v181, 1.0, v181, s[34:35]
	v_cndmask_b32_e64 v223, v144, v186, s[34:35]
	v_mul_f32_e32 v219, v128, v178
	v_cndmask_b32_e64 v224, v148, v187, s[34:35]
	v_mul_f32_e32 v220, v132, v179
	v_cndmask_b32_e64 v225, v152, v188, s[34:35]
	v_mul_f32_e32 v221, v136, v180
	v_cndmask_b32_e64 v226, v156, v189, s[34:35]
	v_mul_f32_e32 v222, v140, v181
	ds_bpermute_b32 v178, v205, v219
	ds_bpermute_b32 v182, v205, v223
	ds_bpermute_b32 v179, v205, v220
	ds_bpermute_b32 v183, v205, v224
	ds_bpermute_b32 v180, v205, v221
	ds_bpermute_b32 v184, v205, v225
	ds_bpermute_b32 v181, v205, v222
	ds_bpermute_b32 v185, v205, v226
	s_waitcnt lgkmcnt(0)
	v_fma_f32 v186, v182, v219, v223
	v_cndmask_b32_e64 v178, 1.0, v178, s[36:37]
	v_fma_f32 v187, v183, v220, v224
	v_cndmask_b32_e64 v179, 1.0, v179, s[36:37]
	v_fma_f32 v188, v184, v221, v225
	v_cndmask_b32_e64 v180, 1.0, v180, s[36:37]
	v_fma_f32 v189, v185, v222, v226
	v_cndmask_b32_e64 v181, 1.0, v181, s[36:37]
	v_cndmask_b32_e64 v223, v223, v186, s[36:37]
	v_mul_f32_e32 v219, v219, v178
	v_cndmask_b32_e64 v224, v224, v187, s[36:37]
	v_mul_f32_e32 v220, v220, v179
	v_cndmask_b32_e64 v225, v225, v188, s[36:37]
	v_mul_f32_e32 v221, v221, v180
	v_cndmask_b32_e64 v226, v226, v189, s[36:37]
	v_mul_f32_e32 v222, v222, v181
	ds_bpermute_b32 v227, v204, v219
	ds_bpermute_b32 v231, v204, v223
	ds_bpermute_b32 v235, v206, v219
	ds_bpermute_b32 v239, v206, v223
	ds_bpermute_b32 v228, v204, v220
	ds_bpermute_b32 v232, v204, v224
	ds_bpermute_b32 v236, v206, v220
	ds_bpermute_b32 v244, v206, v224
	ds_bpermute_b32 v229, v204, v221
	ds_bpermute_b32 v233, v204, v225
	ds_bpermute_b32 v237, v206, v221
	ds_bpermute_b32 v245, v206, v225
	ds_bpermute_b32 v230, v204, v222
	ds_bpermute_b32 v234, v204, v226
	ds_bpermute_b32 v238, v206, v222
	ds_bpermute_b32 v246, v206, v226
	s_waitcnt lgkmcnt(0)
	v_cndmask_b32_e64 v227, 1.0, v227, s[34:35]
	v_cndmask_b32_e64 v231, 0, v231, s[34:35]
	v_cndmask_b32_e64 v228, 1.0, v228, s[34:35]
	v_cndmask_b32_e64 v232, 0, v232, s[34:35]
	v_cndmask_b32_e64 v229, 1.0, v229, s[34:35]
	v_cndmask_b32_e64 v233, 0, v233, s[34:35]
	v_cndmask_b32_e64 v230, 1.0, v230, s[34:35]
	v_cndmask_b32_e64 v234, 0, v234, s[34:35]
	v_mov_b32_e32 v190, v238
	v_mov_b32_e32 v194, v246
	v_mov_b32_e32 v198, v190
	v_mov_b32_e32 v201, v194
	v_fma_f32 v194, v194, v237, v245
	v_mul_f32_e32 v190, v190, v237
	v_mov_b32_e32 v199, v190
	v_mov_b32_e32 v177, v194
	v_fma_f32 v194, v194, v236, v244
	v_mul_f32_e32 v190, v190, v236
	v_mov_b32_e32 v200, v190
	v_mov_b32_e32 v203, v194
	v_fma_f32 v194, v194, v235, v239
	v_mul_f32_e32 v190, v190, v235
	v_mov_b32_e32 v191, v194
	ds_write_b64 v207, v[190:191] offset:1024
	s_waitcnt lgkmcnt(0)
	s_barrier
	ds_read_b64 v[178:179], v208 offset:1536
	ds_read_b64 v[180:181], v208 offset:1024
	s_waitcnt lgkmcnt(0)
	v_fma_f32 v182, v176, v178, v179
	v_cndmask_b32_e64 v183, v176, v182, s[38:39]
	v_fma_f32 v176, v182, v180, v181
	v_fma_f32 v184, v183, v200, v203
	v_fma_f32 v185, v183, v199, v177
	v_fma_f32 v186, v183, v198, v201
	v_mov_b32_e32 v187, v183
	v_fma_f32 v184, v184, v227, v231
	v_fma_f32 v185, v185, v228, v232
	v_fma_f32 v186, v186, v229, v233
	v_fma_f32 v187, v187, v230, v234
	v_fma_f32 v144, v184, v128, v144
	v_fma_f32 v148, v185, v132, v148
	v_fma_f32 v152, v186, v136, v152
	v_fma_f32 v156, v187, v140, v156
	v_fma_f32 v145, v184, v129, v145
	v_fma_f32 v149, v185, v133, v149
	v_fma_f32 v153, v186, v137, v153
	v_fma_f32 v157, v187, v141, v157
	v_fma_f32 v146, v184, v130, v146
	v_fma_f32 v150, v185, v134, v150
	v_fma_f32 v154, v186, v138, v154
	v_fma_f32 v158, v187, v142, v158
	v_fma_f32 v147, v184, v131, v147
	v_fma_f32 v151, v185, v135, v151
	v_fma_f32 v155, v186, v139, v155
	v_fma_f32 v159, v187, v143, v159
	s_waitcnt vmcnt(0)
	v_lshlrev_b32_e32 v178, 16, v247
	v_add_f32_e32 v144, v144, v178
	v_lshlrev_b32_e32 v96, 16, v96
	v_mul_f32_e32 v144, v144, v96
	v_cvt_pk_bf16_f32 v144, v144, v144
	v_and_b32_e32 v179, 0xffff0000, v247
	v_add_f32_e32 v145, v145, v179
	v_lshlrev_b32_e32 v97, 16, v97
	v_mul_f32_e32 v145, v145, v97
	v_cvt_pk_bf16_f32 v145, v145, v145
	v_lshlrev_b32_e32 v180, 16, v248
	v_add_f32_e32 v146, v146, v180
	v_lshlrev_b32_e32 v98, 16, v98
	v_mul_f32_e32 v146, v146, v98
	v_cvt_pk_bf16_f32 v146, v146, v146
	v_and_b32_e32 v181, 0xffff0000, v248
	v_add_f32_e32 v147, v147, v181
	v_lshlrev_b32_e32 v99, 16, v99
	v_mul_f32_e32 v147, v147, v99
	v_cvt_pk_bf16_f32 v147, v147, v147
	v_lshlrev_b32_e32 v178, 16, v249
	v_add_f32_e32 v148, v148, v178
	v_lshlrev_b32_e32 v100, 16, v100
	v_mul_f32_e32 v148, v148, v100
	v_cvt_pk_bf16_f32 v148, v148, v148
	v_and_b32_e32 v179, 0xffff0000, v249
	v_add_f32_e32 v149, v149, v179
	v_lshlrev_b32_e32 v101, 16, v101
	v_mul_f32_e32 v149, v149, v101
	v_cvt_pk_bf16_f32 v149, v149, v149
	v_lshlrev_b32_e32 v180, 16, v250
	v_add_f32_e32 v150, v150, v180
	v_lshlrev_b32_e32 v102, 16, v102
	v_mul_f32_e32 v150, v150, v102
	v_cvt_pk_bf16_f32 v150, v150, v150
	v_and_b32_e32 v181, 0xffff0000, v250
	v_add_f32_e32 v151, v151, v181
	v_lshlrev_b32_e32 v103, 16, v103
	v_mul_f32_e32 v151, v151, v103
	v_cvt_pk_bf16_f32 v151, v151, v151
	v_lshlrev_b32_e32 v178, 16, v251
	v_add_f32_e32 v152, v152, v178
	v_lshlrev_b32_e32 v104, 16, v104
	v_mul_f32_e32 v152, v152, v104
	v_cvt_pk_bf16_f32 v152, v152, v152
	v_and_b32_e32 v179, 0xffff0000, v251
	v_add_f32_e32 v153, v153, v179
	v_lshlrev_b32_e32 v105, 16, v105
	v_mul_f32_e32 v153, v153, v105
	v_cvt_pk_bf16_f32 v153, v153, v153
	v_lshlrev_b32_e32 v180, 16, v252
	v_add_f32_e32 v154, v154, v180
	v_lshlrev_b32_e32 v106, 16, v106
	v_mul_f32_e32 v154, v154, v106
	v_cvt_pk_bf16_f32 v154, v154, v154
	v_and_b32_e32 v181, 0xffff0000, v252
	v_add_f32_e32 v155, v155, v181
	v_lshlrev_b32_e32 v107, 16, v107
	v_mul_f32_e32 v155, v155, v107
	v_cvt_pk_bf16_f32 v155, v155, v155
	v_lshlrev_b32_e32 v178, 16, v253
	v_add_f32_e32 v156, v156, v178
	v_lshlrev_b32_e32 v108, 16, v108
	v_mul_f32_e32 v156, v156, v108
	v_cvt_pk_bf16_f32 v156, v156, v156
	v_and_b32_e32 v179, 0xffff0000, v253
	v_add_f32_e32 v157, v157, v179
	v_lshlrev_b32_e32 v109, 16, v109
	v_mul_f32_e32 v157, v157, v109
	v_cvt_pk_bf16_f32 v157, v157, v157
	v_lshlrev_b32_e32 v180, 16, v254
	v_add_f32_e32 v158, v158, v180
	v_lshlrev_b32_e32 v110, 16, v110
	v_mul_f32_e32 v158, v158, v110
	v_cvt_pk_bf16_f32 v158, v158, v158
	v_and_b32_e32 v181, 0xffff0000, v254
	v_add_f32_e32 v159, v159, v181
	v_lshlrev_b32_e32 v111, 16, v111
	v_mul_f32_e32 v159, v159, v111
	v_cvt_pk_bf16_f32 v159, v159, v159
	v_add_u32_e32 v182, 0x0, v210
	v_add_u32_e32 v183, 0x1000, v182
	global_store_short v182, v144, s[42:43]
	global_store_short v182, v145, s[42:43] offset:2048
	global_store_short v183, v146, s[42:43]
	global_store_short v183, v147, s[42:43] offset:2048
	v_add_u32_e32 v182, 0x8000, v210
	v_add_u32_e32 v183, 0x1000, v182
	global_store_short v182, v148, s[42:43]
	global_store_short v182, v149, s[42:43] offset:2048
	global_store_short v183, v150, s[42:43]
	global_store_short v183, v151, s[42:43] offset:2048
	v_add_u32_e32 v182, 0x10000, v210
	v_add_u32_e32 v183, 0x1000, v182
	global_store_short v182, v152, s[42:43]
	global_store_short v182, v153, s[42:43] offset:2048
	global_store_short v183, v154, s[42:43]
	global_store_short v183, v155, s[42:43] offset:2048
	v_add_u32_e32 v182, 0x18000, v210
	v_add_u32_e32 v183, 0x1000, v182
	global_store_short v182, v156, s[42:43]
	global_store_short v182, v157, s[42:43] offset:2048
	global_store_short v183, v158, s[42:43]
	global_store_short v183, v159, s[42:43] offset:2048
	s_add_i32 s13, s13, 1
	s_add_i32 s60, s60, -1
	s_cmp_lg_u32 s60, 0
	s_cbranch_scc1 .Lmylru_loop_1
	s_waitcnt vmcnt(0) lgkmcnt(0)
